# skip-branches around short predicated VALU+store blocks removed (M1 fp8 store blocks), plus loop-edge trims of the unrolled attention loop
# baseline (speedup 1.0000x reference)
.LBB0_799:
	v_exp_f32_e32 v159, v96
	v_exp_f32_e32 v161, v97
	v_exp_f32_e32 v157, v98
	v_exp_f32_e32 v160, v99
	v_exp_f32_e32 v155, v100
	v_exp_f32_e32 v158, v101
	v_exp_f32_e32 v154, v102
	v_exp_f32_e32 v156, v103
	v_exp_f32_e32 v151, v104
	v_exp_f32_e32 v153, v105
	v_exp_f32_e32 v149, v106
	v_exp_f32_e32 v152, v107
	v_exp_f32_e32 v147, v108
	v_exp_f32_e32 v150, v109
	v_exp_f32_e32 v146, v110
	v_exp_f32_e32 v148, v111
	v_fma_f32 v80, v193, v179, v195
	v_fma_f32 v179, v80, v198, v199
	v_mov_b32_e32 v193, v197
	s_waitcnt vmcnt(4) lgkmcnt(0)
	s_barrier
	ds_read_b128 v[80:83], v130 offset:50176
	ds_read_b128 v[84:87], v130 offset:58368
	ds_read_b128 v[196:199], v131 offset:50176
	ds_read_b128 v[200:203], v131 offset:58368
	s_waitcnt lgkmcnt(2)
	v_mfma_f32_32x32x16_bf16 v[96:111], v[80:83], v[122:125], 0
	v_exp_f32_e32 v204, v72
	v_exp_f32_e32 v205, v73
	v_exp_f32_e32 v206, v74
	v_exp_f32_e32 v207, v75
	v_exp_f32_e32 v208, v76
	v_exp_f32_e32 v209, v77
	v_mfma_f32_32x32x16_bf16 v[80:95], v[84:87], v[122:125], 0
	v_exp_f32_e32 v210, v78
	v_exp_f32_e32 v79, v79
	s_waitcnt lgkmcnt(0)
	v_mfma_f32_32x32x16_bf16 v[96:111], v[196:199], v[126:129], v[96:111]
	v_mfma_f32_32x32x16_bf16 v[80:95], v[200:203], v[126:129], v[80:95]
	ds_read_b128 v[196:199], v132 offset:50176
	ds_read_b128 v[200:203], v132 offset:58368
	s_waitcnt lgkmcnt(0)
	v_mfma_f32_32x32x16_bf16 v[96:111], v[196:199], v[118:121], v[96:111]
	v_mfma_f32_32x32x16_bf16 v[80:95], v[200:203], v[118:121], v[80:95]
	ds_read_b128 v[196:199], v133 offset:50176
	ds_read_b128 v[200:203], v133 offset:58368
	v_exp_f32_e32 v180, v64
	v_add_f32_e32 v64, v161, v159
	v_add_f32_e32 v195, v157, v160
	v_add_f32_e32 v64, v155, v64
	v_add_f32_e32 v195, v158, v195
	v_add_f32_e32 v64, v154, v64
	v_add_f32_e32 v195, v156, v195
	v_add_f32_e32 v64, v151, v64
	v_add_f32_e32 v195, v153, v195
	v_add_f32_e32 v64, v149, v64
	v_add_f32_e32 v195, v152, v195
	v_add_f32_e32 v64, v147, v64
	s_waitcnt lgkmcnt(0)
	v_mfma_f32_32x32x16_bf16 v[96:111], v[196:199], v[114:117], v[96:111]
	v_exp_f32_e32 v197, v65
	v_add_f32_e32 v195, v150, v195
	v_exp_f32_e32 v198, v66
	v_add_f32_e32 v64, v146, v64
	v_exp_f32_e32 v199, v67
	v_add_f32_e32 v195, v148, v195
	v_add_f32_e32 v64, v180, v64
	v_mfma_f32_32x32x16_bf16 v[80:95], v[200:203], v[114:117], v[80:95]
	v_exp_f32_e32 v200, v68
	v_exp_f32_e32 v201, v69
	v_add_f32_e32 v195, v197, v195
	v_exp_f32_e32 v202, v70
	v_add_f32_e32 v64, v198, v64
	v_exp_f32_e32 v203, v71
	v_add_f32_e32 v195, v199, v195
	v_add_f32_e32 v64, v200, v64
	v_add_f32_e32 v195, v201, v195
	v_add_f32_e32 v64, v202, v64
	v_add_f32_e32 v195, v203, v195
	v_add_f32_e32 v64, v204, v64
	v_add_f32_e32 v195, v205, v195
	v_add_f32_e32 v64, v206, v64
	v_add_f32_e32 v195, v207, v195
	v_add_f32_e32 v64, v208, v64
	v_add_f32_e32 v195, v209, v195
	v_add_f32_e32 v64, v210, v64
	v_add_f32_e32 v195, v79, v195
	v_add_f32_e32 v195, v195, v64
	v_cvt_pk_bf16_f32 v64, v159, v161
	v_cvt_pk_bf16_f32 v65, v157, v160
	v_cvt_pk_bf16_f32 v66, v155, v158
	v_cvt_pk_bf16_f32 v67, v154, v156
	v_cvt_pk_bf16_f32 v68, v151, v153
	v_cvt_pk_bf16_f32 v69, v149, v152
	v_cvt_pk_bf16_f32 v70, v147, v150
	v_cvt_pk_bf16_f32 v71, v146, v148
	v_cvt_pk_bf16_f32 v72, v180, v197
	v_cvt_pk_bf16_f32 v73, v198, v199
	v_cvt_pk_bf16_f32 v74, v200, v201
	v_cvt_pk_bf16_f32 v75, v202, v203
	v_cvt_pk_bf16_f32 v76, v204, v205
	v_cvt_pk_bf16_f32 v77, v206, v207
	v_cvt_pk_bf16_f32 v78, v208, v209
	v_cvt_pk_bf16_f32 v79, v210, v79
	s_add_i32 m0, s84, 0x4400
	s_add_u32 s66, s78, s65
	s_addc_u32 s67, s79, 0
	global_load_lds_dwordx4 v185, s[66:67]
	s_add_i32 m0, s84, 0x6400
	s_add_i32 s64, s65, 0x60000
	global_load_lds_dwordx4 v184, s[66:67]
	s_add_i32 m0, s84, 0x14400
	s_add_u32 s70, s80, s64
	s_addc_u32 s71, s81, 0
	global_load_lds_dwordx4 v183, s[70:71]
	s_add_i32 m0, s84, 0x16400
	s_mov_b32 s65, s64
	global_load_lds_dwordx4 v182, s[70:71]
	ds_read_b64_tr_b16 v[198:199], v192 offset:33792
	ds_read_b64_tr_b16 v[200:201], v192 offset:35840
	ds_read_b64_tr_b16 v[202:203], v192 offset:37888
	ds_read_b64_tr_b16 v[204:205], v192 offset:39936
	ds_read_b64_tr_b16 v[206:207], v192 offset:41984
	ds_read_b64_tr_b16 v[208:209], v192 offset:44032
	ds_read_b64_tr_b16 v[222:223], v192 offset:46080
	ds_read_b64_tr_b16 v[224:225], v192 offset:48128
	s_waitcnt lgkmcnt(0)
	v_mfma_f32_32x32x16_bf16 v[0:15], v[64:67], v[198:201], v[0:15]
	ds_read_b64_tr_b16 v[198:199], v192 offset:34304
	ds_read_b64_tr_b16 v[200:201], v192 offset:36352
	ds_read_b64_tr_b16 v[138:139], v192 offset:42496
	ds_read_b64_tr_b16 v[140:141], v192 offset:44544
	v_mfma_f32_32x32x16_bf16 v[0:15], v[68:71], v[202:205], v[0:15]
	ds_read_b64_tr_b16 v[202:203], v192 offset:38400
	ds_read_b64_tr_b16 v[204:205], v192 offset:40448
	ds_read_b64_tr_b16 v[142:143], v192 offset:46592
	ds_read_b64_tr_b16 v[144:145], v192 offset:48640
	v_mfma_f32_32x32x16_bf16 v[0:15], v[72:75], v[206:209], v[0:15]
	v_mfma_f32_32x32x16_bf16 v[0:15], v[76:79], v[222:225], v[0:15]
	s_waitcnt lgkmcnt(0)
	v_mfma_f32_32x32x16_bf16 v[48:63], v[64:67], v[198:201], v[48:63]
	ds_read_b64_tr_b16 v[198:199], v192 offset:34816
	ds_read_b64_tr_b16 v[200:201], v192 offset:36864
	ds_read_b64_tr_b16 v[206:207], v192 offset:43008
	ds_read_b64_tr_b16 v[208:209], v192 offset:45056
	v_mfma_f32_32x32x16_bf16 v[48:63], v[68:71], v[202:205], v[48:63]
	ds_read_b64_tr_b16 v[202:203], v192 offset:38912
	ds_read_b64_tr_b16 v[204:205], v192 offset:40960
	ds_read_b64_tr_b16 v[222:223], v192 offset:47104
	ds_read_b64_tr_b16 v[224:225], v192 offset:49152
	v_mfma_f32_32x32x16_bf16 v[48:63], v[72:75], v[138:141], v[48:63]
	v_mfma_f32_32x32x16_bf16 v[48:63], v[76:79], v[142:145], v[48:63]
	s_waitcnt lgkmcnt(0)
	v_mfma_f32_32x32x16_bf16 v[32:47], v[64:67], v[198:201], v[32:47]
	ds_read_b64_tr_b16 v[198:199], v192 offset:35328
	ds_read_b64_tr_b16 v[200:201], v192 offset:37376
	ds_read_b64_tr_b16 v[138:139], v192 offset:43520
	ds_read_b64_tr_b16 v[140:141], v192 offset:45568
	v_mfma_f32_32x32x16_bf16 v[32:47], v[68:71], v[202:205], v[32:47]
	ds_read_b64_tr_b16 v[202:203], v192 offset:39424
	ds_read_b64_tr_b16 v[204:205], v192 offset:41472
	ds_read_b64_tr_b16 v[142:143], v192 offset:47616
	ds_read_b64_tr_b16 v[144:145], v192 offset:49664
	v_mfma_f32_32x32x16_bf16 v[32:47], v[72:75], v[206:209], v[32:47]
	v_mfma_f32_32x32x16_bf16 v[32:47], v[76:79], v[222:225], v[32:47]
	s_waitcnt lgkmcnt(0)
	v_mfma_f32_32x32x16_bf16 v[16:31], v[64:67], v[198:201], v[16:31]
	v_max_f32_e32 v64, v96, v97
	v_max3_f32 v65, v80, v81, v82
	v_max3_f32 v64, v64, v98, v99
	v_max3_f32 v65, v65, v83, v84
	v_max3_f32 v64, v64, v100, v101
	v_mfma_f32_32x32x16_bf16 v[16:31], v[68:71], v[202:205], v[16:31]
	v_max3_f32 v65, v65, v85, v86
	v_max3_f32 v64, v64, v102, v103
	v_max3_f32 v65, v65, v87, v88
	v_max3_f32 v64, v64, v104, v105
	v_max3_f32 v65, v65, v89, v90
	v_max3_f32 v64, v64, v106, v107
	v_max3_f32 v65, v65, v91, v92
	v_mfma_f32_32x32x16_bf16 v[16:31], v[72:75], v[138:141], v[16:31]
	v_max3_f32 v64, v64, v108, v109
	v_max3_f32 v65, v65, v93, v94
	v_max3_f32 v64, v64, v110, v111
	v_max3_f32 v64, v64, v65, v95
	v_mov_b32_e32 v198, 1.0
	v_mfma_f32_32x32x16_bf16 v[16:31], v[76:79], v[142:145], v[16:31]
	v_cmp_ge_f32_e64 s[0:1], s56, v64
	s_cmp_eq_u64 s[0:1], exec
	s_cbranch_scc1 .Lc1_792
	s_branch .Lc1_801

.Lc1_799:
	v_exp_f32_e32 v159, v96
	v_exp_f32_e32 v161, v97
	v_exp_f32_e32 v157, v98
	v_exp_f32_e32 v160, v99
	v_exp_f32_e32 v155, v100
	v_exp_f32_e32 v158, v101
	v_exp_f32_e32 v154, v102
	v_exp_f32_e32 v156, v103
	v_exp_f32_e32 v151, v104
	v_exp_f32_e32 v153, v105
	v_exp_f32_e32 v149, v106
	v_exp_f32_e32 v152, v107
	v_exp_f32_e32 v147, v108
	v_exp_f32_e32 v150, v109
	v_exp_f32_e32 v146, v110
	v_exp_f32_e32 v148, v111
	v_fma_f32 v80, v193, v179, v195
	v_fma_f32 v179, v80, v198, v199
	v_mov_b32_e32 v193, v197
	s_cmp_gt_u32 s55, 30
	s_waitcnt vmcnt(4) lgkmcnt(0)
	s_barrier
	s_cbranch_scc1 .LBB0_803
	ds_read_b128 v[80:83], v134 offset:50176
	ds_read_b128 v[84:87], v134 offset:58368
	ds_read_b128 v[196:199], v135 offset:50176
	ds_read_b128 v[200:203], v135 offset:58368
	s_waitcnt lgkmcnt(2)
	v_mfma_f32_32x32x16_bf16 v[96:111], v[80:83], v[122:125], 0
	v_exp_f32_e32 v204, v72
	v_exp_f32_e32 v205, v73
	v_exp_f32_e32 v206, v74
	v_exp_f32_e32 v207, v75
	v_exp_f32_e32 v208, v76
	v_exp_f32_e32 v209, v77
	v_mfma_f32_32x32x16_bf16 v[80:95], v[84:87], v[122:125], 0
	v_exp_f32_e32 v210, v78
	v_exp_f32_e32 v79, v79
	s_waitcnt lgkmcnt(0)
	v_mfma_f32_32x32x16_bf16 v[96:111], v[196:199], v[126:129], v[96:111]
	v_mfma_f32_32x32x16_bf16 v[80:95], v[200:203], v[126:129], v[80:95]
	ds_read_b128 v[196:199], v136 offset:50176
	ds_read_b128 v[200:203], v136 offset:58368
	s_waitcnt lgkmcnt(0)
	v_mfma_f32_32x32x16_bf16 v[96:111], v[196:199], v[118:121], v[96:111]
	v_mfma_f32_32x32x16_bf16 v[80:95], v[200:203], v[118:121], v[80:95]
	ds_read_b128 v[196:199], v137 offset:50176
	ds_read_b128 v[200:203], v137 offset:58368
	v_exp_f32_e32 v180, v64
	v_add_f32_e32 v64, v161, v159
	v_add_f32_e32 v195, v157, v160
	v_add_f32_e32 v64, v155, v64
	v_add_f32_e32 v195, v158, v195
	v_add_f32_e32 v64, v154, v64
	v_add_f32_e32 v195, v156, v195
	v_add_f32_e32 v64, v151, v64
	v_add_f32_e32 v195, v153, v195
	v_add_f32_e32 v64, v149, v64
	v_add_f32_e32 v195, v152, v195
	v_add_f32_e32 v64, v147, v64
	s_waitcnt lgkmcnt(0)
	v_mfma_f32_32x32x16_bf16 v[96:111], v[196:199], v[114:117], v[96:111]
	v_exp_f32_e32 v197, v65
	v_add_f32_e32 v195, v150, v195
	v_exp_f32_e32 v198, v66
	v_add_f32_e32 v64, v146, v64
	v_exp_f32_e32 v199, v67
	v_add_f32_e32 v195, v148, v195
	v_add_f32_e32 v64, v180, v64
	v_mfma_f32_32x32x16_bf16 v[80:95], v[200:203], v[114:117], v[80:95]
	v_exp_f32_e32 v200, v68
	v_exp_f32_e32 v201, v69
	v_add_f32_e32 v195, v197, v195
	v_exp_f32_e32 v202, v70
	v_add_f32_e32 v64, v198, v64
	v_exp_f32_e32 v203, v71
	v_add_f32_e32 v195, v199, v195
	v_add_f32_e32 v64, v200, v64
	v_add_f32_e32 v195, v201, v195
	v_add_f32_e32 v64, v202, v64
	v_add_f32_e32 v195, v203, v195
	v_add_f32_e32 v64, v204, v64
	v_add_f32_e32 v195, v205, v195
	v_add_f32_e32 v64, v206, v64
	v_add_f32_e32 v195, v207, v195
	v_add_f32_e32 v64, v208, v64
	v_add_f32_e32 v195, v209, v195
	v_add_f32_e32 v64, v210, v64
	v_add_f32_e32 v195, v79, v195
	v_add_f32_e32 v195, v195, v64
	v_cvt_pk_bf16_f32 v64, v159, v161
	v_cvt_pk_bf16_f32 v65, v157, v160
	v_cvt_pk_bf16_f32 v66, v155, v158
	v_cvt_pk_bf16_f32 v67, v154, v156
	v_cvt_pk_bf16_f32 v68, v151, v153
	v_cvt_pk_bf16_f32 v69, v149, v152
	v_cvt_pk_bf16_f32 v70, v147, v150
	v_cvt_pk_bf16_f32 v71, v146, v148
	v_cvt_pk_bf16_f32 v72, v180, v197
	v_cvt_pk_bf16_f32 v73, v198, v199
	v_cvt_pk_bf16_f32 v74, v200, v201
	v_cvt_pk_bf16_f32 v75, v202, v203
	v_cvt_pk_bf16_f32 v76, v204, v205
	v_cvt_pk_bf16_f32 v77, v206, v207
	v_cvt_pk_bf16_f32 v78, v208, v209
	v_cvt_pk_bf16_f32 v79, v210, v79
	s_add_i32 m0, s84, 0x400
	s_add_u32 s66, s78, s65
	s_addc_u32 s67, s79, 0
	global_load_lds_dwordx4 v185, s[66:67]
	s_add_i32 m0, s84, 0x2400
	s_add_i32 s64, s65, 0x60000
	global_load_lds_dwordx4 v184, s[66:67]
	s_add_i32 m0, s84, 0x10400
	s_add_u32 s70, s80, s64
	s_addc_u32 s71, s81, 0
	global_load_lds_dwordx4 v183, s[70:71]
	s_add_i32 m0, s84, 0x12400
	s_mov_b32 s65, s64
	global_load_lds_dwordx4 v182, s[70:71]
	ds_read_b64_tr_b16 v[198:199], v192 offset:17408
	ds_read_b64_tr_b16 v[200:201], v192 offset:19456
	ds_read_b64_tr_b16 v[202:203], v192 offset:21504
	ds_read_b64_tr_b16 v[204:205], v192 offset:23552
	ds_read_b64_tr_b16 v[206:207], v192 offset:25600
	ds_read_b64_tr_b16 v[208:209], v192 offset:27648
	ds_read_b64_tr_b16 v[222:223], v192 offset:29696
	ds_read_b64_tr_b16 v[224:225], v192 offset:31744
	s_waitcnt lgkmcnt(0)
	v_mfma_f32_32x32x16_bf16 v[0:15], v[64:67], v[198:201], v[0:15]
	ds_read_b64_tr_b16 v[198:199], v192 offset:17920
	ds_read_b64_tr_b16 v[200:201], v192 offset:19968
	ds_read_b64_tr_b16 v[138:139], v192 offset:26112
	ds_read_b64_tr_b16 v[140:141], v192 offset:28160
	v_mfma_f32_32x32x16_bf16 v[0:15], v[68:71], v[202:205], v[0:15]
	ds_read_b64_tr_b16 v[202:203], v192 offset:22016
	ds_read_b64_tr_b16 v[204:205], v192 offset:24064
	ds_read_b64_tr_b16 v[142:143], v192 offset:30208
	ds_read_b64_tr_b16 v[144:145], v192 offset:32256
	v_mfma_f32_32x32x16_bf16 v[0:15], v[72:75], v[206:209], v[0:15]
	v_mfma_f32_32x32x16_bf16 v[0:15], v[76:79], v[222:225], v[0:15]
	s_waitcnt lgkmcnt(0)
	v_mfma_f32_32x32x16_bf16 v[48:63], v[64:67], v[198:201], v[48:63]
	ds_read_b64_tr_b16 v[198:199], v192 offset:18432
	ds_read_b64_tr_b16 v[200:201], v192 offset:20480
	ds_read_b64_tr_b16 v[206:207], v192 offset:26624
	ds_read_b64_tr_b16 v[208:209], v192 offset:28672
	v_mfma_f32_32x32x16_bf16 v[48:63], v[68:71], v[202:205], v[48:63]
	ds_read_b64_tr_b16 v[202:203], v192 offset:22528
	ds_read_b64_tr_b16 v[204:205], v192 offset:24576
	ds_read_b64_tr_b16 v[222:223], v192 offset:30720
	ds_read_b64_tr_b16 v[224:225], v192 offset:32768
	v_mfma_f32_32x32x16_bf16 v[48:63], v[72:75], v[138:141], v[48:63]
	v_mfma_f32_32x32x16_bf16 v[48:63], v[76:79], v[142:145], v[48:63]
	s_waitcnt lgkmcnt(0)
	v_mfma_f32_32x32x16_bf16 v[32:47], v[64:67], v[198:201], v[32:47]
	ds_read_b64_tr_b16 v[198:199], v192 offset:18944
	ds_read_b64_tr_b16 v[200:201], v192 offset:20992
	ds_read_b64_tr_b16 v[138:139], v192 offset:27136
	ds_read_b64_tr_b16 v[140:141], v192 offset:29184
	v_mfma_f32_32x32x16_bf16 v[32:47], v[68:71], v[202:205], v[32:47]
	ds_read_b64_tr_b16 v[202:203], v192 offset:23040
	ds_read_b64_tr_b16 v[204:205], v192 offset:25088
	ds_read_b64_tr_b16 v[142:143], v192 offset:31232
	ds_read_b64_tr_b16 v[144:145], v192 offset:33280
	v_mfma_f32_32x32x16_bf16 v[32:47], v[72:75], v[206:209], v[32:47]
	v_mfma_f32_32x32x16_bf16 v[32:47], v[76:79], v[222:225], v[32:47]
	s_waitcnt lgkmcnt(0)
	v_mfma_f32_32x32x16_bf16 v[16:31], v[64:67], v[198:201], v[16:31]
	v_max_f32_e32 v64, v96, v97
	v_max3_f32 v65, v80, v81, v82
	v_max3_f32 v64, v64, v98, v99
	v_max3_f32 v65, v65, v83, v84
	v_max3_f32 v64, v64, v100, v101
	v_mfma_f32_32x32x16_bf16 v[16:31], v[68:71], v[202:205], v[16:31]
	v_max3_f32 v65, v65, v85, v86
	v_max3_f32 v64, v64, v102, v103
	v_max3_f32 v65, v65, v87, v88
	v_max3_f32 v64, v64, v104, v105
	v_max3_f32 v65, v65, v89, v90
	v_max3_f32 v64, v64, v106, v107
	v_max3_f32 v65, v65, v91, v92
	v_mfma_f32_32x32x16_bf16 v[16:31], v[72:75], v[138:141], v[16:31]
	v_max3_f32 v64, v64, v108, v109
	v_max3_f32 v65, v65, v93, v94
	v_max3_f32 v64, v64, v110, v111
	v_max3_f32 v64, v64, v65, v95
	v_mov_b32_e32 v198, 1.0
	v_mfma_f32_32x32x16_bf16 v[16:31], v[76:79], v[142:145], v[16:31]
	v_cmp_ge_f32_e64 s[0:1], s56, v64
	s_cmp_eq_u64 s[0:1], exec
	s_cbranch_scc1 .Lc2_792
	s_branch .Lc2_801

.LBB0_1230:
	s_mul_i32 s0, s5, s2
	s_add_i32 s5, s4, s0
	s_and_b64 s[0:1], s[40:41], exec
	s_cselect_b32 s6, s2, s3
	s_add_i32 s0, s6, -1
	v_min_i32_e32 v0, s0, v147
	v_max_i32_e32 v0, 0, v0
	v_add_u32_e32 v0, s5, v0
	v_min_i32_e32 v0, s12, v0
	v_min_i32_e32 v1, 0x8000, v0
	v_ashrrev_i32_e32 v112, 11, v1
	v_ashrrev_i32_e32 v1, 31, v0
	v_lshlrev_b64 v[130:131], 10, v[0:1]
	v_lshlrev_b64 v[0:1], 11, v[0:1]
	v_lshl_add_u64 v[0:1], v[138:139], 0, v[0:1]
	global_load_dwordx4 v[126:129], v[0:1], off
	global_load_dwordx4 v[122:125], v[0:1], off offset:64
	global_load_dwordx4 v[118:121], v[0:1], off offset:128
	global_load_dwordx4 v[114:117], v[0:1], off offset:192
	global_load_dwordx4 v[108:111], v[0:1], off offset:256
	global_load_dwordx4 v[104:107], v[0:1], off offset:320
	global_load_dwordx4 v[100:103], v[0:1], off offset:384
	global_load_dwordx4 v[96:99], v[0:1], off offset:448
	global_load_dwordx4 v[92:95], v[0:1], off offset:512
	global_load_dwordx4 v[88:91], v[0:1], off offset:576
	global_load_dwordx4 v[84:87], v[0:1], off offset:640
	global_load_dwordx4 v[80:83], v[0:1], off offset:704
	global_load_dwordx4 v[76:79], v[0:1], off offset:768
	global_load_dwordx4 v[72:75], v[0:1], off offset:832
	global_load_dwordx4 v[68:71], v[0:1], off offset:896
	global_load_dwordx4 v[64:67], v[0:1], off offset:960
	global_load_dwordx4 v[60:63], v[0:1], off offset:1024
	global_load_dwordx4 v[56:59], v[0:1], off offset:1088
	global_load_dwordx4 v[52:55], v[0:1], off offset:1152
	global_load_dwordx4 v[48:51], v[0:1], off offset:1216
	global_load_dwordx4 v[44:47], v[0:1], off offset:1280
	global_load_dwordx4 v[40:43], v[0:1], off offset:1344
	global_load_dwordx4 v[36:39], v[0:1], off offset:1408
	global_load_dwordx4 v[32:35], v[0:1], off offset:1472
	global_load_dwordx4 v[28:31], v[0:1], off offset:1536
	global_load_dwordx4 v[24:27], v[0:1], off offset:1600
	global_load_dwordx4 v[20:23], v[0:1], off offset:1664
	global_load_dwordx4 v[16:19], v[0:1], off offset:1728
	global_load_dwordx4 v[12:15], v[0:1], off offset:1792
	global_load_dwordx4 v[8:11], v[0:1], off offset:1856
	global_load_dwordx4 v[4:7], v[0:1], off offset:1920
	s_waitcnt lgkmcnt(0)
	global_load_dwordx4 v[0:3], v[0:1], off offset:1984
	v_cmp_lt_i32_e32 vcc, s5, v149
	v_cmp_gt_i32_e64 s[38:39], s6, v147
	s_and_b64 s[42:43], s[38:39], vcc
	v_cmp_eq_u32_e64 s[38:39], v112, v146
	s_waitcnt vmcnt(31)
	v_and_b32_e32 v133, 0xffff0000, v126
	v_lshlrev_b32_e32 v132, 16, v126
	v_mul_f32_e32 v133, v133, v133
	v_lshlrev_b32_e32 v134, 16, v127
	v_fmac_f32_e32 v133, v132, v132
	v_fmac_f32_e32 v133, v134, v134
	s_waitcnt vmcnt(30)
	v_and_b32_e32 v134, 0xffff0000, v122
	v_and_b32_e32 v135, 0xffff0000, v127
	v_lshlrev_b32_e32 v132, 16, v122
	v_mul_f32_e32 v134, v134, v134
	v_lshlrev_b32_e32 v136, 16, v128
	v_fmac_f32_e32 v133, v135, v135
	v_lshlrev_b32_e32 v135, 16, v123
	v_fmac_f32_e32 v134, v132, v132
	v_and_b32_e32 v137, 0xffff0000, v128
	v_fmac_f32_e32 v133, v136, v136
	v_and_b32_e32 v136, 0xffff0000, v123
	v_fmac_f32_e32 v134, v135, v135
	v_lshlrev_b32_e32 v144, 16, v129
	v_fmac_f32_e32 v133, v137, v137
	v_lshlrev_b32_e32 v137, 16, v124
	v_fmac_f32_e32 v134, v136, v136
	v_and_b32_e32 v145, 0xffff0000, v129
	v_fmac_f32_e32 v133, v144, v144
	v_and_b32_e32 v144, 0xffff0000, v124
	v_fmac_f32_e32 v134, v137, v137
	v_fmac_f32_e32 v133, v145, v145
	v_lshlrev_b32_e32 v145, 16, v125
	v_fmac_f32_e32 v134, v144, v144
	v_and_b32_e32 v162, 0xffff0000, v125
	v_fmac_f32_e32 v134, v145, v145
	v_fmac_f32_e32 v134, v162, v162
	v_add_f32_e32 v132, v133, v134
	s_waitcnt vmcnt(29)
	v_and_b32_e32 v134, 0xffff0000, v118
	v_lshlrev_b32_e32 v133, 16, v118
	v_mul_f32_e32 v134, v134, v134
	v_lshlrev_b32_e32 v135, 16, v119
	v_fmac_f32_e32 v134, v133, v133
	v_and_b32_e32 v136, 0xffff0000, v119
	v_fmac_f32_e32 v134, v135, v135
	v_lshlrev_b32_e32 v137, 16, v120
	v_fmac_f32_e32 v134, v136, v136
	v_and_b32_e32 v144, 0xffff0000, v120
	v_fmac_f32_e32 v134, v137, v137
	v_lshlrev_b32_e32 v145, 16, v121
	v_fmac_f32_e32 v134, v144, v144
	v_and_b32_e32 v162, 0xffff0000, v121
	v_fmac_f32_e32 v134, v145, v145
	v_fmac_f32_e32 v134, v162, v162
	v_add_f32_e32 v132, v132, v134
	s_waitcnt vmcnt(28)
	v_and_b32_e32 v134, 0xffff0000, v114
	v_lshlrev_b32_e32 v133, 16, v114
	v_mul_f32_e32 v134, v134, v134
	v_lshlrev_b32_e32 v135, 16, v115
	v_fmac_f32_e32 v134, v133, v133
	v_and_b32_e32 v136, 0xffff0000, v115
	v_fmac_f32_e32 v134, v135, v135
	v_lshlrev_b32_e32 v137, 16, v116
	v_fmac_f32_e32 v134, v136, v136
	v_and_b32_e32 v144, 0xffff0000, v116
	v_fmac_f32_e32 v134, v137, v137
	v_lshlrev_b32_e32 v145, 16, v117
	v_fmac_f32_e32 v134, v144, v144
	v_and_b32_e32 v162, 0xffff0000, v117
	v_fmac_f32_e32 v134, v145, v145
	v_fmac_f32_e32 v134, v162, v162
	v_add_f32_e32 v132, v132, v134
	s_waitcnt vmcnt(27)
	v_and_b32_e32 v134, 0xffff0000, v108
	v_lshlrev_b32_e32 v133, 16, v108
	v_mul_f32_e32 v134, v134, v134
	v_lshlrev_b32_e32 v135, 16, v109
	v_fmac_f32_e32 v134, v133, v133
	v_and_b32_e32 v136, 0xffff0000, v109
	v_fmac_f32_e32 v134, v135, v135
	v_lshlrev_b32_e32 v137, 16, v110
	v_fmac_f32_e32 v134, v136, v136
	v_and_b32_e32 v144, 0xffff0000, v110
	v_fmac_f32_e32 v134, v137, v137
	v_lshlrev_b32_e32 v145, 16, v111
	v_fmac_f32_e32 v134, v144, v144
	v_and_b32_e32 v162, 0xffff0000, v111
	v_fmac_f32_e32 v134, v145, v145
	v_fmac_f32_e32 v134, v162, v162
	v_add_f32_e32 v132, v132, v134
	s_waitcnt vmcnt(26)
	v_and_b32_e32 v134, 0xffff0000, v104
	v_lshlrev_b32_e32 v133, 16, v104
	v_mul_f32_e32 v134, v134, v134
	v_lshlrev_b32_e32 v135, 16, v105
	v_fmac_f32_e32 v134, v133, v133
	v_and_b32_e32 v136, 0xffff0000, v105
	v_fmac_f32_e32 v134, v135, v135
	v_lshlrev_b32_e32 v137, 16, v106
	v_fmac_f32_e32 v134, v136, v136
	v_and_b32_e32 v144, 0xffff0000, v106
	v_fmac_f32_e32 v134, v137, v137
	v_lshlrev_b32_e32 v145, 16, v107
	v_fmac_f32_e32 v134, v144, v144
	v_and_b32_e32 v162, 0xffff0000, v107
	v_fmac_f32_e32 v134, v145, v145
	v_fmac_f32_e32 v134, v162, v162
	v_add_f32_e32 v132, v132, v134
	s_waitcnt vmcnt(25)
	v_and_b32_e32 v134, 0xffff0000, v100
	v_lshlrev_b32_e32 v133, 16, v100
	v_mul_f32_e32 v134, v134, v134
	v_lshlrev_b32_e32 v135, 16, v101
	v_fmac_f32_e32 v134, v133, v133
	v_and_b32_e32 v136, 0xffff0000, v101
	v_fmac_f32_e32 v134, v135, v135
	v_lshlrev_b32_e32 v137, 16, v102
	v_fmac_f32_e32 v134, v136, v136
	v_and_b32_e32 v144, 0xffff0000, v102
	v_fmac_f32_e32 v134, v137, v137
	v_lshlrev_b32_e32 v145, 16, v103
	v_fmac_f32_e32 v134, v144, v144
	v_and_b32_e32 v162, 0xffff0000, v103
	v_fmac_f32_e32 v134, v145, v145
	v_fmac_f32_e32 v134, v162, v162
	v_add_f32_e32 v132, v132, v134
	s_waitcnt vmcnt(24)
	v_and_b32_e32 v134, 0xffff0000, v96
	v_lshlrev_b32_e32 v133, 16, v96
	v_mul_f32_e32 v134, v134, v134
	v_lshlrev_b32_e32 v135, 16, v97
	v_fmac_f32_e32 v134, v133, v133
	v_and_b32_e32 v136, 0xffff0000, v97
	v_fmac_f32_e32 v134, v135, v135
	v_lshlrev_b32_e32 v137, 16, v98
	v_fmac_f32_e32 v134, v136, v136
	v_and_b32_e32 v144, 0xffff0000, v98
	v_fmac_f32_e32 v134, v137, v137
	v_lshlrev_b32_e32 v145, 16, v99
	v_fmac_f32_e32 v134, v144, v144
	v_and_b32_e32 v162, 0xffff0000, v99
	v_fmac_f32_e32 v134, v145, v145
	v_fmac_f32_e32 v134, v162, v162
	v_add_f32_e32 v132, v132, v134
	s_waitcnt vmcnt(23)
	v_and_b32_e32 v134, 0xffff0000, v92
	v_lshlrev_b32_e32 v133, 16, v92
	v_mul_f32_e32 v134, v134, v134
	v_lshlrev_b32_e32 v135, 16, v93
	v_fmac_f32_e32 v134, v133, v133
	v_and_b32_e32 v136, 0xffff0000, v93
	v_fmac_f32_e32 v134, v135, v135
	v_lshlrev_b32_e32 v137, 16, v94
	v_fmac_f32_e32 v134, v136, v136
	v_and_b32_e32 v144, 0xffff0000, v94
	v_fmac_f32_e32 v134, v137, v137
	v_lshlrev_b32_e32 v145, 16, v95
	v_fmac_f32_e32 v134, v144, v144
	v_and_b32_e32 v162, 0xffff0000, v95
	v_fmac_f32_e32 v134, v145, v145
	v_fmac_f32_e32 v134, v162, v162
	v_add_f32_e32 v132, v132, v134
	s_waitcnt vmcnt(22)
	v_and_b32_e32 v134, 0xffff0000, v88
	v_lshlrev_b32_e32 v133, 16, v88
	v_mul_f32_e32 v134, v134, v134
	v_lshlrev_b32_e32 v135, 16, v89
	v_fmac_f32_e32 v134, v133, v133
	v_and_b32_e32 v136, 0xffff0000, v89
	v_fmac_f32_e32 v134, v135, v135
	v_lshlrev_b32_e32 v137, 16, v90
	v_fmac_f32_e32 v134, v136, v136
	v_and_b32_e32 v144, 0xffff0000, v90
	v_fmac_f32_e32 v134, v137, v137
	v_lshlrev_b32_e32 v145, 16, v91
	v_fmac_f32_e32 v134, v144, v144
	v_and_b32_e32 v162, 0xffff0000, v91
	v_fmac_f32_e32 v134, v145, v145
	v_fmac_f32_e32 v134, v162, v162
	v_add_f32_e32 v132, v132, v134
	s_waitcnt vmcnt(21)
	v_and_b32_e32 v134, 0xffff0000, v84
	v_lshlrev_b32_e32 v133, 16, v84
	v_mul_f32_e32 v134, v134, v134
	v_lshlrev_b32_e32 v135, 16, v85
	v_fmac_f32_e32 v134, v133, v133
	v_and_b32_e32 v136, 0xffff0000, v85
	v_fmac_f32_e32 v134, v135, v135
	v_lshlrev_b32_e32 v137, 16, v86
	v_fmac_f32_e32 v134, v136, v136
	v_and_b32_e32 v144, 0xffff0000, v86
	v_fmac_f32_e32 v134, v137, v137
	v_lshlrev_b32_e32 v145, 16, v87
	v_fmac_f32_e32 v134, v144, v144
	v_and_b32_e32 v162, 0xffff0000, v87
	v_fmac_f32_e32 v134, v145, v145
	v_fmac_f32_e32 v134, v162, v162
	v_add_f32_e32 v132, v132, v134
	s_waitcnt vmcnt(20)
	v_and_b32_e32 v134, 0xffff0000, v80
	v_lshlrev_b32_e32 v133, 16, v80
	v_mul_f32_e32 v134, v134, v134
	v_lshlrev_b32_e32 v135, 16, v81
	v_fmac_f32_e32 v134, v133, v133
	v_and_b32_e32 v136, 0xffff0000, v81
	v_fmac_f32_e32 v134, v135, v135
	v_lshlrev_b32_e32 v137, 16, v82
	v_fmac_f32_e32 v134, v136, v136
	v_and_b32_e32 v144, 0xffff0000, v82
	v_fmac_f32_e32 v134, v137, v137
	v_lshlrev_b32_e32 v145, 16, v83
	v_fmac_f32_e32 v134, v144, v144
	v_and_b32_e32 v162, 0xffff0000, v83
	v_fmac_f32_e32 v134, v145, v145
	v_fmac_f32_e32 v134, v162, v162
	v_add_f32_e32 v132, v132, v134
	s_waitcnt vmcnt(19)
	v_and_b32_e32 v134, 0xffff0000, v76
	v_lshlrev_b32_e32 v133, 16, v76
	v_mul_f32_e32 v134, v134, v134
	v_lshlrev_b32_e32 v135, 16, v77
	v_fmac_f32_e32 v134, v133, v133
	v_and_b32_e32 v136, 0xffff0000, v77
	v_fmac_f32_e32 v134, v135, v135
	v_lshlrev_b32_e32 v137, 16, v78
	v_fmac_f32_e32 v134, v136, v136
	v_and_b32_e32 v144, 0xffff0000, v78
	v_fmac_f32_e32 v134, v137, v137
	v_lshlrev_b32_e32 v145, 16, v79
	v_fmac_f32_e32 v134, v144, v144
	v_and_b32_e32 v162, 0xffff0000, v79
	v_fmac_f32_e32 v134, v145, v145
	v_fmac_f32_e32 v134, v162, v162
	v_add_f32_e32 v132, v132, v134
	s_waitcnt vmcnt(18)
	v_and_b32_e32 v134, 0xffff0000, v72
	v_lshlrev_b32_e32 v133, 16, v72
	v_mul_f32_e32 v134, v134, v134
	v_lshlrev_b32_e32 v135, 16, v73
	v_fmac_f32_e32 v134, v133, v133
	v_and_b32_e32 v136, 0xffff0000, v73
	v_fmac_f32_e32 v134, v135, v135
	v_lshlrev_b32_e32 v137, 16, v74
	v_fmac_f32_e32 v134, v136, v136
	v_and_b32_e32 v144, 0xffff0000, v74
	v_fmac_f32_e32 v134, v137, v137
	v_lshlrev_b32_e32 v145, 16, v75
	v_fmac_f32_e32 v134, v144, v144
	v_and_b32_e32 v162, 0xffff0000, v75
	v_fmac_f32_e32 v134, v145, v145
	v_fmac_f32_e32 v134, v162, v162
	v_add_f32_e32 v132, v132, v134
	s_waitcnt vmcnt(17)
	v_and_b32_e32 v134, 0xffff0000, v68
	v_lshlrev_b32_e32 v133, 16, v68
	v_mul_f32_e32 v134, v134, v134
	v_lshlrev_b32_e32 v135, 16, v69
	v_fmac_f32_e32 v134, v133, v133
	v_and_b32_e32 v136, 0xffff0000, v69
	v_fmac_f32_e32 v134, v135, v135
	v_lshlrev_b32_e32 v137, 16, v70
	v_fmac_f32_e32 v134, v136, v136
	v_and_b32_e32 v144, 0xffff0000, v70
	v_fmac_f32_e32 v134, v137, v137
	v_lshlrev_b32_e32 v145, 16, v71
	v_fmac_f32_e32 v134, v144, v144
	v_and_b32_e32 v162, 0xffff0000, v71
	v_fmac_f32_e32 v134, v145, v145
	v_fmac_f32_e32 v134, v162, v162
	v_add_f32_e32 v132, v132, v134
	s_waitcnt vmcnt(16)
	v_and_b32_e32 v134, 0xffff0000, v64
	v_lshlrev_b32_e32 v133, 16, v64
	v_mul_f32_e32 v134, v134, v134
	v_lshlrev_b32_e32 v135, 16, v65
	v_fmac_f32_e32 v134, v133, v133
	v_and_b32_e32 v136, 0xffff0000, v65
	v_fmac_f32_e32 v134, v135, v135
	v_lshlrev_b32_e32 v137, 16, v66
	v_fmac_f32_e32 v134, v136, v136
	v_and_b32_e32 v144, 0xffff0000, v66
	v_fmac_f32_e32 v134, v137, v137
	v_lshlrev_b32_e32 v145, 16, v67
	v_fmac_f32_e32 v134, v144, v144
	v_and_b32_e32 v162, 0xffff0000, v67
	v_fmac_f32_e32 v134, v145, v145
	v_fmac_f32_e32 v134, v162, v162
	v_add_f32_e32 v132, v132, v134
	s_waitcnt vmcnt(15)
	v_and_b32_e32 v134, 0xffff0000, v60
	v_lshlrev_b32_e32 v133, 16, v60
	v_mul_f32_e32 v134, v134, v134
	v_lshlrev_b32_e32 v135, 16, v61
	v_fmac_f32_e32 v134, v133, v133
	v_and_b32_e32 v136, 0xffff0000, v61
	v_fmac_f32_e32 v134, v135, v135
	v_lshlrev_b32_e32 v137, 16, v62
	v_fmac_f32_e32 v134, v136, v136
	v_and_b32_e32 v144, 0xffff0000, v62
	v_fmac_f32_e32 v134, v137, v137
	v_lshlrev_b32_e32 v145, 16, v63
	v_fmac_f32_e32 v134, v144, v144
	v_and_b32_e32 v162, 0xffff0000, v63
	v_fmac_f32_e32 v134, v145, v145
	v_fmac_f32_e32 v134, v162, v162
	v_add_f32_e32 v132, v132, v134
	s_waitcnt vmcnt(14)
	v_and_b32_e32 v134, 0xffff0000, v56
	v_lshlrev_b32_e32 v133, 16, v56
	v_mul_f32_e32 v134, v134, v134
	v_lshlrev_b32_e32 v135, 16, v57
	v_fmac_f32_e32 v134, v133, v133
	v_and_b32_e32 v136, 0xffff0000, v57
	v_fmac_f32_e32 v134, v135, v135
	v_lshlrev_b32_e32 v137, 16, v58
	v_fmac_f32_e32 v134, v136, v136
	v_and_b32_e32 v144, 0xffff0000, v58
	v_fmac_f32_e32 v134, v137, v137
	v_lshlrev_b32_e32 v145, 16, v59
	v_fmac_f32_e32 v134, v144, v144
	v_and_b32_e32 v162, 0xffff0000, v59
	v_fmac_f32_e32 v134, v145, v145
	v_fmac_f32_e32 v134, v162, v162
	v_add_f32_e32 v132, v132, v134
	s_waitcnt vmcnt(13)
	v_and_b32_e32 v134, 0xffff0000, v52
	v_lshlrev_b32_e32 v133, 16, v52
	v_mul_f32_e32 v134, v134, v134
	v_lshlrev_b32_e32 v135, 16, v53
	v_fmac_f32_e32 v134, v133, v133
	v_and_b32_e32 v136, 0xffff0000, v53
	v_fmac_f32_e32 v134, v135, v135
	v_lshlrev_b32_e32 v137, 16, v54
	v_fmac_f32_e32 v134, v136, v136
	v_and_b32_e32 v144, 0xffff0000, v54
	v_fmac_f32_e32 v134, v137, v137
	v_lshlrev_b32_e32 v145, 16, v55
	v_fmac_f32_e32 v134, v144, v144
	v_and_b32_e32 v162, 0xffff0000, v55
	v_fmac_f32_e32 v134, v145, v145
	v_fmac_f32_e32 v134, v162, v162
	v_add_f32_e32 v132, v132, v134
	s_waitcnt vmcnt(12)
	v_and_b32_e32 v134, 0xffff0000, v48
	v_lshlrev_b32_e32 v133, 16, v48
	v_mul_f32_e32 v134, v134, v134
	v_lshlrev_b32_e32 v135, 16, v49
	v_fmac_f32_e32 v134, v133, v133
	v_and_b32_e32 v136, 0xffff0000, v49
	v_fmac_f32_e32 v134, v135, v135
	v_lshlrev_b32_e32 v137, 16, v50
	v_fmac_f32_e32 v134, v136, v136
	v_and_b32_e32 v144, 0xffff0000, v50
	v_fmac_f32_e32 v134, v137, v137
	v_lshlrev_b32_e32 v145, 16, v51
	v_fmac_f32_e32 v134, v144, v144
	v_and_b32_e32 v162, 0xffff0000, v51
	v_fmac_f32_e32 v134, v145, v145
	v_fmac_f32_e32 v134, v162, v162
	v_add_f32_e32 v132, v132, v134
	s_waitcnt vmcnt(11)
	v_and_b32_e32 v134, 0xffff0000, v44
	v_lshlrev_b32_e32 v133, 16, v44
	v_mul_f32_e32 v134, v134, v134
	v_lshlrev_b32_e32 v135, 16, v45
	v_fmac_f32_e32 v134, v133, v133
	v_and_b32_e32 v136, 0xffff0000, v45
	v_fmac_f32_e32 v134, v135, v135
	v_lshlrev_b32_e32 v137, 16, v46
	v_fmac_f32_e32 v134, v136, v136
	v_and_b32_e32 v144, 0xffff0000, v46
	v_fmac_f32_e32 v134, v137, v137
	v_lshlrev_b32_e32 v145, 16, v47
	v_fmac_f32_e32 v134, v144, v144
	v_and_b32_e32 v162, 0xffff0000, v47
	v_fmac_f32_e32 v134, v145, v145
	v_fmac_f32_e32 v134, v162, v162
	v_add_f32_e32 v132, v132, v134
	s_waitcnt vmcnt(10)
	v_and_b32_e32 v134, 0xffff0000, v40
	v_lshlrev_b32_e32 v133, 16, v40
	v_mul_f32_e32 v134, v134, v134
	v_lshlrev_b32_e32 v135, 16, v41
	v_fmac_f32_e32 v134, v133, v133
	v_and_b32_e32 v136, 0xffff0000, v41
	v_fmac_f32_e32 v134, v135, v135
	v_lshlrev_b32_e32 v137, 16, v42
	v_fmac_f32_e32 v134, v136, v136
	v_and_b32_e32 v144, 0xffff0000, v42
	v_fmac_f32_e32 v134, v137, v137
	v_lshlrev_b32_e32 v145, 16, v43
	v_fmac_f32_e32 v134, v144, v144
	v_and_b32_e32 v162, 0xffff0000, v43
	v_fmac_f32_e32 v134, v145, v145
	v_fmac_f32_e32 v134, v162, v162
	v_add_f32_e32 v132, v132, v134
	s_waitcnt vmcnt(9)
	v_and_b32_e32 v134, 0xffff0000, v36
	v_lshlrev_b32_e32 v133, 16, v36
	v_mul_f32_e32 v134, v134, v134
	v_lshlrev_b32_e32 v135, 16, v37
	v_fmac_f32_e32 v134, v133, v133
	v_and_b32_e32 v136, 0xffff0000, v37
	v_fmac_f32_e32 v134, v135, v135
	v_lshlrev_b32_e32 v137, 16, v38
	v_fmac_f32_e32 v134, v136, v136
	v_and_b32_e32 v144, 0xffff0000, v38
	v_fmac_f32_e32 v134, v137, v137
	v_lshlrev_b32_e32 v145, 16, v39
	v_fmac_f32_e32 v134, v144, v144
	v_and_b32_e32 v162, 0xffff0000, v39
	v_fmac_f32_e32 v134, v145, v145
	v_fmac_f32_e32 v134, v162, v162
	v_add_f32_e32 v132, v132, v134
	s_waitcnt vmcnt(8)
	v_and_b32_e32 v134, 0xffff0000, v32
	v_lshlrev_b32_e32 v133, 16, v32
	v_mul_f32_e32 v134, v134, v134
	v_lshlrev_b32_e32 v135, 16, v33
	v_fmac_f32_e32 v134, v133, v133
	v_and_b32_e32 v136, 0xffff0000, v33
	v_fmac_f32_e32 v134, v135, v135
	v_lshlrev_b32_e32 v137, 16, v34
	v_fmac_f32_e32 v134, v136, v136
	v_and_b32_e32 v144, 0xffff0000, v34
	v_fmac_f32_e32 v134, v137, v137
	v_lshlrev_b32_e32 v145, 16, v35
	v_fmac_f32_e32 v134, v144, v144
	v_and_b32_e32 v162, 0xffff0000, v35
	v_fmac_f32_e32 v134, v145, v145
	v_fmac_f32_e32 v134, v162, v162
	v_add_f32_e32 v170, v132, v134
	s_waitcnt vmcnt(6)
	v_and_b32_e32 v135, 0xffff0000, v24
	v_and_b32_e32 v134, 0xffff0000, v28
	v_lshlrev_b32_e32 v133, 16, v24
	v_lshlrev_b32_e32 v132, 16, v28
	v_pk_mul_f32 v[134:135], v[134:135], v[134:135]
	v_lshlrev_b32_e32 v137, 16, v25
	v_lshlrev_b32_e32 v136, 16, v29
	v_pk_fma_f32 v[132:133], v[132:133], v[132:133], v[134:135]
	v_and_b32_e32 v145, 0xffff0000, v25
	v_and_b32_e32 v144, 0xffff0000, v29
	v_pk_fma_f32 v[132:133], v[136:137], v[136:137], v[132:133]
	v_lshlrev_b32_e32 v163, 16, v26
	v_lshlrev_b32_e32 v162, 16, v30
	v_pk_fma_f32 v[132:133], v[144:145], v[144:145], v[132:133]
	v_and_b32_e32 v165, 0xffff0000, v26
	v_and_b32_e32 v164, 0xffff0000, v30
	v_pk_fma_f32 v[132:133], v[162:163], v[162:163], v[132:133]
	v_lshlrev_b32_e32 v167, 16, v27
	v_lshlrev_b32_e32 v166, 16, v31
	v_pk_fma_f32 v[132:133], v[164:165], v[164:165], v[132:133]
	v_and_b32_e32 v169, 0xffff0000, v27
	v_and_b32_e32 v168, 0xffff0000, v31
	v_pk_fma_f32 v[132:133], v[166:167], v[166:167], v[132:133]
	s_waitcnt vmcnt(4)
	v_and_b32_e32 v135, 0xffff0000, v16
	v_pk_fma_f32 v[132:133], v[168:169], v[168:169], v[132:133]
	v_and_b32_e32 v134, 0xffff0000, v20
	v_add_f32_e32 v132, v170, v132
	v_add_f32_e32 v170, v132, v133
	v_lshlrev_b32_e32 v133, 16, v16
	v_lshlrev_b32_e32 v132, 16, v20
	v_pk_mul_f32 v[134:135], v[134:135], v[134:135]
	v_lshlrev_b32_e32 v137, 16, v17
	v_lshlrev_b32_e32 v136, 16, v21
	v_pk_fma_f32 v[132:133], v[132:133], v[132:133], v[134:135]
	v_and_b32_e32 v145, 0xffff0000, v17
	v_and_b32_e32 v144, 0xffff0000, v21
	v_pk_fma_f32 v[132:133], v[136:137], v[136:137], v[132:133]
	v_lshlrev_b32_e32 v163, 16, v18
	v_lshlrev_b32_e32 v162, 16, v22
	v_pk_fma_f32 v[132:133], v[144:145], v[144:145], v[132:133]
	v_and_b32_e32 v165, 0xffff0000, v18
	v_and_b32_e32 v164, 0xffff0000, v22
	v_pk_fma_f32 v[132:133], v[162:163], v[162:163], v[132:133]
	v_lshlrev_b32_e32 v167, 16, v19
	v_lshlrev_b32_e32 v166, 16, v23
	v_pk_fma_f32 v[132:133], v[164:165], v[164:165], v[132:133]
	v_and_b32_e32 v169, 0xffff0000, v19
	v_and_b32_e32 v168, 0xffff0000, v23
	v_pk_fma_f32 v[132:133], v[166:167], v[166:167], v[132:133]
	s_waitcnt vmcnt(2)
	v_and_b32_e32 v135, 0xffff0000, v8
	v_pk_fma_f32 v[132:133], v[168:169], v[168:169], v[132:133]
	v_and_b32_e32 v134, 0xffff0000, v12
	v_add_f32_e32 v132, v170, v132
	v_add_f32_e32 v170, v132, v133
	v_lshlrev_b32_e32 v133, 16, v8
	v_lshlrev_b32_e32 v132, 16, v12
	v_pk_mul_f32 v[134:135], v[134:135], v[134:135]
	v_lshlrev_b32_e32 v137, 16, v9
	v_lshlrev_b32_e32 v136, 16, v13
	v_pk_fma_f32 v[132:133], v[132:133], v[132:133], v[134:135]
	v_and_b32_e32 v145, 0xffff0000, v9
	v_and_b32_e32 v144, 0xffff0000, v13
	v_pk_fma_f32 v[132:133], v[136:137], v[136:137], v[132:133]
	v_lshlrev_b32_e32 v163, 16, v10
	v_lshlrev_b32_e32 v162, 16, v14
	v_pk_fma_f32 v[132:133], v[144:145], v[144:145], v[132:133]
	v_and_b32_e32 v165, 0xffff0000, v10
	v_and_b32_e32 v164, 0xffff0000, v14
	v_pk_fma_f32 v[132:133], v[162:163], v[162:163], v[132:133]
	v_lshlrev_b32_e32 v167, 16, v11
	v_lshlrev_b32_e32 v166, 16, v15
	v_pk_fma_f32 v[132:133], v[164:165], v[164:165], v[132:133]
	v_and_b32_e32 v169, 0xffff0000, v11
	v_and_b32_e32 v168, 0xffff0000, v15
	v_pk_fma_f32 v[132:133], v[166:167], v[166:167], v[132:133]
	s_waitcnt vmcnt(0)
	v_and_b32_e32 v135, 0xffff0000, v0
	v_pk_fma_f32 v[132:133], v[168:169], v[168:169], v[132:133]
	v_and_b32_e32 v134, 0xffff0000, v4
	v_add_f32_e32 v132, v170, v132
	v_add_f32_e32 v170, v132, v133
	v_lshlrev_b32_e32 v133, 16, v0
	v_lshlrev_b32_e32 v132, 16, v4
	v_pk_mul_f32 v[134:135], v[134:135], v[134:135]
	v_lshlrev_b32_e32 v137, 16, v1
	v_lshlrev_b32_e32 v136, 16, v5
	v_pk_fma_f32 v[132:133], v[132:133], v[132:133], v[134:135]
	v_and_b32_e32 v145, 0xffff0000, v1
	v_and_b32_e32 v144, 0xffff0000, v5
	v_pk_fma_f32 v[132:133], v[136:137], v[136:137], v[132:133]
	v_lshlrev_b32_e32 v163, 16, v2
	v_lshlrev_b32_e32 v162, 16, v6
	v_pk_fma_f32 v[132:133], v[144:145], v[144:145], v[132:133]
	v_and_b32_e32 v165, 0xffff0000, v2
	v_and_b32_e32 v164, 0xffff0000, v6
	v_pk_fma_f32 v[132:133], v[162:163], v[162:163], v[132:133]
	v_lshlrev_b32_e32 v167, 16, v3
	v_lshlrev_b32_e32 v166, 16, v7
	v_pk_fma_f32 v[132:133], v[164:165], v[164:165], v[132:133]
	v_and_b32_e32 v169, 0xffff0000, v3
	v_and_b32_e32 v168, 0xffff0000, v7
	v_pk_fma_f32 v[132:133], v[166:167], v[166:167], v[132:133]
	s_nop 0
	v_pk_fma_f32 v[132:133], v[168:169], v[168:169], v[132:133]
	s_nop 0
	v_add_f32_e32 v132, v170, v132
	v_add_f32_e32 v132, v132, v133
	ds_bpermute_b32 v133, v150, v132
	s_waitcnt lgkmcnt(0)
	v_add_f32_e32 v132, v132, v133
	ds_bpermute_b32 v133, v151, v132
	s_waitcnt lgkmcnt(0)
	v_add_f32_e32 v132, v132, v133
	v_fmamk_f32 v132, v132, 0x3a800000, v213
	v_cmp_gt_f32_e32 vcc, s63, v132
	v_mul_f32_e32 v133, 0x4b800000, v132
	s_nop 0
	v_cndmask_b32_e32 v132, v132, v133, vcc
	v_rsq_f32_e32 v132, v132
	s_nop 0
	v_mul_f32_e32 v133, 0x45800000, v132
	v_cndmask_b32_e32 v112, v132, v133, vcc
	v_mov_b32_e32 v132, 0x2000
	v_cndmask_b32_e64 v132, v132, 0, s[38:39]
	v_add_u32_e32 v162, v152, v132
	v_lshl_add_u64 v[144:145], v[140:141], 0, v[130:131]
	ds_read_b128 v[164:167], v162
	ds_read_b128 v[168:171], v162 offset:16
	ds_read_b128 v[134:137], v162 offset:4096
	ds_read_b128 v[130:133], v162 offset:4112
	v_lshlrev_b32_e32 v163, 16, v126
	v_and_b32_e32 v126, 0xffff0000, v126
	v_mul_f32_e32 v126, v112, v126
	s_waitcnt lgkmcnt(1)
	v_fma_f32 v126, v126, v165, v135
	v_lshlrev_b32_e32 v135, 16, v127
	v_and_b32_e32 v127, 0xffff0000, v127
	v_mul_f32_e32 v127, v112, v127
	v_fmac_f32_e32 v137, v127, v167
	v_lshlrev_b32_e32 v127, 16, v128
	v_mul_f32_e32 v127, v112, v127
	s_waitcnt lgkmcnt(0)
	v_fma_f32 v127, v127, v168, v130
	v_and_b32_e32 v128, 0xffff0000, v128
	v_lshlrev_b32_e32 v130, 16, v129
	v_and_b32_e32 v129, 0xffff0000, v129
	v_mul_f32_e32 v163, v112, v163
	v_mul_f32_e32 v135, v112, v135
	v_mul_f32_e32 v128, v112, v128
	v_mul_f32_e32 v130, v112, v130
	v_mul_f32_e32 v129, v112, v129
	v_fma_f32 v134, v163, v164, v134
	v_fma_f32 v135, v135, v166, v136
	v_fma_f32 v128, v128, v169, v131
	v_fma_f32 v130, v130, v170, v132
	v_fmac_f32_e32 v133, v129, v171
	s_and_saveexec_b64 s[0:1], s[42:43]
	v_mul_f32_e32 v129, 0x41800000, v134
	v_mul_f32_e32 v131, 0x41800000, v126
	v_med3_f32 v129, v129, s25, v218
	v_med3_f32 v131, v131, s25, v218
	v_cvt_pk_fp8_f32 v164, v129, v131
	v_mul_f32_e32 v132, 0x41800000, v135
	v_mul_f32_e32 v129, 0x41800000, v137
	v_med3_f32 v131, v132, s25, v218
	v_med3_f32 v129, v129, s25, v218
	v_cvt_pk_fp8_f32 v164, v131, v129 op_sel:[0,0,1]
	v_mul_f32_e32 v129, 0x41800000, v127
	v_mul_f32_e32 v131, 0x41800000, v128
	v_med3_f32 v129, v129, s25, v218
	v_med3_f32 v131, v131, s25, v218
	v_cvt_pk_fp8_f32 v165, v129, v131
	v_mul_f32_e32 v132, 0x41800000, v130
	v_mul_f32_e32 v129, 0x41800000, v133
	v_med3_f32 v131, v132, s25, v218
	v_med3_f32 v129, v129, s25, v218
	v_cvt_pk_fp8_f32 v165, v131, v129 op_sel:[0,0,1]
	global_store_dwordx2 v[144:145], v[164:165], off
.LBB0_1232:
	s_or_b64 exec, exec, s[0:1]
	v_cvt_pk_bf16_f32 v164, v134, v126
	v_cvt_pk_bf16_f32 v165, v135, v137
	v_cvt_pk_bf16_f32 v166, v127, v128
	v_cvt_pk_bf16_f32 v167, v130, v133
	v_lshlrev_b32_e32 v163, 16, v122
	v_and_b32_e32 v131, 0xffff0000, v164
	v_lshlrev_b32_e32 v129, 16, v164
	v_sub_f32_e32 v126, v126, v131
	v_sub_f32_e32 v129, v134, v129
	v_cvt_pk_bf16_f32 v134, v129, v126
	v_lshlrev_b32_e32 v126, 16, v165
	v_sub_f32_e32 v126, v135, v126
	v_and_b32_e32 v129, 0xffff0000, v165
	v_sub_f32_e32 v129, v137, v129
	v_cvt_pk_bf16_f32 v135, v126, v129
	v_lshlrev_b32_e32 v126, 16, v166
	v_sub_f32_e32 v126, v127, v126
	v_and_b32_e32 v127, 0xffff0000, v166
	v_sub_f32_e32 v127, v128, v127
	v_cvt_pk_bf16_f32 v136, v126, v127
	v_lshlrev_b32_e32 v126, 16, v167
	v_and_b32_e32 v127, 0xffff0000, v167
	v_sub_f32_e32 v126, v130, v126
	v_sub_f32_e32 v127, v133, v127
	v_cvt_pk_bf16_f32 v137, v126, v127
	ds_read_b128 v[126:129], v153 offset:1024
	v_and_b32_e32 v122, 0xffff0000, v122
	s_waitcnt lgkmcnt(0)
	v_mfma_f32_16x16x32_bf16 v[130:133], v[164:167], v[126:129], 0
	v_mul_f32_e32 v122, v112, v122
	v_mul_f32_e32 v163, v112, v163
	v_mfma_f32_16x16x32_bf16 v[126:129], v[134:137], v[126:129], v[130:133]
	s_nop 4
	ds_read_b128 v[130:133], v153 offset:34048
	s_waitcnt lgkmcnt(0)
	v_mfma_f32_16x16x32_bf16 v[126:129], v[164:167], v[130:133], v[126:129]
	ds_read_b128 v[134:137], v162 offset:4224
	ds_read_b128 v[164:167], v162 offset:128
	ds_read_b128 v[130:133], v162 offset:4240
	ds_read_b128 v[168:171], v162 offset:144
	s_waitcnt lgkmcnt(2)
	v_fma_f32 v122, v122, v165, v135
	v_lshlrev_b32_e32 v135, 16, v123
	v_and_b32_e32 v123, 0xffff0000, v123
	v_mul_f32_e32 v123, v112, v123
	v_fmac_f32_e32 v137, v123, v167
	v_lshlrev_b32_e32 v123, 16, v124
	v_mul_f32_e32 v123, v112, v123
	s_waitcnt lgkmcnt(0)
	v_fma_f32 v123, v123, v168, v130
	v_and_b32_e32 v124, 0xffff0000, v124
	v_lshlrev_b32_e32 v130, 16, v125
	v_and_b32_e32 v125, 0xffff0000, v125
	v_mul_f32_e32 v135, v112, v135
	v_mul_f32_e32 v124, v112, v124
	v_mul_f32_e32 v130, v112, v130
	v_mul_f32_e32 v125, v112, v125
	v_fma_f32 v134, v163, v164, v134
	v_fma_f32 v135, v135, v166, v136
	v_fma_f32 v124, v124, v169, v131
	v_fma_f32 v130, v130, v170, v132
	v_fmac_f32_e32 v133, v125, v171
	s_and_saveexec_b64 s[0:1], s[42:43]
	v_mul_f32_e32 v125, 0x41800000, v134
	v_mul_f32_e32 v131, 0x41800000, v122
	v_med3_f32 v125, v125, s25, v218
	v_med3_f32 v131, v131, s25, v218
	v_cvt_pk_fp8_f32 v164, v125, v131
	v_mul_f32_e32 v132, 0x41800000, v135
	v_mul_f32_e32 v125, 0x41800000, v137
	v_med3_f32 v131, v132, s25, v218
	v_med3_f32 v125, v125, s25, v218
	v_cvt_pk_fp8_f32 v164, v131, v125 op_sel:[0,0,1]
	v_mul_f32_e32 v125, 0x41800000, v123
	v_mul_f32_e32 v131, 0x41800000, v124
	v_med3_f32 v125, v125, s25, v218
	v_med3_f32 v131, v131, s25, v218
	v_cvt_pk_fp8_f32 v165, v125, v131
	v_mul_f32_e32 v132, 0x41800000, v130
	v_mul_f32_e32 v125, 0x41800000, v133
	v_med3_f32 v131, v132, s25, v218
	v_med3_f32 v125, v125, s25, v218
	v_cvt_pk_fp8_f32 v165, v131, v125 op_sel:[0,0,1]
	global_store_dwordx2 v[144:145], v[164:165], off offset:32
.LBB0_1234:
	s_or_b64 exec, exec, s[0:1]
	v_cvt_pk_bf16_f32 v164, v134, v122
	v_cvt_pk_bf16_f32 v165, v135, v137
	v_cvt_pk_bf16_f32 v166, v123, v124
	v_cvt_pk_bf16_f32 v167, v130, v133
	s_nop 0
	v_and_b32_e32 v131, 0xffff0000, v164
	v_lshlrev_b32_e32 v125, 16, v164
	v_sub_f32_e32 v122, v122, v131
	v_sub_f32_e32 v125, v134, v125
	v_cvt_pk_bf16_f32 v134, v125, v122
	v_lshlrev_b32_e32 v122, 16, v165
	v_sub_f32_e32 v122, v135, v122
	v_and_b32_e32 v125, 0xffff0000, v165
	v_sub_f32_e32 v125, v137, v125
	v_cvt_pk_bf16_f32 v135, v122, v125
	v_lshlrev_b32_e32 v122, 16, v166
	v_sub_f32_e32 v122, v123, v122
	v_and_b32_e32 v123, 0xffff0000, v166
	v_sub_f32_e32 v123, v124, v123
	v_cvt_pk_bf16_f32 v136, v122, v123
	v_lshlrev_b32_e32 v122, 16, v167
	v_and_b32_e32 v123, 0xffff0000, v167
	v_sub_f32_e32 v122, v130, v122
	v_sub_f32_e32 v123, v133, v123
	v_cvt_pk_bf16_f32 v137, v122, v123
	ds_read_b128 v[122:125], v153 offset:1088
	s_waitcnt lgkmcnt(0)
	v_mfma_f32_16x16x32_bf16 v[126:129], v[164:167], v[122:125], v[126:129]
	v_mfma_f32_16x16x32_bf16 v[122:125], v[134:137], v[122:125], v[126:129]
	s_nop 6
	ds_read_b128 v[126:129], v153 offset:34112
	s_waitcnt lgkmcnt(0)
	v_mfma_f32_16x16x32_bf16 v[122:125], v[164:167], v[126:129], v[122:125]
	ds_read_b128 v[130:133], v162 offset:4352
	ds_read_b128 v[134:137], v162 offset:256
	ds_read_b128 v[164:167], v162 offset:272
	ds_read_b128 v[126:129], v162 offset:4368
	v_lshlrev_b32_e32 v163, 16, v118
	v_and_b32_e32 v118, 0xffff0000, v118
	v_mul_f32_e32 v118, v112, v118
	s_waitcnt lgkmcnt(2)
	v_fma_f32 v118, v118, v135, v131
	v_lshlrev_b32_e32 v131, 16, v119
	v_and_b32_e32 v119, 0xffff0000, v119
	v_mul_f32_e32 v119, v112, v119
	v_fmac_f32_e32 v133, v119, v137
	v_lshlrev_b32_e32 v119, 16, v120
	v_mul_f32_e32 v119, v112, v119
	s_waitcnt lgkmcnt(0)
	v_fma_f32 v119, v119, v164, v126
	v_and_b32_e32 v120, 0xffff0000, v120
	v_lshlrev_b32_e32 v126, 16, v121
	v_and_b32_e32 v121, 0xffff0000, v121
	v_mul_f32_e32 v163, v112, v163
	v_mul_f32_e32 v131, v112, v131
	v_mul_f32_e32 v120, v112, v120
	v_mul_f32_e32 v126, v112, v126
	v_mul_f32_e32 v121, v112, v121
	v_fma_f32 v130, v163, v134, v130
	v_fma_f32 v131, v131, v136, v132
	v_fma_f32 v120, v120, v165, v127
	v_fma_f32 v126, v126, v166, v128
	v_fmac_f32_e32 v129, v121, v167
	s_and_saveexec_b64 s[0:1], s[42:43]
	v_mul_f32_e32 v121, 0x41800000, v130
	v_mul_f32_e32 v127, 0x41800000, v118
	v_med3_f32 v121, v121, s25, v218
	v_med3_f32 v127, v127, s25, v218
	v_cvt_pk_fp8_f32 v134, v121, v127
	v_mul_f32_e32 v128, 0x41800000, v131
	v_mul_f32_e32 v121, 0x41800000, v133
	v_med3_f32 v127, v128, s25, v218
	v_med3_f32 v121, v121, s25, v218
	v_cvt_pk_fp8_f32 v134, v127, v121 op_sel:[0,0,1]
	v_mul_f32_e32 v121, 0x41800000, v119
	v_mul_f32_e32 v127, 0x41800000, v120
	v_med3_f32 v121, v121, s25, v218
	v_med3_f32 v127, v127, s25, v218
	v_cvt_pk_fp8_f32 v135, v121, v127
	v_mul_f32_e32 v128, 0x41800000, v126
	v_mul_f32_e32 v121, 0x41800000, v129
	v_med3_f32 v127, v128, s25, v218
	v_med3_f32 v121, v121, s25, v218
	v_cvt_pk_fp8_f32 v135, v127, v121 op_sel:[0,0,1]
	global_store_dwordx2 v[144:145], v[134:135], off offset:64
.LBB0_1236:
	s_or_b64 exec, exec, s[0:1]
	v_cvt_pk_bf16_f32 v134, v130, v118
	v_cvt_pk_bf16_f32 v135, v131, v133
	v_cvt_pk_bf16_f32 v136, v119, v120
	v_cvt_pk_bf16_f32 v137, v126, v129
	v_lshlrev_b32_e32 v163, 16, v114
	v_and_b32_e32 v127, 0xffff0000, v134
	v_lshlrev_b32_e32 v121, 16, v134
	v_sub_f32_e32 v118, v118, v127
	v_sub_f32_e32 v121, v130, v121
	v_cvt_pk_bf16_f32 v130, v121, v118
	v_lshlrev_b32_e32 v118, 16, v135
	v_sub_f32_e32 v118, v131, v118
	v_and_b32_e32 v121, 0xffff0000, v135
	v_sub_f32_e32 v121, v133, v121
	v_cvt_pk_bf16_f32 v131, v118, v121
	v_lshlrev_b32_e32 v118, 16, v136
	v_sub_f32_e32 v118, v119, v118
	v_and_b32_e32 v119, 0xffff0000, v136
	v_sub_f32_e32 v119, v120, v119
	v_cvt_pk_bf16_f32 v132, v118, v119
	v_lshlrev_b32_e32 v118, 16, v137
	v_and_b32_e32 v119, 0xffff0000, v137
	v_sub_f32_e32 v118, v126, v118
	v_sub_f32_e32 v119, v129, v119
	v_cvt_pk_bf16_f32 v133, v118, v119
	ds_read_b128 v[118:121], v153 offset:1152
	v_and_b32_e32 v114, 0xffff0000, v114
	s_waitcnt lgkmcnt(0)
	v_mfma_f32_16x16x32_bf16 v[122:125], v[134:137], v[118:121], v[122:125]
	v_mul_f32_e32 v114, v112, v114
	v_mul_f32_e32 v163, v112, v163
	v_mfma_f32_16x16x32_bf16 v[118:121], v[130:133], v[118:121], v[122:125]
	s_nop 4
	ds_read_b128 v[122:125], v153 offset:34176
	s_waitcnt lgkmcnt(0)
	v_mfma_f32_16x16x32_bf16 v[118:121], v[134:137], v[122:125], v[118:121]
	ds_read_b128 v[126:129], v162 offset:4480
	ds_read_b128 v[130:133], v162 offset:384
	ds_read_b128 v[122:125], v162 offset:4496
	ds_read_b128 v[134:137], v162 offset:400
	s_waitcnt lgkmcnt(2)
	v_fma_f32 v114, v114, v131, v127
	v_lshlrev_b32_e32 v127, 16, v115
	v_and_b32_e32 v115, 0xffff0000, v115
	v_mul_f32_e32 v115, v112, v115
	v_fmac_f32_e32 v129, v115, v133
	v_lshlrev_b32_e32 v115, 16, v116
	v_mul_f32_e32 v115, v112, v115
	s_waitcnt lgkmcnt(0)
	v_fma_f32 v115, v115, v134, v122
	v_and_b32_e32 v116, 0xffff0000, v116
	v_lshlrev_b32_e32 v122, 16, v117
	v_and_b32_e32 v117, 0xffff0000, v117
	v_mul_f32_e32 v127, v112, v127
	v_mul_f32_e32 v116, v112, v116
	v_mul_f32_e32 v122, v112, v122
	v_mul_f32_e32 v117, v112, v117
	v_fma_f32 v126, v163, v130, v126
	v_fma_f32 v127, v127, v132, v128
	v_fma_f32 v116, v116, v135, v123
	v_fma_f32 v122, v122, v136, v124
	v_fmac_f32_e32 v125, v117, v137
	s_and_saveexec_b64 s[0:1], s[42:43]
	v_mul_f32_e32 v117, 0x41800000, v126
	v_mul_f32_e32 v123, 0x41800000, v114
	v_med3_f32 v117, v117, s25, v218
	v_med3_f32 v123, v123, s25, v218
	v_cvt_pk_fp8_f32 v130, v117, v123
	v_mul_f32_e32 v124, 0x41800000, v127
	v_mul_f32_e32 v117, 0x41800000, v129
	v_med3_f32 v123, v124, s25, v218
	v_med3_f32 v117, v117, s25, v218
	v_cvt_pk_fp8_f32 v130, v123, v117 op_sel:[0,0,1]
	v_mul_f32_e32 v117, 0x41800000, v115
	v_mul_f32_e32 v123, 0x41800000, v116
	v_med3_f32 v117, v117, s25, v218
	v_med3_f32 v123, v123, s25, v218
	v_cvt_pk_fp8_f32 v131, v117, v123
	v_mul_f32_e32 v124, 0x41800000, v122
	v_mul_f32_e32 v117, 0x41800000, v125
	v_med3_f32 v123, v124, s25, v218
	v_med3_f32 v117, v117, s25, v218
	v_cvt_pk_fp8_f32 v131, v123, v117 op_sel:[0,0,1]
	global_store_dwordx2 v[144:145], v[130:131], off offset:96
.LBB0_1238:
	s_or_b64 exec, exec, s[0:1]
	v_cvt_pk_bf16_f32 v130, v126, v114
	v_cvt_pk_bf16_f32 v131, v127, v129
	v_cvt_pk_bf16_f32 v132, v115, v116
	v_cvt_pk_bf16_f32 v133, v122, v125
	s_nop 0
	v_and_b32_e32 v123, 0xffff0000, v130
	v_lshlrev_b32_e32 v117, 16, v130
	v_sub_f32_e32 v114, v114, v123
	v_sub_f32_e32 v117, v126, v117
	v_cvt_pk_bf16_f32 v126, v117, v114
	v_lshlrev_b32_e32 v114, 16, v131
	v_sub_f32_e32 v114, v127, v114
	v_and_b32_e32 v117, 0xffff0000, v131
	v_sub_f32_e32 v117, v129, v117
	v_cvt_pk_bf16_f32 v127, v114, v117
	v_lshlrev_b32_e32 v114, 16, v132
	v_sub_f32_e32 v114, v115, v114
	v_and_b32_e32 v115, 0xffff0000, v132
	v_sub_f32_e32 v115, v116, v115
	v_cvt_pk_bf16_f32 v128, v114, v115
	v_lshlrev_b32_e32 v114, 16, v133
	v_and_b32_e32 v115, 0xffff0000, v133
	v_sub_f32_e32 v114, v122, v114
	v_sub_f32_e32 v115, v125, v115
	v_cvt_pk_bf16_f32 v129, v114, v115
	ds_read_b128 v[114:117], v153 offset:1216
	s_waitcnt lgkmcnt(0)
	v_mfma_f32_16x16x32_bf16 v[118:121], v[130:133], v[114:117], v[118:121]
	v_mfma_f32_16x16x32_bf16 v[114:117], v[126:129], v[114:117], v[118:121]
	s_nop 6
	ds_read_b128 v[118:121], v153 offset:34240
	s_waitcnt lgkmcnt(0)
	v_mfma_f32_16x16x32_bf16 v[114:117], v[130:133], v[118:121], v[114:117]
	ds_read_b128 v[122:125], v162 offset:4608
	ds_read_b128 v[126:129], v162 offset:512
	ds_read_b128 v[130:133], v162 offset:528
	ds_read_b128 v[118:121], v162 offset:4624
	v_lshlrev_b32_e32 v134, 16, v108
	v_and_b32_e32 v108, 0xffff0000, v108
	v_mul_f32_e32 v108, v112, v108
	s_waitcnt lgkmcnt(2)
	v_fma_f32 v108, v108, v127, v123
	v_lshlrev_b32_e32 v123, 16, v109
	v_and_b32_e32 v109, 0xffff0000, v109
	v_mul_f32_e32 v109, v112, v109
	v_fmac_f32_e32 v125, v109, v129
	v_lshlrev_b32_e32 v109, 16, v110
	v_mul_f32_e32 v109, v112, v109
	s_waitcnt lgkmcnt(0)
	v_fma_f32 v109, v109, v130, v118
	v_and_b32_e32 v110, 0xffff0000, v110
	v_lshlrev_b32_e32 v118, 16, v111
	v_and_b32_e32 v111, 0xffff0000, v111
	v_mul_f32_e32 v134, v112, v134
	v_mul_f32_e32 v123, v112, v123
	v_mul_f32_e32 v110, v112, v110
	v_mul_f32_e32 v118, v112, v118
	v_mul_f32_e32 v111, v112, v111
	v_fma_f32 v122, v134, v126, v122
	v_fma_f32 v123, v123, v128, v124
	v_fma_f32 v110, v110, v131, v119
	v_fma_f32 v118, v118, v132, v120
	v_fmac_f32_e32 v121, v111, v133
	s_and_saveexec_b64 s[0:1], s[42:43]
	v_mul_f32_e32 v111, 0x41800000, v122
	v_mul_f32_e32 v119, 0x41800000, v108
	v_med3_f32 v111, v111, s25, v218
	v_med3_f32 v119, v119, s25, v218
	v_cvt_pk_fp8_f32 v126, v111, v119
	v_mul_f32_e32 v120, 0x41800000, v123
	v_mul_f32_e32 v111, 0x41800000, v125
	v_med3_f32 v119, v120, s25, v218
	v_med3_f32 v111, v111, s25, v218
	v_cvt_pk_fp8_f32 v126, v119, v111 op_sel:[0,0,1]
	v_mul_f32_e32 v111, 0x41800000, v109
	v_mul_f32_e32 v119, 0x41800000, v110
	v_med3_f32 v111, v111, s25, v218
	v_med3_f32 v119, v119, s25, v218
	v_cvt_pk_fp8_f32 v127, v111, v119
	v_mul_f32_e32 v120, 0x41800000, v118
	v_mul_f32_e32 v111, 0x41800000, v121
	v_med3_f32 v119, v120, s25, v218
	v_med3_f32 v111, v111, s25, v218
	v_cvt_pk_fp8_f32 v127, v119, v111 op_sel:[0,0,1]
	global_store_dwordx2 v[144:145], v[126:127], off offset:128
.LBB0_1240:
	s_or_b64 exec, exec, s[0:1]
	v_cvt_pk_bf16_f32 v126, v122, v108
	v_cvt_pk_bf16_f32 v127, v123, v125
	v_cvt_pk_bf16_f32 v128, v109, v110
	v_cvt_pk_bf16_f32 v129, v118, v121
	v_lshlrev_b32_e32 v130, 16, v104
	v_and_b32_e32 v119, 0xffff0000, v126
	v_lshlrev_b32_e32 v111, 16, v126
	v_sub_f32_e32 v108, v108, v119
	v_sub_f32_e32 v111, v122, v111
	v_cvt_pk_bf16_f32 v122, v111, v108
	v_lshlrev_b32_e32 v108, 16, v127
	v_sub_f32_e32 v108, v123, v108
	v_and_b32_e32 v111, 0xffff0000, v127
	v_sub_f32_e32 v111, v125, v111
	v_cvt_pk_bf16_f32 v123, v108, v111
	v_lshlrev_b32_e32 v108, 16, v128
	v_sub_f32_e32 v108, v109, v108
	v_and_b32_e32 v109, 0xffff0000, v128
	v_sub_f32_e32 v109, v110, v109
	v_cvt_pk_bf16_f32 v124, v108, v109
	v_lshlrev_b32_e32 v108, 16, v129
	v_and_b32_e32 v109, 0xffff0000, v129
	v_sub_f32_e32 v108, v118, v108
	v_sub_f32_e32 v109, v121, v109
	v_cvt_pk_bf16_f32 v125, v108, v109
	ds_read_b128 v[108:111], v153 offset:1280
	v_and_b32_e32 v104, 0xffff0000, v104
	s_waitcnt lgkmcnt(0)
	v_mfma_f32_16x16x32_bf16 v[114:117], v[126:129], v[108:111], v[114:117]
	v_mul_f32_e32 v104, v112, v104
	v_mul_f32_e32 v130, v112, v130
	v_mfma_f32_16x16x32_bf16 v[108:111], v[122:125], v[108:111], v[114:117]
	s_nop 4
	ds_read_b128 v[114:117], v153 offset:34304
	s_waitcnt lgkmcnt(0)
	v_mfma_f32_16x16x32_bf16 v[108:111], v[126:129], v[114:117], v[108:111]
	ds_read_b128 v[118:121], v162 offset:4736
	ds_read_b128 v[122:125], v162 offset:640
	ds_read_b128 v[114:117], v162 offset:4752
	ds_read_b128 v[126:129], v162 offset:656
	s_waitcnt lgkmcnt(2)
	v_fma_f32 v104, v104, v123, v119
	v_lshlrev_b32_e32 v119, 16, v105
	v_and_b32_e32 v105, 0xffff0000, v105
	v_mul_f32_e32 v105, v112, v105
	v_fmac_f32_e32 v121, v105, v125
	v_lshlrev_b32_e32 v105, 16, v106
	v_mul_f32_e32 v105, v112, v105
	s_waitcnt lgkmcnt(0)
	v_fma_f32 v105, v105, v126, v114
	v_and_b32_e32 v106, 0xffff0000, v106
	v_lshlrev_b32_e32 v114, 16, v107
	v_and_b32_e32 v107, 0xffff0000, v107
	v_mul_f32_e32 v119, v112, v119
	v_mul_f32_e32 v106, v112, v106
	v_mul_f32_e32 v114, v112, v114
	v_mul_f32_e32 v107, v112, v107
	v_fma_f32 v118, v130, v122, v118
	v_fma_f32 v119, v119, v124, v120
	v_fma_f32 v106, v106, v127, v115
	v_fma_f32 v114, v114, v128, v116
	v_fmac_f32_e32 v117, v107, v129
	s_and_saveexec_b64 s[0:1], s[42:43]
	v_mul_f32_e32 v107, 0x41800000, v118
	v_mul_f32_e32 v115, 0x41800000, v104
	v_med3_f32 v107, v107, s25, v218
	v_med3_f32 v115, v115, s25, v218
	v_cvt_pk_fp8_f32 v122, v107, v115
	v_mul_f32_e32 v116, 0x41800000, v119
	v_mul_f32_e32 v107, 0x41800000, v121
	v_med3_f32 v115, v116, s25, v218
	v_med3_f32 v107, v107, s25, v218
	v_cvt_pk_fp8_f32 v122, v115, v107 op_sel:[0,0,1]
	v_mul_f32_e32 v107, 0x41800000, v105
	v_mul_f32_e32 v115, 0x41800000, v106
	v_med3_f32 v107, v107, s25, v218
	v_med3_f32 v115, v115, s25, v218
	v_cvt_pk_fp8_f32 v123, v107, v115
	v_mul_f32_e32 v116, 0x41800000, v114
	v_mul_f32_e32 v107, 0x41800000, v117
	v_med3_f32 v115, v116, s25, v218
	v_med3_f32 v107, v107, s25, v218
	v_cvt_pk_fp8_f32 v123, v115, v107 op_sel:[0,0,1]
	global_store_dwordx2 v[144:145], v[122:123], off offset:160
.LBB0_1242:
	s_or_b64 exec, exec, s[0:1]
	v_cvt_pk_bf16_f32 v122, v118, v104
	v_cvt_pk_bf16_f32 v123, v119, v121
	v_cvt_pk_bf16_f32 v124, v105, v106
	v_cvt_pk_bf16_f32 v125, v114, v117
	s_nop 0
	v_and_b32_e32 v115, 0xffff0000, v122
	v_lshlrev_b32_e32 v107, 16, v122
	v_sub_f32_e32 v104, v104, v115
	v_sub_f32_e32 v107, v118, v107
	v_cvt_pk_bf16_f32 v118, v107, v104
	v_lshlrev_b32_e32 v104, 16, v123
	v_sub_f32_e32 v104, v119, v104
	v_and_b32_e32 v107, 0xffff0000, v123
	v_sub_f32_e32 v107, v121, v107
	v_cvt_pk_bf16_f32 v119, v104, v107
	v_lshlrev_b32_e32 v104, 16, v124
	v_sub_f32_e32 v104, v105, v104
	v_and_b32_e32 v105, 0xffff0000, v124
	v_sub_f32_e32 v105, v106, v105
	v_cvt_pk_bf16_f32 v120, v104, v105
	v_lshlrev_b32_e32 v104, 16, v125
	v_and_b32_e32 v105, 0xffff0000, v125
	v_sub_f32_e32 v104, v114, v104
	v_sub_f32_e32 v105, v117, v105
	v_cvt_pk_bf16_f32 v121, v104, v105
	ds_read_b128 v[104:107], v153 offset:1344
	s_waitcnt lgkmcnt(0)
	v_mfma_f32_16x16x32_bf16 v[108:111], v[122:125], v[104:107], v[108:111]
	v_mfma_f32_16x16x32_bf16 v[104:107], v[118:121], v[104:107], v[108:111]
	s_nop 6
	ds_read_b128 v[108:111], v153 offset:34368
	s_waitcnt lgkmcnt(0)
	v_mfma_f32_16x16x32_bf16 v[104:107], v[122:125], v[108:111], v[104:107]
	ds_read_b128 v[114:117], v162 offset:4864
	ds_read_b128 v[118:121], v162 offset:768
	ds_read_b128 v[122:125], v162 offset:784
	ds_read_b128 v[108:111], v162 offset:4880
	v_lshlrev_b32_e32 v126, 16, v100
	v_and_b32_e32 v100, 0xffff0000, v100
	v_mul_f32_e32 v100, v112, v100
	s_waitcnt lgkmcnt(2)
	v_fma_f32 v100, v100, v119, v115
	v_lshlrev_b32_e32 v115, 16, v101
	v_and_b32_e32 v101, 0xffff0000, v101
	v_mul_f32_e32 v101, v112, v101
	v_fmac_f32_e32 v117, v101, v121
	v_lshlrev_b32_e32 v101, 16, v102
	v_mul_f32_e32 v101, v112, v101
	s_waitcnt lgkmcnt(0)
	v_fma_f32 v101, v101, v122, v108
	v_and_b32_e32 v102, 0xffff0000, v102
	v_lshlrev_b32_e32 v108, 16, v103
	v_and_b32_e32 v103, 0xffff0000, v103
	v_mul_f32_e32 v126, v112, v126
	v_mul_f32_e32 v115, v112, v115
	v_mul_f32_e32 v102, v112, v102
	v_mul_f32_e32 v108, v112, v108
	v_mul_f32_e32 v103, v112, v103
	v_fma_f32 v114, v126, v118, v114
	v_fma_f32 v115, v115, v120, v116
	v_fma_f32 v102, v102, v123, v109
	v_fma_f32 v108, v108, v124, v110
	v_fmac_f32_e32 v111, v103, v125
	s_and_saveexec_b64 s[0:1], s[42:43]
	v_mul_f32_e32 v103, 0x41800000, v114
	v_mul_f32_e32 v109, 0x41800000, v100
	v_med3_f32 v103, v103, s25, v218
	v_med3_f32 v109, v109, s25, v218
	v_cvt_pk_fp8_f32 v118, v103, v109
	v_mul_f32_e32 v110, 0x41800000, v115
	v_mul_f32_e32 v103, 0x41800000, v117
	v_med3_f32 v109, v110, s25, v218
	v_med3_f32 v103, v103, s25, v218
	v_cvt_pk_fp8_f32 v118, v109, v103 op_sel:[0,0,1]
	v_mul_f32_e32 v103, 0x41800000, v101
	v_mul_f32_e32 v109, 0x41800000, v102
	v_med3_f32 v103, v103, s25, v218
	v_med3_f32 v109, v109, s25, v218
	v_cvt_pk_fp8_f32 v119, v103, v109
	v_mul_f32_e32 v110, 0x41800000, v108
	v_mul_f32_e32 v103, 0x41800000, v111
	v_med3_f32 v109, v110, s25, v218
	v_med3_f32 v103, v103, s25, v218
	v_cvt_pk_fp8_f32 v119, v109, v103 op_sel:[0,0,1]
	global_store_dwordx2 v[144:145], v[118:119], off offset:192
.LBB0_1244:
	s_or_b64 exec, exec, s[0:1]
	v_cvt_pk_bf16_f32 v118, v114, v100
	v_cvt_pk_bf16_f32 v119, v115, v117
	v_cvt_pk_bf16_f32 v120, v101, v102
	v_cvt_pk_bf16_f32 v121, v108, v111
	v_lshlrev_b32_e32 v122, 16, v96
	v_and_b32_e32 v109, 0xffff0000, v118
	v_lshlrev_b32_e32 v103, 16, v118
	v_sub_f32_e32 v100, v100, v109
	v_sub_f32_e32 v103, v114, v103
	v_cvt_pk_bf16_f32 v114, v103, v100
	v_lshlrev_b32_e32 v100, 16, v119
	v_sub_f32_e32 v100, v115, v100
	v_and_b32_e32 v103, 0xffff0000, v119
	v_sub_f32_e32 v103, v117, v103
	v_cvt_pk_bf16_f32 v115, v100, v103
	v_lshlrev_b32_e32 v100, 16, v120
	v_sub_f32_e32 v100, v101, v100
	v_and_b32_e32 v101, 0xffff0000, v120
	v_sub_f32_e32 v101, v102, v101
	v_cvt_pk_bf16_f32 v116, v100, v101
	v_lshlrev_b32_e32 v100, 16, v121
	v_and_b32_e32 v101, 0xffff0000, v121
	v_sub_f32_e32 v100, v108, v100
	v_sub_f32_e32 v101, v111, v101
	v_cvt_pk_bf16_f32 v117, v100, v101
	ds_read_b128 v[100:103], v153 offset:1408
	v_and_b32_e32 v96, 0xffff0000, v96
	s_waitcnt lgkmcnt(0)
	v_mfma_f32_16x16x32_bf16 v[104:107], v[118:121], v[100:103], v[104:107]
	v_mul_f32_e32 v96, v112, v96
	v_mul_f32_e32 v122, v112, v122
	v_mfma_f32_16x16x32_bf16 v[100:103], v[114:117], v[100:103], v[104:107]
	s_nop 4
	ds_read_b128 v[104:107], v153 offset:34432
	s_waitcnt lgkmcnt(0)
	v_mfma_f32_16x16x32_bf16 v[100:103], v[118:121], v[104:107], v[100:103]
	ds_read_b128 v[108:111], v162 offset:4992
	ds_read_b128 v[114:117], v162 offset:896
	ds_read_b128 v[104:107], v162 offset:5008
	ds_read_b128 v[118:121], v162 offset:912
	s_waitcnt lgkmcnt(2)
	v_fma_f32 v96, v96, v115, v109
	v_lshlrev_b32_e32 v109, 16, v97
	v_and_b32_e32 v97, 0xffff0000, v97
	v_mul_f32_e32 v97, v112, v97
	v_fmac_f32_e32 v111, v97, v117
	v_lshlrev_b32_e32 v97, 16, v98
	v_mul_f32_e32 v97, v112, v97
	s_waitcnt lgkmcnt(0)
	v_fma_f32 v97, v97, v118, v104
	v_and_b32_e32 v98, 0xffff0000, v98
	v_lshlrev_b32_e32 v104, 16, v99
	v_and_b32_e32 v99, 0xffff0000, v99
	v_mul_f32_e32 v109, v112, v109
	v_mul_f32_e32 v98, v112, v98
	v_mul_f32_e32 v104, v112, v104
	v_mul_f32_e32 v99, v112, v99
	v_fma_f32 v108, v122, v114, v108
	v_fma_f32 v109, v109, v116, v110
	v_fma_f32 v98, v98, v119, v105
	v_fma_f32 v104, v104, v120, v106
	v_fmac_f32_e32 v107, v99, v121
	s_and_saveexec_b64 s[0:1], s[42:43]
	v_mul_f32_e32 v99, 0x41800000, v108
	v_mul_f32_e32 v105, 0x41800000, v96
	v_med3_f32 v99, v99, s25, v218
	v_med3_f32 v105, v105, s25, v218
	v_cvt_pk_fp8_f32 v114, v99, v105
	v_mul_f32_e32 v106, 0x41800000, v109
	v_mul_f32_e32 v99, 0x41800000, v111
	v_med3_f32 v105, v106, s25, v218
	v_med3_f32 v99, v99, s25, v218
	v_cvt_pk_fp8_f32 v114, v105, v99 op_sel:[0,0,1]
	v_mul_f32_e32 v99, 0x41800000, v97
	v_mul_f32_e32 v105, 0x41800000, v98
	v_med3_f32 v99, v99, s25, v218
	v_med3_f32 v105, v105, s25, v218
	v_cvt_pk_fp8_f32 v115, v99, v105
	v_mul_f32_e32 v106, 0x41800000, v104
	v_mul_f32_e32 v99, 0x41800000, v107
	v_med3_f32 v105, v106, s25, v218
	v_med3_f32 v99, v99, s25, v218
	v_cvt_pk_fp8_f32 v115, v105, v99 op_sel:[0,0,1]
	global_store_dwordx2 v[144:145], v[114:115], off offset:224
.LBB0_1246:
	s_or_b64 exec, exec, s[0:1]
	v_cvt_pk_bf16_f32 v114, v108, v96
	v_cvt_pk_bf16_f32 v115, v109, v111
	v_cvt_pk_bf16_f32 v116, v97, v98
	v_cvt_pk_bf16_f32 v117, v104, v107
	s_nop 0
	v_and_b32_e32 v105, 0xffff0000, v114
	v_lshlrev_b32_e32 v99, 16, v114
	v_sub_f32_e32 v96, v96, v105
	v_sub_f32_e32 v99, v108, v99
	v_cvt_pk_bf16_f32 v108, v99, v96
	v_lshlrev_b32_e32 v96, 16, v115
	v_sub_f32_e32 v96, v109, v96
	v_and_b32_e32 v99, 0xffff0000, v115
	v_sub_f32_e32 v99, v111, v99
	v_cvt_pk_bf16_f32 v109, v96, v99
	v_lshlrev_b32_e32 v96, 16, v116
	v_sub_f32_e32 v96, v97, v96
	v_and_b32_e32 v97, 0xffff0000, v116
	v_sub_f32_e32 v97, v98, v97
	v_cvt_pk_bf16_f32 v110, v96, v97
	v_lshlrev_b32_e32 v96, 16, v117
	v_and_b32_e32 v97, 0xffff0000, v117
	v_sub_f32_e32 v96, v104, v96
	v_sub_f32_e32 v97, v107, v97
	v_cvt_pk_bf16_f32 v111, v96, v97
	ds_read_b128 v[96:99], v153 offset:1472
	s_waitcnt lgkmcnt(0)
	v_mfma_f32_16x16x32_bf16 v[100:103], v[114:117], v[96:99], v[100:103]
	v_mfma_f32_16x16x32_bf16 v[96:99], v[108:111], v[96:99], v[100:103]
	s_nop 6
	ds_read_b128 v[100:103], v153 offset:34496
	s_waitcnt lgkmcnt(0)
	v_mfma_f32_16x16x32_bf16 v[96:99], v[114:117], v[100:103], v[96:99]
	ds_read_b128 v[104:107], v162 offset:5120
	ds_read_b128 v[108:111], v162 offset:1024
	ds_read_b128 v[114:117], v162 offset:1040
	ds_read_b128 v[100:103], v162 offset:5136
	v_lshlrev_b32_e32 v118, 16, v92
	v_and_b32_e32 v92, 0xffff0000, v92
	v_mul_f32_e32 v92, v112, v92
	s_waitcnt lgkmcnt(2)
	v_fma_f32 v92, v92, v109, v105
	v_lshlrev_b32_e32 v105, 16, v93
	v_and_b32_e32 v93, 0xffff0000, v93
	v_mul_f32_e32 v93, v112, v93
	v_fmac_f32_e32 v107, v93, v111
	v_lshlrev_b32_e32 v93, 16, v94
	v_mul_f32_e32 v93, v112, v93
	s_waitcnt lgkmcnt(0)
	v_fma_f32 v93, v93, v114, v100
	v_and_b32_e32 v94, 0xffff0000, v94
	v_lshlrev_b32_e32 v100, 16, v95
	v_and_b32_e32 v95, 0xffff0000, v95
	v_mul_f32_e32 v118, v112, v118
	v_mul_f32_e32 v105, v112, v105
	v_mul_f32_e32 v94, v112, v94
	v_mul_f32_e32 v100, v112, v100
	v_mul_f32_e32 v95, v112, v95
	v_fma_f32 v104, v118, v108, v104
	v_fma_f32 v105, v105, v110, v106
	v_fma_f32 v94, v94, v115, v101
	v_fma_f32 v100, v100, v116, v102
	v_fmac_f32_e32 v103, v95, v117
	s_and_saveexec_b64 s[0:1], s[42:43]
	v_mul_f32_e32 v95, 0x41800000, v104
	v_mul_f32_e32 v101, 0x41800000, v92
	v_med3_f32 v95, v95, s25, v218
	v_med3_f32 v101, v101, s25, v218
	v_cvt_pk_fp8_f32 v108, v95, v101
	v_mul_f32_e32 v102, 0x41800000, v105
	v_mul_f32_e32 v95, 0x41800000, v107
	v_med3_f32 v101, v102, s25, v218
	v_med3_f32 v95, v95, s25, v218
	v_cvt_pk_fp8_f32 v108, v101, v95 op_sel:[0,0,1]
	v_mul_f32_e32 v95, 0x41800000, v93
	v_mul_f32_e32 v101, 0x41800000, v94
	v_med3_f32 v95, v95, s25, v218
	v_med3_f32 v101, v101, s25, v218
	v_cvt_pk_fp8_f32 v109, v95, v101
	v_mul_f32_e32 v102, 0x41800000, v100
	v_mul_f32_e32 v95, 0x41800000, v103
	v_med3_f32 v101, v102, s25, v218
	v_med3_f32 v95, v95, s25, v218
	v_cvt_pk_fp8_f32 v109, v101, v95 op_sel:[0,0,1]
	global_store_dwordx2 v[144:145], v[108:109], off offset:256
.LBB0_1248:
	s_or_b64 exec, exec, s[0:1]
	v_cvt_pk_bf16_f32 v108, v104, v92
	v_cvt_pk_bf16_f32 v109, v105, v107
	v_cvt_pk_bf16_f32 v110, v93, v94
	v_cvt_pk_bf16_f32 v111, v100, v103
	v_lshlrev_b32_e32 v114, 16, v88
	v_and_b32_e32 v101, 0xffff0000, v108
	v_lshlrev_b32_e32 v95, 16, v108
	v_sub_f32_e32 v92, v92, v101
	v_sub_f32_e32 v95, v104, v95
	v_cvt_pk_bf16_f32 v104, v95, v92
	v_lshlrev_b32_e32 v92, 16, v109
	v_sub_f32_e32 v92, v105, v92
	v_and_b32_e32 v95, 0xffff0000, v109
	v_sub_f32_e32 v95, v107, v95
	v_cvt_pk_bf16_f32 v105, v92, v95
	v_lshlrev_b32_e32 v92, 16, v110
	v_sub_f32_e32 v92, v93, v92
	v_and_b32_e32 v93, 0xffff0000, v110
	v_sub_f32_e32 v93, v94, v93
	v_cvt_pk_bf16_f32 v106, v92, v93
	v_lshlrev_b32_e32 v92, 16, v111
	v_and_b32_e32 v93, 0xffff0000, v111
	v_sub_f32_e32 v92, v100, v92
	v_sub_f32_e32 v93, v103, v93
	v_cvt_pk_bf16_f32 v107, v92, v93
	ds_read_b128 v[92:95], v153 offset:1536
	v_and_b32_e32 v88, 0xffff0000, v88
	s_waitcnt lgkmcnt(0)
	v_mfma_f32_16x16x32_bf16 v[96:99], v[108:111], v[92:95], v[96:99]
	v_mul_f32_e32 v88, v112, v88
	v_mul_f32_e32 v114, v112, v114
	v_mfma_f32_16x16x32_bf16 v[92:95], v[104:107], v[92:95], v[96:99]
	s_nop 4
	ds_read_b128 v[96:99], v153 offset:34560
	s_waitcnt lgkmcnt(0)
	v_mfma_f32_16x16x32_bf16 v[92:95], v[108:111], v[96:99], v[92:95]
	ds_read_b128 v[100:103], v162 offset:5248
	ds_read_b128 v[104:107], v162 offset:1152
	ds_read_b128 v[96:99], v162 offset:5264
	ds_read_b128 v[108:111], v162 offset:1168
	s_waitcnt lgkmcnt(2)
	v_fma_f32 v88, v88, v105, v101
	v_lshlrev_b32_e32 v101, 16, v89
	v_and_b32_e32 v89, 0xffff0000, v89
	v_mul_f32_e32 v89, v112, v89
	v_fmac_f32_e32 v103, v89, v107
	v_lshlrev_b32_e32 v89, 16, v90
	v_mul_f32_e32 v89, v112, v89
	s_waitcnt lgkmcnt(0)
	v_fma_f32 v89, v89, v108, v96
	v_and_b32_e32 v90, 0xffff0000, v90
	v_lshlrev_b32_e32 v96, 16, v91
	v_and_b32_e32 v91, 0xffff0000, v91
	v_mul_f32_e32 v101, v112, v101
	v_mul_f32_e32 v90, v112, v90
	v_mul_f32_e32 v96, v112, v96
	v_mul_f32_e32 v91, v112, v91
	v_fma_f32 v100, v114, v104, v100
	v_fma_f32 v101, v101, v106, v102
	v_fma_f32 v90, v90, v109, v97
	v_fma_f32 v96, v96, v110, v98
	v_fmac_f32_e32 v99, v91, v111
	s_and_saveexec_b64 s[0:1], s[42:43]
	v_mul_f32_e32 v91, 0x41800000, v100
	v_mul_f32_e32 v97, 0x41800000, v88
	v_med3_f32 v91, v91, s25, v218
	v_med3_f32 v97, v97, s25, v218
	v_cvt_pk_fp8_f32 v104, v91, v97
	v_mul_f32_e32 v98, 0x41800000, v101
	v_mul_f32_e32 v91, 0x41800000, v103
	v_med3_f32 v97, v98, s25, v218
	v_med3_f32 v91, v91, s25, v218
	v_cvt_pk_fp8_f32 v104, v97, v91 op_sel:[0,0,1]
	v_mul_f32_e32 v91, 0x41800000, v89
	v_mul_f32_e32 v97, 0x41800000, v90
	v_med3_f32 v91, v91, s25, v218
	v_med3_f32 v97, v97, s25, v218
	v_cvt_pk_fp8_f32 v105, v91, v97
	v_mul_f32_e32 v98, 0x41800000, v96
	v_mul_f32_e32 v91, 0x41800000, v99
	v_med3_f32 v97, v98, s25, v218
	v_med3_f32 v91, v91, s25, v218
	v_cvt_pk_fp8_f32 v105, v97, v91 op_sel:[0,0,1]
	global_store_dwordx2 v[144:145], v[104:105], off offset:288
.LBB0_1250:
	s_or_b64 exec, exec, s[0:1]
	v_cvt_pk_bf16_f32 v104, v100, v88
	v_cvt_pk_bf16_f32 v105, v101, v103
	v_cvt_pk_bf16_f32 v106, v89, v90
	v_cvt_pk_bf16_f32 v107, v96, v99
	s_nop 0
	v_and_b32_e32 v97, 0xffff0000, v104
	v_lshlrev_b32_e32 v91, 16, v104
	v_sub_f32_e32 v88, v88, v97
	v_sub_f32_e32 v91, v100, v91
	v_cvt_pk_bf16_f32 v100, v91, v88
	v_lshlrev_b32_e32 v88, 16, v105
	v_sub_f32_e32 v88, v101, v88
	v_and_b32_e32 v91, 0xffff0000, v105
	v_sub_f32_e32 v91, v103, v91
	v_cvt_pk_bf16_f32 v101, v88, v91
	v_lshlrev_b32_e32 v88, 16, v106
	v_sub_f32_e32 v88, v89, v88
	v_and_b32_e32 v89, 0xffff0000, v106
	v_sub_f32_e32 v89, v90, v89
	v_cvt_pk_bf16_f32 v102, v88, v89
	v_lshlrev_b32_e32 v88, 16, v107
	v_and_b32_e32 v89, 0xffff0000, v107
	v_sub_f32_e32 v88, v96, v88
	v_sub_f32_e32 v89, v99, v89
	v_cvt_pk_bf16_f32 v103, v88, v89
	ds_read_b128 v[88:91], v153 offset:1600
	s_waitcnt lgkmcnt(0)
	v_mfma_f32_16x16x32_bf16 v[92:95], v[104:107], v[88:91], v[92:95]
	v_mfma_f32_16x16x32_bf16 v[88:91], v[100:103], v[88:91], v[92:95]
	s_nop 6
	ds_read_b128 v[92:95], v153 offset:34624
	s_waitcnt lgkmcnt(0)
	v_mfma_f32_16x16x32_bf16 v[88:91], v[104:107], v[92:95], v[88:91]
	ds_read_b128 v[96:99], v162 offset:5376
	ds_read_b128 v[100:103], v162 offset:1280
	ds_read_b128 v[104:107], v162 offset:1296
	ds_read_b128 v[92:95], v162 offset:5392
	v_lshlrev_b32_e32 v108, 16, v84
	v_and_b32_e32 v84, 0xffff0000, v84
	v_mul_f32_e32 v84, v112, v84
	s_waitcnt lgkmcnt(2)
	v_fma_f32 v84, v84, v101, v97
	v_lshlrev_b32_e32 v97, 16, v85
	v_and_b32_e32 v85, 0xffff0000, v85
	v_mul_f32_e32 v85, v112, v85
	v_fmac_f32_e32 v99, v85, v103
	v_lshlrev_b32_e32 v85, 16, v86
	v_mul_f32_e32 v85, v112, v85
	s_waitcnt lgkmcnt(0)
	v_fma_f32 v85, v85, v104, v92
	v_and_b32_e32 v86, 0xffff0000, v86
	v_lshlrev_b32_e32 v92, 16, v87
	v_and_b32_e32 v87, 0xffff0000, v87
	v_mul_f32_e32 v108, v112, v108
	v_mul_f32_e32 v97, v112, v97
	v_mul_f32_e32 v86, v112, v86
	v_mul_f32_e32 v92, v112, v92
	v_mul_f32_e32 v87, v112, v87
	v_fma_f32 v96, v108, v100, v96
	v_fma_f32 v97, v97, v102, v98
	v_fma_f32 v86, v86, v105, v93
	v_fma_f32 v92, v92, v106, v94
	v_fmac_f32_e32 v95, v87, v107
	s_and_saveexec_b64 s[0:1], s[42:43]
	v_mul_f32_e32 v87, 0x41800000, v96
	v_mul_f32_e32 v93, 0x41800000, v84
	v_med3_f32 v87, v87, s25, v218
	v_med3_f32 v93, v93, s25, v218
	v_cvt_pk_fp8_f32 v100, v87, v93
	v_mul_f32_e32 v94, 0x41800000, v97
	v_mul_f32_e32 v87, 0x41800000, v99
	v_med3_f32 v93, v94, s25, v218
	v_med3_f32 v87, v87, s25, v218
	v_cvt_pk_fp8_f32 v100, v93, v87 op_sel:[0,0,1]
	v_mul_f32_e32 v87, 0x41800000, v85
	v_mul_f32_e32 v93, 0x41800000, v86
	v_med3_f32 v87, v87, s25, v218
	v_med3_f32 v93, v93, s25, v218
	v_cvt_pk_fp8_f32 v101, v87, v93
	v_mul_f32_e32 v94, 0x41800000, v92
	v_mul_f32_e32 v87, 0x41800000, v95
	v_med3_f32 v93, v94, s25, v218
	v_med3_f32 v87, v87, s25, v218
	v_cvt_pk_fp8_f32 v101, v93, v87 op_sel:[0,0,1]
	global_store_dwordx2 v[144:145], v[100:101], off offset:320
.LBB0_1252:
	s_or_b64 exec, exec, s[0:1]
	v_cvt_pk_bf16_f32 v100, v96, v84
	v_cvt_pk_bf16_f32 v101, v97, v99
	v_cvt_pk_bf16_f32 v102, v85, v86
	v_cvt_pk_bf16_f32 v103, v92, v95
	v_lshlrev_b32_e32 v104, 16, v80
	v_and_b32_e32 v93, 0xffff0000, v100
	v_lshlrev_b32_e32 v87, 16, v100
	v_sub_f32_e32 v84, v84, v93
	v_sub_f32_e32 v87, v96, v87
	v_cvt_pk_bf16_f32 v96, v87, v84
	v_lshlrev_b32_e32 v84, 16, v101
	v_sub_f32_e32 v84, v97, v84
	v_and_b32_e32 v87, 0xffff0000, v101
	v_sub_f32_e32 v87, v99, v87
	v_cvt_pk_bf16_f32 v97, v84, v87
	v_lshlrev_b32_e32 v84, 16, v102
	v_sub_f32_e32 v84, v85, v84
	v_and_b32_e32 v85, 0xffff0000, v102
	v_sub_f32_e32 v85, v86, v85
	v_cvt_pk_bf16_f32 v98, v84, v85
	v_lshlrev_b32_e32 v84, 16, v103
	v_and_b32_e32 v85, 0xffff0000, v103
	v_sub_f32_e32 v84, v92, v84
	v_sub_f32_e32 v85, v95, v85
	v_cvt_pk_bf16_f32 v99, v84, v85
	ds_read_b128 v[84:87], v153 offset:1664
	v_and_b32_e32 v80, 0xffff0000, v80
	s_waitcnt lgkmcnt(0)
	v_mfma_f32_16x16x32_bf16 v[88:91], v[100:103], v[84:87], v[88:91]
	v_mul_f32_e32 v80, v112, v80
	v_mul_f32_e32 v104, v112, v104
	v_mfma_f32_16x16x32_bf16 v[84:87], v[96:99], v[84:87], v[88:91]
	s_nop 4
	ds_read_b128 v[88:91], v153 offset:34688
	s_waitcnt lgkmcnt(0)
	v_mfma_f32_16x16x32_bf16 v[84:87], v[100:103], v[88:91], v[84:87]
	ds_read_b128 v[92:95], v162 offset:5504
	ds_read_b128 v[96:99], v162 offset:1408
	ds_read_b128 v[88:91], v162 offset:5520
	ds_read_b128 v[100:103], v162 offset:1424
	s_waitcnt lgkmcnt(2)
	v_fma_f32 v80, v80, v97, v93
	v_lshlrev_b32_e32 v93, 16, v81
	v_and_b32_e32 v81, 0xffff0000, v81
	v_mul_f32_e32 v81, v112, v81
	v_fmac_f32_e32 v95, v81, v99
	v_lshlrev_b32_e32 v81, 16, v82
	v_mul_f32_e32 v81, v112, v81
	s_waitcnt lgkmcnt(0)
	v_fma_f32 v81, v81, v100, v88
	v_and_b32_e32 v82, 0xffff0000, v82
	v_lshlrev_b32_e32 v88, 16, v83
	v_and_b32_e32 v83, 0xffff0000, v83
	v_mul_f32_e32 v93, v112, v93
	v_mul_f32_e32 v82, v112, v82
	v_mul_f32_e32 v88, v112, v88
	v_mul_f32_e32 v83, v112, v83
	v_fma_f32 v92, v104, v96, v92
	v_fma_f32 v93, v93, v98, v94
	v_fma_f32 v82, v82, v101, v89
	v_fma_f32 v88, v88, v102, v90
	v_fmac_f32_e32 v91, v83, v103
	s_and_saveexec_b64 s[0:1], s[42:43]
	v_mul_f32_e32 v83, 0x41800000, v92
	v_mul_f32_e32 v89, 0x41800000, v80
	v_med3_f32 v83, v83, s25, v218
	v_med3_f32 v89, v89, s25, v218
	v_cvt_pk_fp8_f32 v96, v83, v89
	v_mul_f32_e32 v90, 0x41800000, v93
	v_mul_f32_e32 v83, 0x41800000, v95
	v_med3_f32 v89, v90, s25, v218
	v_med3_f32 v83, v83, s25, v218
	v_cvt_pk_fp8_f32 v96, v89, v83 op_sel:[0,0,1]
	v_mul_f32_e32 v83, 0x41800000, v81
	v_mul_f32_e32 v89, 0x41800000, v82
	v_med3_f32 v83, v83, s25, v218
	v_med3_f32 v89, v89, s25, v218
	v_cvt_pk_fp8_f32 v97, v83, v89
	v_mul_f32_e32 v90, 0x41800000, v88
	v_mul_f32_e32 v83, 0x41800000, v91
	v_med3_f32 v89, v90, s25, v218
	v_med3_f32 v83, v83, s25, v218
	v_cvt_pk_fp8_f32 v97, v89, v83 op_sel:[0,0,1]
	global_store_dwordx2 v[144:145], v[96:97], off offset:352
.LBB0_1254:
	s_or_b64 exec, exec, s[0:1]
	v_cvt_pk_bf16_f32 v96, v92, v80
	v_cvt_pk_bf16_f32 v97, v93, v95
	v_cvt_pk_bf16_f32 v98, v81, v82
	v_cvt_pk_bf16_f32 v99, v88, v91
	s_nop 0
	v_and_b32_e32 v89, 0xffff0000, v96
	v_lshlrev_b32_e32 v83, 16, v96
	v_sub_f32_e32 v80, v80, v89
	v_sub_f32_e32 v83, v92, v83
	v_cvt_pk_bf16_f32 v92, v83, v80
	v_lshlrev_b32_e32 v80, 16, v97
	v_sub_f32_e32 v80, v93, v80
	v_and_b32_e32 v83, 0xffff0000, v97
	v_sub_f32_e32 v83, v95, v83
	v_cvt_pk_bf16_f32 v93, v80, v83
	v_lshlrev_b32_e32 v80, 16, v98
	v_sub_f32_e32 v80, v81, v80
	v_and_b32_e32 v81, 0xffff0000, v98
	v_sub_f32_e32 v81, v82, v81
	v_cvt_pk_bf16_f32 v94, v80, v81
	v_lshlrev_b32_e32 v80, 16, v99
	v_and_b32_e32 v81, 0xffff0000, v99
	v_sub_f32_e32 v80, v88, v80
	v_sub_f32_e32 v81, v91, v81
	v_cvt_pk_bf16_f32 v95, v80, v81
	ds_read_b128 v[80:83], v153 offset:1728
	s_waitcnt lgkmcnt(0)
	v_mfma_f32_16x16x32_bf16 v[84:87], v[96:99], v[80:83], v[84:87]
	v_mfma_f32_16x16x32_bf16 v[80:83], v[92:95], v[80:83], v[84:87]
	s_nop 6
	ds_read_b128 v[84:87], v153 offset:34752
	s_waitcnt lgkmcnt(0)
	v_mfma_f32_16x16x32_bf16 v[80:83], v[96:99], v[84:87], v[80:83]
	ds_read_b128 v[88:91], v162 offset:5632
	ds_read_b128 v[92:95], v162 offset:1536
	ds_read_b128 v[96:99], v162 offset:1552
	ds_read_b128 v[84:87], v162 offset:5648
	v_lshlrev_b32_e32 v100, 16, v76
	v_and_b32_e32 v76, 0xffff0000, v76
	v_mul_f32_e32 v76, v112, v76
	s_waitcnt lgkmcnt(2)
	v_fma_f32 v76, v76, v93, v89
	v_lshlrev_b32_e32 v89, 16, v77
	v_and_b32_e32 v77, 0xffff0000, v77
	v_mul_f32_e32 v77, v112, v77
	v_fmac_f32_e32 v91, v77, v95
	v_lshlrev_b32_e32 v77, 16, v78
	v_mul_f32_e32 v77, v112, v77
	s_waitcnt lgkmcnt(0)
	v_fma_f32 v77, v77, v96, v84
	v_and_b32_e32 v78, 0xffff0000, v78
	v_lshlrev_b32_e32 v84, 16, v79
	v_and_b32_e32 v79, 0xffff0000, v79
	v_mul_f32_e32 v100, v112, v100
	v_mul_f32_e32 v89, v112, v89
	v_mul_f32_e32 v78, v112, v78
	v_mul_f32_e32 v84, v112, v84
	v_mul_f32_e32 v79, v112, v79
	v_fma_f32 v88, v100, v92, v88
	v_fma_f32 v89, v89, v94, v90
	v_fma_f32 v78, v78, v97, v85
	v_fma_f32 v84, v84, v98, v86
	v_fmac_f32_e32 v87, v79, v99
	s_and_saveexec_b64 s[0:1], s[42:43]
	v_mul_f32_e32 v79, 0x41800000, v88
	v_mul_f32_e32 v85, 0x41800000, v76
	v_med3_f32 v79, v79, s25, v218
	v_med3_f32 v85, v85, s25, v218
	v_cvt_pk_fp8_f32 v92, v79, v85
	v_mul_f32_e32 v86, 0x41800000, v89
	v_mul_f32_e32 v79, 0x41800000, v91
	v_med3_f32 v85, v86, s25, v218
	v_med3_f32 v79, v79, s25, v218
	v_cvt_pk_fp8_f32 v92, v85, v79 op_sel:[0,0,1]
	v_mul_f32_e32 v79, 0x41800000, v77
	v_mul_f32_e32 v85, 0x41800000, v78
	v_med3_f32 v79, v79, s25, v218
	v_med3_f32 v85, v85, s25, v218
	v_cvt_pk_fp8_f32 v93, v79, v85
	v_mul_f32_e32 v86, 0x41800000, v84
	v_mul_f32_e32 v79, 0x41800000, v87
	v_med3_f32 v85, v86, s25, v218
	v_med3_f32 v79, v79, s25, v218
	v_cvt_pk_fp8_f32 v93, v85, v79 op_sel:[0,0,1]
	global_store_dwordx2 v[144:145], v[92:93], off offset:384
.LBB0_1256:
	s_or_b64 exec, exec, s[0:1]
	v_cvt_pk_bf16_f32 v92, v88, v76
	v_cvt_pk_bf16_f32 v93, v89, v91
	v_cvt_pk_bf16_f32 v94, v77, v78
	v_cvt_pk_bf16_f32 v95, v84, v87
	v_lshlrev_b32_e32 v96, 16, v72
	v_and_b32_e32 v85, 0xffff0000, v92
	v_lshlrev_b32_e32 v79, 16, v92
	v_sub_f32_e32 v76, v76, v85
	v_sub_f32_e32 v79, v88, v79
	v_cvt_pk_bf16_f32 v88, v79, v76
	v_lshlrev_b32_e32 v76, 16, v93
	v_sub_f32_e32 v76, v89, v76
	v_and_b32_e32 v79, 0xffff0000, v93
	v_sub_f32_e32 v79, v91, v79
	v_cvt_pk_bf16_f32 v89, v76, v79
	v_lshlrev_b32_e32 v76, 16, v94
	v_sub_f32_e32 v76, v77, v76
	v_and_b32_e32 v77, 0xffff0000, v94
	v_sub_f32_e32 v77, v78, v77
	v_cvt_pk_bf16_f32 v90, v76, v77
	v_lshlrev_b32_e32 v76, 16, v95
	v_and_b32_e32 v77, 0xffff0000, v95
	v_sub_f32_e32 v76, v84, v76
	v_sub_f32_e32 v77, v87, v77
	v_cvt_pk_bf16_f32 v91, v76, v77
	ds_read_b128 v[76:79], v153 offset:1792
	v_and_b32_e32 v72, 0xffff0000, v72
	s_waitcnt lgkmcnt(0)
	v_mfma_f32_16x16x32_bf16 v[80:83], v[92:95], v[76:79], v[80:83]
	v_mul_f32_e32 v72, v112, v72
	v_mul_f32_e32 v96, v112, v96
	v_mfma_f32_16x16x32_bf16 v[76:79], v[88:91], v[76:79], v[80:83]
	s_nop 4
	ds_read_b128 v[80:83], v153 offset:34816
	s_waitcnt lgkmcnt(0)
	v_mfma_f32_16x16x32_bf16 v[76:79], v[92:95], v[80:83], v[76:79]
	ds_read_b128 v[84:87], v162 offset:5760
	ds_read_b128 v[88:91], v162 offset:1664
	ds_read_b128 v[80:83], v162 offset:5776
	ds_read_b128 v[92:95], v162 offset:1680
	s_waitcnt lgkmcnt(2)
	v_fma_f32 v72, v72, v89, v85
	v_lshlrev_b32_e32 v85, 16, v73
	v_and_b32_e32 v73, 0xffff0000, v73
	v_mul_f32_e32 v73, v112, v73
	v_fmac_f32_e32 v87, v73, v91
	v_lshlrev_b32_e32 v73, 16, v74
	v_mul_f32_e32 v73, v112, v73
	s_waitcnt lgkmcnt(0)
	v_fma_f32 v73, v73, v92, v80
	v_and_b32_e32 v74, 0xffff0000, v74
	v_lshlrev_b32_e32 v80, 16, v75
	v_and_b32_e32 v75, 0xffff0000, v75
	v_mul_f32_e32 v85, v112, v85
	v_mul_f32_e32 v74, v112, v74
	v_mul_f32_e32 v80, v112, v80
	v_mul_f32_e32 v75, v112, v75
	v_fma_f32 v84, v96, v88, v84
	v_fma_f32 v85, v85, v90, v86
	v_fma_f32 v74, v74, v93, v81
	v_fma_f32 v80, v80, v94, v82
	v_fmac_f32_e32 v83, v75, v95
	s_and_saveexec_b64 s[0:1], s[42:43]
	v_mul_f32_e32 v75, 0x41800000, v84
	v_mul_f32_e32 v81, 0x41800000, v72
	v_med3_f32 v75, v75, s25, v218
	v_med3_f32 v81, v81, s25, v218
	v_cvt_pk_fp8_f32 v88, v75, v81
	v_mul_f32_e32 v82, 0x41800000, v85
	v_mul_f32_e32 v75, 0x41800000, v87
	v_med3_f32 v81, v82, s25, v218
	v_med3_f32 v75, v75, s25, v218
	v_cvt_pk_fp8_f32 v88, v81, v75 op_sel:[0,0,1]
	v_mul_f32_e32 v75, 0x41800000, v73
	v_mul_f32_e32 v81, 0x41800000, v74
	v_med3_f32 v75, v75, s25, v218
	v_med3_f32 v81, v81, s25, v218
	v_cvt_pk_fp8_f32 v89, v75, v81
	v_mul_f32_e32 v82, 0x41800000, v80
	v_mul_f32_e32 v75, 0x41800000, v83
	v_med3_f32 v81, v82, s25, v218
	v_med3_f32 v75, v75, s25, v218
	v_cvt_pk_fp8_f32 v89, v81, v75 op_sel:[0,0,1]
	global_store_dwordx2 v[144:145], v[88:89], off offset:416
.LBB0_1258:
	s_or_b64 exec, exec, s[0:1]
	v_cvt_pk_bf16_f32 v88, v84, v72
	v_cvt_pk_bf16_f32 v89, v85, v87
	v_cvt_pk_bf16_f32 v90, v73, v74
	v_cvt_pk_bf16_f32 v91, v80, v83
	s_nop 0
	v_and_b32_e32 v81, 0xffff0000, v88
	v_lshlrev_b32_e32 v75, 16, v88
	v_sub_f32_e32 v72, v72, v81
	v_sub_f32_e32 v75, v84, v75
	v_cvt_pk_bf16_f32 v84, v75, v72
	v_lshlrev_b32_e32 v72, 16, v89
	v_sub_f32_e32 v72, v85, v72
	v_and_b32_e32 v75, 0xffff0000, v89
	v_sub_f32_e32 v75, v87, v75
	v_cvt_pk_bf16_f32 v85, v72, v75
	v_lshlrev_b32_e32 v72, 16, v90
	v_sub_f32_e32 v72, v73, v72
	v_and_b32_e32 v73, 0xffff0000, v90
	v_sub_f32_e32 v73, v74, v73
	v_cvt_pk_bf16_f32 v86, v72, v73
	v_lshlrev_b32_e32 v72, 16, v91
	v_and_b32_e32 v73, 0xffff0000, v91
	v_sub_f32_e32 v72, v80, v72
	v_sub_f32_e32 v73, v83, v73
	v_cvt_pk_bf16_f32 v87, v72, v73
	ds_read_b128 v[72:75], v153 offset:1856
	s_waitcnt lgkmcnt(0)
	v_mfma_f32_16x16x32_bf16 v[76:79], v[88:91], v[72:75], v[76:79]
	v_mfma_f32_16x16x32_bf16 v[72:75], v[84:87], v[72:75], v[76:79]
	s_nop 6
	ds_read_b128 v[76:79], v153 offset:34880
	s_waitcnt lgkmcnt(0)
	v_mfma_f32_16x16x32_bf16 v[72:75], v[88:91], v[76:79], v[72:75]
	ds_read_b128 v[80:83], v162 offset:5888
	ds_read_b128 v[84:87], v162 offset:1792
	ds_read_b128 v[88:91], v162 offset:1808
	ds_read_b128 v[76:79], v162 offset:5904
	v_lshlrev_b32_e32 v92, 16, v68
	v_and_b32_e32 v68, 0xffff0000, v68
	v_mul_f32_e32 v68, v112, v68
	s_waitcnt lgkmcnt(2)
	v_fma_f32 v68, v68, v85, v81
	v_lshlrev_b32_e32 v81, 16, v69
	v_and_b32_e32 v69, 0xffff0000, v69
	v_mul_f32_e32 v69, v112, v69
	v_fmac_f32_e32 v83, v69, v87
	v_lshlrev_b32_e32 v69, 16, v70
	v_mul_f32_e32 v69, v112, v69
	s_waitcnt lgkmcnt(0)
	v_fma_f32 v69, v69, v88, v76
	v_and_b32_e32 v70, 0xffff0000, v70
	v_lshlrev_b32_e32 v76, 16, v71
	v_and_b32_e32 v71, 0xffff0000, v71
	v_mul_f32_e32 v92, v112, v92
	v_mul_f32_e32 v81, v112, v81
	v_mul_f32_e32 v70, v112, v70
	v_mul_f32_e32 v76, v112, v76
	v_mul_f32_e32 v71, v112, v71
	v_fma_f32 v80, v92, v84, v80
	v_fma_f32 v81, v81, v86, v82
	v_fma_f32 v70, v70, v89, v77
	v_fma_f32 v76, v76, v90, v78
	v_fmac_f32_e32 v79, v71, v91
	s_and_saveexec_b64 s[0:1], s[42:43]
	v_mul_f32_e32 v71, 0x41800000, v80
	v_mul_f32_e32 v77, 0x41800000, v68
	v_med3_f32 v71, v71, s25, v218
	v_med3_f32 v77, v77, s25, v218
	v_cvt_pk_fp8_f32 v84, v71, v77
	v_mul_f32_e32 v78, 0x41800000, v81
	v_mul_f32_e32 v71, 0x41800000, v83
	v_med3_f32 v77, v78, s25, v218
	v_med3_f32 v71, v71, s25, v218
	v_cvt_pk_fp8_f32 v84, v77, v71 op_sel:[0,0,1]
	v_mul_f32_e32 v71, 0x41800000, v69
	v_mul_f32_e32 v77, 0x41800000, v70
	v_med3_f32 v71, v71, s25, v218
	v_med3_f32 v77, v77, s25, v218
	v_cvt_pk_fp8_f32 v85, v71, v77
	v_mul_f32_e32 v78, 0x41800000, v76
	v_mul_f32_e32 v71, 0x41800000, v79
	v_med3_f32 v77, v78, s25, v218
	v_med3_f32 v71, v71, s25, v218
	v_cvt_pk_fp8_f32 v85, v77, v71 op_sel:[0,0,1]
	global_store_dwordx2 v[144:145], v[84:85], off offset:448
.LBB0_1260:
	s_or_b64 exec, exec, s[0:1]
	v_cvt_pk_bf16_f32 v84, v80, v68
	v_cvt_pk_bf16_f32 v85, v81, v83
	v_cvt_pk_bf16_f32 v86, v69, v70
	v_cvt_pk_bf16_f32 v87, v76, v79
	v_lshlrev_b32_e32 v88, 16, v64
	v_and_b32_e32 v77, 0xffff0000, v84
	v_lshlrev_b32_e32 v71, 16, v84
	v_sub_f32_e32 v68, v68, v77
	v_sub_f32_e32 v71, v80, v71
	v_cvt_pk_bf16_f32 v80, v71, v68
	v_lshlrev_b32_e32 v68, 16, v85
	v_sub_f32_e32 v68, v81, v68
	v_and_b32_e32 v71, 0xffff0000, v85
	v_sub_f32_e32 v71, v83, v71
	v_cvt_pk_bf16_f32 v81, v68, v71
	v_lshlrev_b32_e32 v68, 16, v86
	v_sub_f32_e32 v68, v69, v68
	v_and_b32_e32 v69, 0xffff0000, v86
	v_sub_f32_e32 v69, v70, v69
	v_cvt_pk_bf16_f32 v82, v68, v69
	v_lshlrev_b32_e32 v68, 16, v87
	v_and_b32_e32 v69, 0xffff0000, v87
	v_sub_f32_e32 v68, v76, v68
	v_sub_f32_e32 v69, v79, v69
	v_cvt_pk_bf16_f32 v83, v68, v69
	ds_read_b128 v[68:71], v153 offset:1920
	v_and_b32_e32 v64, 0xffff0000, v64
	s_waitcnt lgkmcnt(0)
	v_mfma_f32_16x16x32_bf16 v[72:75], v[84:87], v[68:71], v[72:75]
	v_mul_f32_e32 v64, v112, v64
	v_mul_f32_e32 v88, v112, v88
	v_mfma_f32_16x16x32_bf16 v[68:71], v[80:83], v[68:71], v[72:75]
	s_nop 4
	ds_read_b128 v[72:75], v153 offset:34944
	s_waitcnt lgkmcnt(0)
	v_mfma_f32_16x16x32_bf16 v[68:71], v[84:87], v[72:75], v[68:71]
	ds_read_b128 v[76:79], v162 offset:6016
	ds_read_b128 v[80:83], v162 offset:1920
	ds_read_b128 v[72:75], v162 offset:6032
	ds_read_b128 v[84:87], v162 offset:1936
	s_waitcnt lgkmcnt(2)
	v_fma_f32 v64, v64, v81, v77
	v_lshlrev_b32_e32 v77, 16, v65
	v_and_b32_e32 v65, 0xffff0000, v65
	v_mul_f32_e32 v65, v112, v65
	v_fmac_f32_e32 v79, v65, v83
	v_lshlrev_b32_e32 v65, 16, v66
	v_mul_f32_e32 v65, v112, v65
	s_waitcnt lgkmcnt(0)
	v_fma_f32 v65, v65, v84, v72
	v_and_b32_e32 v66, 0xffff0000, v66
	v_lshlrev_b32_e32 v72, 16, v67
	v_and_b32_e32 v67, 0xffff0000, v67
	v_mul_f32_e32 v77, v112, v77
	v_mul_f32_e32 v66, v112, v66
	v_mul_f32_e32 v72, v112, v72
	v_mul_f32_e32 v67, v112, v67
	v_fma_f32 v76, v88, v80, v76
	v_fma_f32 v77, v77, v82, v78
	v_fma_f32 v66, v66, v85, v73
	v_fma_f32 v72, v72, v86, v74
	v_fmac_f32_e32 v75, v67, v87
	s_and_saveexec_b64 s[0:1], s[42:43]
	v_mul_f32_e32 v67, 0x41800000, v76
	v_mul_f32_e32 v73, 0x41800000, v64
	v_med3_f32 v67, v67, s25, v218
	v_med3_f32 v73, v73, s25, v218
	v_cvt_pk_fp8_f32 v80, v67, v73
	v_mul_f32_e32 v74, 0x41800000, v77
	v_mul_f32_e32 v67, 0x41800000, v79
	v_med3_f32 v73, v74, s25, v218
	v_med3_f32 v67, v67, s25, v218
	v_cvt_pk_fp8_f32 v80, v73, v67 op_sel:[0,0,1]
	v_mul_f32_e32 v67, 0x41800000, v65
	v_mul_f32_e32 v73, 0x41800000, v66
	v_med3_f32 v67, v67, s25, v218
	v_med3_f32 v73, v73, s25, v218
	v_cvt_pk_fp8_f32 v81, v67, v73
	v_mul_f32_e32 v74, 0x41800000, v72
	v_mul_f32_e32 v67, 0x41800000, v75
	v_med3_f32 v73, v74, s25, v218
	v_med3_f32 v67, v67, s25, v218
	v_cvt_pk_fp8_f32 v81, v73, v67 op_sel:[0,0,1]
	global_store_dwordx2 v[144:145], v[80:81], off offset:480
.LBB0_1262:
	s_or_b64 exec, exec, s[0:1]
	v_cvt_pk_bf16_f32 v80, v76, v64
	v_cvt_pk_bf16_f32 v81, v77, v79
	v_cvt_pk_bf16_f32 v82, v65, v66
	v_cvt_pk_bf16_f32 v83, v72, v75
	s_nop 0
	v_and_b32_e32 v73, 0xffff0000, v80
	v_lshlrev_b32_e32 v67, 16, v80
	v_sub_f32_e32 v64, v64, v73
	v_sub_f32_e32 v67, v76, v67
	v_cvt_pk_bf16_f32 v76, v67, v64
	v_lshlrev_b32_e32 v64, 16, v81
	v_sub_f32_e32 v64, v77, v64
	v_and_b32_e32 v67, 0xffff0000, v81
	v_sub_f32_e32 v67, v79, v67
	v_cvt_pk_bf16_f32 v77, v64, v67
	v_lshlrev_b32_e32 v64, 16, v82
	v_sub_f32_e32 v64, v65, v64
	v_and_b32_e32 v65, 0xffff0000, v82
	v_sub_f32_e32 v65, v66, v65
	v_cvt_pk_bf16_f32 v78, v64, v65
	v_lshlrev_b32_e32 v64, 16, v83
	v_and_b32_e32 v65, 0xffff0000, v83
	v_sub_f32_e32 v64, v72, v64
	v_sub_f32_e32 v65, v75, v65
	v_cvt_pk_bf16_f32 v79, v64, v65
	ds_read_b128 v[64:67], v153 offset:1984
	s_waitcnt lgkmcnt(0)
	v_mfma_f32_16x16x32_bf16 v[68:71], v[80:83], v[64:67], v[68:71]
	v_mfma_f32_16x16x32_bf16 v[64:67], v[76:79], v[64:67], v[68:71]
	s_nop 6
	ds_read_b128 v[68:71], v153 offset:35008
	s_waitcnt lgkmcnt(0)
	v_mfma_f32_16x16x32_bf16 v[64:67], v[80:83], v[68:71], v[64:67]
	ds_read_b128 v[72:75], v162 offset:6144
	ds_read_b128 v[76:79], v162 offset:2048
	ds_read_b128 v[80:83], v162 offset:2064
	ds_read_b128 v[68:71], v162 offset:6160
	v_lshlrev_b32_e32 v84, 16, v60
	v_and_b32_e32 v60, 0xffff0000, v60
	v_mul_f32_e32 v60, v112, v60
	s_waitcnt lgkmcnt(2)
	v_fma_f32 v60, v60, v77, v73
	v_lshlrev_b32_e32 v73, 16, v61
	v_and_b32_e32 v61, 0xffff0000, v61
	v_mul_f32_e32 v61, v112, v61
	v_fmac_f32_e32 v75, v61, v79
	v_lshlrev_b32_e32 v61, 16, v62
	v_mul_f32_e32 v61, v112, v61
	s_waitcnt lgkmcnt(0)
	v_fma_f32 v61, v61, v80, v68
	v_and_b32_e32 v62, 0xffff0000, v62
	v_lshlrev_b32_e32 v68, 16, v63
	v_and_b32_e32 v63, 0xffff0000, v63
	v_mul_f32_e32 v84, v112, v84
	v_mul_f32_e32 v73, v112, v73
	v_mul_f32_e32 v62, v112, v62
	v_mul_f32_e32 v68, v112, v68
	v_mul_f32_e32 v63, v112, v63
	v_fma_f32 v72, v84, v76, v72
	v_fma_f32 v73, v73, v78, v74
	v_fma_f32 v62, v62, v81, v69
	v_fma_f32 v68, v68, v82, v70
	v_fmac_f32_e32 v71, v63, v83
	s_and_saveexec_b64 s[0:1], s[42:43]
	v_mul_f32_e32 v63, 0x41800000, v72
	v_mul_f32_e32 v69, 0x41800000, v60
	v_med3_f32 v63, v63, s25, v218
	v_med3_f32 v69, v69, s25, v218
	v_cvt_pk_fp8_f32 v76, v63, v69
	v_mul_f32_e32 v70, 0x41800000, v73
	v_mul_f32_e32 v63, 0x41800000, v75
	v_med3_f32 v69, v70, s25, v218
	v_med3_f32 v63, v63, s25, v218
	v_cvt_pk_fp8_f32 v76, v69, v63 op_sel:[0,0,1]
	v_mul_f32_e32 v63, 0x41800000, v61
	v_mul_f32_e32 v69, 0x41800000, v62
	v_med3_f32 v63, v63, s25, v218
	v_med3_f32 v69, v69, s25, v218
	v_cvt_pk_fp8_f32 v77, v63, v69
	v_mul_f32_e32 v70, 0x41800000, v68
	v_mul_f32_e32 v63, 0x41800000, v71
	v_med3_f32 v69, v70, s25, v218
	v_med3_f32 v63, v63, s25, v218
	v_cvt_pk_fp8_f32 v77, v69, v63 op_sel:[0,0,1]
	global_store_dwordx2 v[144:145], v[76:77], off offset:512
.LBB0_1264:
	s_or_b64 exec, exec, s[0:1]
	v_cvt_pk_bf16_f32 v76, v72, v60
	v_cvt_pk_bf16_f32 v77, v73, v75
	v_cvt_pk_bf16_f32 v78, v61, v62
	v_cvt_pk_bf16_f32 v79, v68, v71
	v_lshlrev_b32_e32 v80, 16, v56
	v_and_b32_e32 v69, 0xffff0000, v76
	v_lshlrev_b32_e32 v63, 16, v76
	v_sub_f32_e32 v60, v60, v69
	v_sub_f32_e32 v63, v72, v63
	v_cvt_pk_bf16_f32 v72, v63, v60
	v_lshlrev_b32_e32 v60, 16, v77
	v_sub_f32_e32 v60, v73, v60
	v_and_b32_e32 v63, 0xffff0000, v77
	v_sub_f32_e32 v63, v75, v63
	v_cvt_pk_bf16_f32 v73, v60, v63
	v_lshlrev_b32_e32 v60, 16, v78
	v_sub_f32_e32 v60, v61, v60
	v_and_b32_e32 v61, 0xffff0000, v78
	v_sub_f32_e32 v61, v62, v61
	v_cvt_pk_bf16_f32 v74, v60, v61
	v_lshlrev_b32_e32 v60, 16, v79
	v_and_b32_e32 v61, 0xffff0000, v79
	v_sub_f32_e32 v60, v68, v60
	v_sub_f32_e32 v61, v71, v61
	v_cvt_pk_bf16_f32 v75, v60, v61
	ds_read_b128 v[60:63], v153 offset:2048
	v_and_b32_e32 v56, 0xffff0000, v56
	s_waitcnt lgkmcnt(0)
	v_mfma_f32_16x16x32_bf16 v[64:67], v[76:79], v[60:63], v[64:67]
	v_mul_f32_e32 v56, v112, v56
	v_mul_f32_e32 v80, v112, v80
	v_mfma_f32_16x16x32_bf16 v[60:63], v[72:75], v[60:63], v[64:67]
	s_nop 4
	ds_read_b128 v[64:67], v153 offset:35072
	s_waitcnt lgkmcnt(0)
	v_mfma_f32_16x16x32_bf16 v[60:63], v[76:79], v[64:67], v[60:63]
	ds_read_b128 v[68:71], v162 offset:6272
	ds_read_b128 v[72:75], v162 offset:2176
	ds_read_b128 v[64:67], v162 offset:6288
	ds_read_b128 v[76:79], v162 offset:2192
	s_waitcnt lgkmcnt(2)
	v_fma_f32 v56, v56, v73, v69
	v_lshlrev_b32_e32 v69, 16, v57
	v_and_b32_e32 v57, 0xffff0000, v57
	v_mul_f32_e32 v57, v112, v57
	v_fmac_f32_e32 v71, v57, v75
	v_lshlrev_b32_e32 v57, 16, v58
	v_mul_f32_e32 v57, v112, v57
	s_waitcnt lgkmcnt(0)
	v_fma_f32 v57, v57, v76, v64
	v_and_b32_e32 v58, 0xffff0000, v58
	v_lshlrev_b32_e32 v64, 16, v59
	v_and_b32_e32 v59, 0xffff0000, v59
	v_mul_f32_e32 v69, v112, v69
	v_mul_f32_e32 v58, v112, v58
	v_mul_f32_e32 v64, v112, v64
	v_mul_f32_e32 v59, v112, v59
	v_fma_f32 v68, v80, v72, v68
	v_fma_f32 v69, v69, v74, v70
	v_fma_f32 v58, v58, v77, v65
	v_fma_f32 v64, v64, v78, v66
	v_fmac_f32_e32 v67, v59, v79
	s_and_saveexec_b64 s[0:1], s[42:43]
	v_mul_f32_e32 v59, 0x41800000, v68
	v_mul_f32_e32 v65, 0x41800000, v56
	v_med3_f32 v59, v59, s25, v218
	v_med3_f32 v65, v65, s25, v218
	v_cvt_pk_fp8_f32 v72, v59, v65
	v_mul_f32_e32 v66, 0x41800000, v69
	v_mul_f32_e32 v59, 0x41800000, v71
	v_med3_f32 v65, v66, s25, v218
	v_med3_f32 v59, v59, s25, v218
	v_cvt_pk_fp8_f32 v72, v65, v59 op_sel:[0,0,1]
	v_mul_f32_e32 v59, 0x41800000, v57
	v_mul_f32_e32 v65, 0x41800000, v58
	v_med3_f32 v59, v59, s25, v218
	v_med3_f32 v65, v65, s25, v218
	v_cvt_pk_fp8_f32 v73, v59, v65
	v_mul_f32_e32 v66, 0x41800000, v64
	v_mul_f32_e32 v59, 0x41800000, v67
	v_med3_f32 v65, v66, s25, v218
	v_med3_f32 v59, v59, s25, v218
	v_cvt_pk_fp8_f32 v73, v65, v59 op_sel:[0,0,1]
	global_store_dwordx2 v[144:145], v[72:73], off offset:544
.LBB0_1266:
	s_or_b64 exec, exec, s[0:1]
	v_cvt_pk_bf16_f32 v72, v68, v56
	v_cvt_pk_bf16_f32 v73, v69, v71
	v_cvt_pk_bf16_f32 v74, v57, v58
	v_cvt_pk_bf16_f32 v75, v64, v67
	s_nop 0
	v_and_b32_e32 v65, 0xffff0000, v72
	v_lshlrev_b32_e32 v59, 16, v72
	v_sub_f32_e32 v56, v56, v65
	v_sub_f32_e32 v59, v68, v59
	v_cvt_pk_bf16_f32 v68, v59, v56
	v_lshlrev_b32_e32 v56, 16, v73
	v_sub_f32_e32 v56, v69, v56
	v_and_b32_e32 v59, 0xffff0000, v73
	v_sub_f32_e32 v59, v71, v59
	v_cvt_pk_bf16_f32 v69, v56, v59
	v_lshlrev_b32_e32 v56, 16, v74
	v_sub_f32_e32 v56, v57, v56
	v_and_b32_e32 v57, 0xffff0000, v74
	v_sub_f32_e32 v57, v58, v57
	v_cvt_pk_bf16_f32 v70, v56, v57
	v_lshlrev_b32_e32 v56, 16, v75
	v_and_b32_e32 v57, 0xffff0000, v75
	v_sub_f32_e32 v56, v64, v56
	v_sub_f32_e32 v57, v67, v57
	v_cvt_pk_bf16_f32 v71, v56, v57
	ds_read_b128 v[56:59], v153 offset:2112
	s_waitcnt lgkmcnt(0)
	v_mfma_f32_16x16x32_bf16 v[60:63], v[72:75], v[56:59], v[60:63]
	v_mfma_f32_16x16x32_bf16 v[56:59], v[68:71], v[56:59], v[60:63]
	s_nop 6
	ds_read_b128 v[60:63], v153 offset:35136
	s_waitcnt lgkmcnt(0)
	v_mfma_f32_16x16x32_bf16 v[56:59], v[72:75], v[60:63], v[56:59]
	ds_read_b128 v[64:67], v162 offset:6400
	ds_read_b128 v[68:71], v162 offset:2304
	ds_read_b128 v[72:75], v162 offset:2320
	ds_read_b128 v[60:63], v162 offset:6416
	v_lshlrev_b32_e32 v76, 16, v52
	v_and_b32_e32 v52, 0xffff0000, v52
	v_mul_f32_e32 v52, v112, v52
	s_waitcnt lgkmcnt(2)
	v_fma_f32 v52, v52, v69, v65
	v_lshlrev_b32_e32 v65, 16, v53
	v_and_b32_e32 v53, 0xffff0000, v53
	v_mul_f32_e32 v53, v112, v53
	v_fmac_f32_e32 v67, v53, v71
	v_lshlrev_b32_e32 v53, 16, v54
	v_mul_f32_e32 v53, v112, v53
	s_waitcnt lgkmcnt(0)
	v_fma_f32 v53, v53, v72, v60
	v_and_b32_e32 v54, 0xffff0000, v54
	v_lshlrev_b32_e32 v60, 16, v55
	v_and_b32_e32 v55, 0xffff0000, v55
	v_mul_f32_e32 v76, v112, v76
	v_mul_f32_e32 v65, v112, v65
	v_mul_f32_e32 v54, v112, v54
	v_mul_f32_e32 v60, v112, v60
	v_mul_f32_e32 v55, v112, v55
	v_fma_f32 v64, v76, v68, v64
	v_fma_f32 v65, v65, v70, v66
	v_fma_f32 v54, v54, v73, v61
	v_fma_f32 v60, v60, v74, v62
	v_fmac_f32_e32 v63, v55, v75
	s_and_saveexec_b64 s[0:1], s[42:43]
	v_mul_f32_e32 v55, 0x41800000, v64
	v_mul_f32_e32 v61, 0x41800000, v52
	v_med3_f32 v55, v55, s25, v218
	v_med3_f32 v61, v61, s25, v218
	v_cvt_pk_fp8_f32 v68, v55, v61
	v_mul_f32_e32 v62, 0x41800000, v65
	v_mul_f32_e32 v55, 0x41800000, v67
	v_med3_f32 v61, v62, s25, v218
	v_med3_f32 v55, v55, s25, v218
	v_cvt_pk_fp8_f32 v68, v61, v55 op_sel:[0,0,1]
	v_mul_f32_e32 v55, 0x41800000, v53
	v_mul_f32_e32 v61, 0x41800000, v54
	v_med3_f32 v55, v55, s25, v218
	v_med3_f32 v61, v61, s25, v218
	v_cvt_pk_fp8_f32 v69, v55, v61
	v_mul_f32_e32 v62, 0x41800000, v60
	v_mul_f32_e32 v55, 0x41800000, v63
	v_med3_f32 v61, v62, s25, v218
	v_med3_f32 v55, v55, s25, v218
	v_cvt_pk_fp8_f32 v69, v61, v55 op_sel:[0,0,1]
	global_store_dwordx2 v[144:145], v[68:69], off offset:576
.LBB0_1268:
	s_or_b64 exec, exec, s[0:1]
	v_cvt_pk_bf16_f32 v68, v64, v52
	v_cvt_pk_bf16_f32 v69, v65, v67
	v_cvt_pk_bf16_f32 v70, v53, v54
	v_cvt_pk_bf16_f32 v71, v60, v63
	v_lshlrev_b32_e32 v72, 16, v48
	v_and_b32_e32 v61, 0xffff0000, v68
	v_lshlrev_b32_e32 v55, 16, v68
	v_sub_f32_e32 v52, v52, v61
	v_sub_f32_e32 v55, v64, v55
	v_cvt_pk_bf16_f32 v64, v55, v52
	v_lshlrev_b32_e32 v52, 16, v69
	v_sub_f32_e32 v52, v65, v52
	v_and_b32_e32 v55, 0xffff0000, v69
	v_sub_f32_e32 v55, v67, v55
	v_cvt_pk_bf16_f32 v65, v52, v55
	v_lshlrev_b32_e32 v52, 16, v70
	v_sub_f32_e32 v52, v53, v52
	v_and_b32_e32 v53, 0xffff0000, v70
	v_sub_f32_e32 v53, v54, v53
	v_cvt_pk_bf16_f32 v66, v52, v53
	v_lshlrev_b32_e32 v52, 16, v71
	v_and_b32_e32 v53, 0xffff0000, v71
	v_sub_f32_e32 v52, v60, v52
	v_sub_f32_e32 v53, v63, v53
	v_cvt_pk_bf16_f32 v67, v52, v53
	ds_read_b128 v[52:55], v153 offset:2176
	v_and_b32_e32 v48, 0xffff0000, v48
	s_waitcnt lgkmcnt(0)
	v_mfma_f32_16x16x32_bf16 v[56:59], v[68:71], v[52:55], v[56:59]
	v_mul_f32_e32 v48, v112, v48
	v_mul_f32_e32 v72, v112, v72
	v_mfma_f32_16x16x32_bf16 v[52:55], v[64:67], v[52:55], v[56:59]
	s_nop 4
	ds_read_b128 v[56:59], v153 offset:35200
	s_waitcnt lgkmcnt(0)
	v_mfma_f32_16x16x32_bf16 v[52:55], v[68:71], v[56:59], v[52:55]
	ds_read_b128 v[60:63], v162 offset:6528
	ds_read_b128 v[64:67], v162 offset:2432
	ds_read_b128 v[56:59], v162 offset:6544
	ds_read_b128 v[68:71], v162 offset:2448
	s_waitcnt lgkmcnt(2)
	v_fma_f32 v48, v48, v65, v61
	v_lshlrev_b32_e32 v61, 16, v49
	v_and_b32_e32 v49, 0xffff0000, v49
	v_mul_f32_e32 v49, v112, v49
	v_fmac_f32_e32 v63, v49, v67
	v_lshlrev_b32_e32 v49, 16, v50
	v_mul_f32_e32 v49, v112, v49
	s_waitcnt lgkmcnt(0)
	v_fma_f32 v49, v49, v68, v56
	v_and_b32_e32 v50, 0xffff0000, v50
	v_lshlrev_b32_e32 v56, 16, v51
	v_and_b32_e32 v51, 0xffff0000, v51
	v_mul_f32_e32 v61, v112, v61
	v_mul_f32_e32 v50, v112, v50
	v_mul_f32_e32 v56, v112, v56
	v_mul_f32_e32 v51, v112, v51
	v_fma_f32 v60, v72, v64, v60
	v_fma_f32 v61, v61, v66, v62
	v_fma_f32 v50, v50, v69, v57
	v_fma_f32 v56, v56, v70, v58
	v_fmac_f32_e32 v59, v51, v71
	s_and_saveexec_b64 s[0:1], s[42:43]
	v_mul_f32_e32 v51, 0x41800000, v60
	v_mul_f32_e32 v57, 0x41800000, v48
	v_med3_f32 v51, v51, s25, v218
	v_med3_f32 v57, v57, s25, v218
	v_cvt_pk_fp8_f32 v64, v51, v57
	v_mul_f32_e32 v58, 0x41800000, v61
	v_mul_f32_e32 v51, 0x41800000, v63
	v_med3_f32 v57, v58, s25, v218
	v_med3_f32 v51, v51, s25, v218
	v_cvt_pk_fp8_f32 v64, v57, v51 op_sel:[0,0,1]
	v_mul_f32_e32 v51, 0x41800000, v49
	v_mul_f32_e32 v57, 0x41800000, v50
	v_med3_f32 v51, v51, s25, v218
	v_med3_f32 v57, v57, s25, v218
	v_cvt_pk_fp8_f32 v65, v51, v57
	v_mul_f32_e32 v58, 0x41800000, v56
	v_mul_f32_e32 v51, 0x41800000, v59
	v_med3_f32 v57, v58, s25, v218
	v_med3_f32 v51, v51, s25, v218
	v_cvt_pk_fp8_f32 v65, v57, v51 op_sel:[0,0,1]
	global_store_dwordx2 v[144:145], v[64:65], off offset:608
.LBB0_1270:
	s_or_b64 exec, exec, s[0:1]
	v_cvt_pk_bf16_f32 v64, v60, v48
	v_cvt_pk_bf16_f32 v65, v61, v63
	v_cvt_pk_bf16_f32 v66, v49, v50
	v_cvt_pk_bf16_f32 v67, v56, v59
	s_nop 0
	v_and_b32_e32 v57, 0xffff0000, v64
	v_lshlrev_b32_e32 v51, 16, v64
	v_sub_f32_e32 v48, v48, v57
	v_sub_f32_e32 v51, v60, v51
	v_cvt_pk_bf16_f32 v60, v51, v48
	v_lshlrev_b32_e32 v48, 16, v65
	v_sub_f32_e32 v48, v61, v48
	v_and_b32_e32 v51, 0xffff0000, v65
	v_sub_f32_e32 v51, v63, v51
	v_cvt_pk_bf16_f32 v61, v48, v51
	v_lshlrev_b32_e32 v48, 16, v66
	v_sub_f32_e32 v48, v49, v48
	v_and_b32_e32 v49, 0xffff0000, v66
	v_sub_f32_e32 v49, v50, v49
	v_cvt_pk_bf16_f32 v62, v48, v49
	v_lshlrev_b32_e32 v48, 16, v67
	v_and_b32_e32 v49, 0xffff0000, v67
	v_sub_f32_e32 v48, v56, v48
	v_sub_f32_e32 v49, v59, v49
	v_cvt_pk_bf16_f32 v63, v48, v49
	ds_read_b128 v[48:51], v153 offset:2240
	s_waitcnt lgkmcnt(0)
	v_mfma_f32_16x16x32_bf16 v[52:55], v[64:67], v[48:51], v[52:55]
	v_mfma_f32_16x16x32_bf16 v[48:51], v[60:63], v[48:51], v[52:55]
	s_nop 6
	ds_read_b128 v[52:55], v153 offset:35264
	s_waitcnt lgkmcnt(0)
	v_mfma_f32_16x16x32_bf16 v[48:51], v[64:67], v[52:55], v[48:51]
	ds_read_b128 v[56:59], v162 offset:6656
	ds_read_b128 v[60:63], v162 offset:2560
	ds_read_b128 v[64:67], v162 offset:2576
	ds_read_b128 v[52:55], v162 offset:6672
	v_lshlrev_b32_e32 v68, 16, v44
	v_and_b32_e32 v44, 0xffff0000, v44
	v_mul_f32_e32 v44, v112, v44
	s_waitcnt lgkmcnt(2)
	v_fma_f32 v44, v44, v61, v57
	v_lshlrev_b32_e32 v57, 16, v45
	v_and_b32_e32 v45, 0xffff0000, v45
	v_mul_f32_e32 v45, v112, v45
	v_fmac_f32_e32 v59, v45, v63
	v_lshlrev_b32_e32 v45, 16, v46
	v_mul_f32_e32 v45, v112, v45
	s_waitcnt lgkmcnt(0)
	v_fma_f32 v45, v45, v64, v52
	v_and_b32_e32 v46, 0xffff0000, v46
	v_lshlrev_b32_e32 v52, 16, v47
	v_and_b32_e32 v47, 0xffff0000, v47
	v_mul_f32_e32 v68, v112, v68
	v_mul_f32_e32 v57, v112, v57
	v_mul_f32_e32 v46, v112, v46
	v_mul_f32_e32 v52, v112, v52
	v_mul_f32_e32 v47, v112, v47
	v_fma_f32 v56, v68, v60, v56
	v_fma_f32 v57, v57, v62, v58
	v_fma_f32 v46, v46, v65, v53
	v_fma_f32 v52, v52, v66, v54
	v_fmac_f32_e32 v55, v47, v67
	s_and_saveexec_b64 s[0:1], s[42:43]
	v_mul_f32_e32 v47, 0x41800000, v56
	v_mul_f32_e32 v53, 0x41800000, v44
	v_med3_f32 v47, v47, s25, v218
	v_med3_f32 v53, v53, s25, v218
	v_cvt_pk_fp8_f32 v60, v47, v53
	v_mul_f32_e32 v54, 0x41800000, v57
	v_mul_f32_e32 v47, 0x41800000, v59
	v_med3_f32 v53, v54, s25, v218
	v_med3_f32 v47, v47, s25, v218
	v_cvt_pk_fp8_f32 v60, v53, v47 op_sel:[0,0,1]
	v_mul_f32_e32 v47, 0x41800000, v45
	v_mul_f32_e32 v53, 0x41800000, v46
	v_med3_f32 v47, v47, s25, v218
	v_med3_f32 v53, v53, s25, v218
	v_cvt_pk_fp8_f32 v61, v47, v53
	v_mul_f32_e32 v54, 0x41800000, v52
	v_mul_f32_e32 v47, 0x41800000, v55
	v_med3_f32 v53, v54, s25, v218
	v_med3_f32 v47, v47, s25, v218
	v_cvt_pk_fp8_f32 v61, v53, v47 op_sel:[0,0,1]
	global_store_dwordx2 v[144:145], v[60:61], off offset:640
.LBB0_1272:
	s_or_b64 exec, exec, s[0:1]
	v_cvt_pk_bf16_f32 v60, v56, v44
	v_cvt_pk_bf16_f32 v61, v57, v59
	v_cvt_pk_bf16_f32 v62, v45, v46
	v_cvt_pk_bf16_f32 v63, v52, v55
	v_lshlrev_b32_e32 v64, 16, v40
	v_and_b32_e32 v53, 0xffff0000, v60
	v_lshlrev_b32_e32 v47, 16, v60
	v_sub_f32_e32 v44, v44, v53
	v_sub_f32_e32 v47, v56, v47
	v_cvt_pk_bf16_f32 v56, v47, v44
	v_lshlrev_b32_e32 v44, 16, v61
	v_sub_f32_e32 v44, v57, v44
	v_and_b32_e32 v47, 0xffff0000, v61
	v_sub_f32_e32 v47, v59, v47
	v_cvt_pk_bf16_f32 v57, v44, v47
	v_lshlrev_b32_e32 v44, 16, v62
	v_sub_f32_e32 v44, v45, v44
	v_and_b32_e32 v45, 0xffff0000, v62
	v_sub_f32_e32 v45, v46, v45
	v_cvt_pk_bf16_f32 v58, v44, v45
	v_lshlrev_b32_e32 v44, 16, v63
	v_and_b32_e32 v45, 0xffff0000, v63
	v_sub_f32_e32 v44, v52, v44
	v_sub_f32_e32 v45, v55, v45
	v_cvt_pk_bf16_f32 v59, v44, v45
	ds_read_b128 v[44:47], v153 offset:2304
	v_and_b32_e32 v40, 0xffff0000, v40
	s_waitcnt lgkmcnt(0)
	v_mfma_f32_16x16x32_bf16 v[48:51], v[60:63], v[44:47], v[48:51]
	v_mul_f32_e32 v40, v112, v40
	v_mul_f32_e32 v64, v112, v64
	v_mfma_f32_16x16x32_bf16 v[44:47], v[56:59], v[44:47], v[48:51]
	s_nop 4
	ds_read_b128 v[48:51], v153 offset:35328
	s_waitcnt lgkmcnt(0)
	v_mfma_f32_16x16x32_bf16 v[44:47], v[60:63], v[48:51], v[44:47]
	ds_read_b128 v[52:55], v162 offset:6784
	ds_read_b128 v[56:59], v162 offset:2688
	ds_read_b128 v[48:51], v162 offset:6800
	ds_read_b128 v[60:63], v162 offset:2704
	s_waitcnt lgkmcnt(2)
	v_fma_f32 v40, v40, v57, v53
	v_lshlrev_b32_e32 v53, 16, v41
	v_and_b32_e32 v41, 0xffff0000, v41
	v_mul_f32_e32 v41, v112, v41
	v_fmac_f32_e32 v55, v41, v59
	v_lshlrev_b32_e32 v41, 16, v42
	v_mul_f32_e32 v41, v112, v41
	s_waitcnt lgkmcnt(0)
	v_fma_f32 v41, v41, v60, v48
	v_and_b32_e32 v42, 0xffff0000, v42
	v_lshlrev_b32_e32 v48, 16, v43
	v_and_b32_e32 v43, 0xffff0000, v43
	v_mul_f32_e32 v53, v112, v53
	v_mul_f32_e32 v42, v112, v42
	v_mul_f32_e32 v48, v112, v48
	v_mul_f32_e32 v43, v112, v43
	v_fma_f32 v52, v64, v56, v52
	v_fma_f32 v53, v53, v58, v54
	v_fma_f32 v42, v42, v61, v49
	v_fma_f32 v48, v48, v62, v50
	v_fmac_f32_e32 v51, v43, v63
	s_and_saveexec_b64 s[0:1], s[42:43]
	v_mul_f32_e32 v43, 0x41800000, v52
	v_mul_f32_e32 v49, 0x41800000, v40
	v_med3_f32 v43, v43, s25, v218
	v_med3_f32 v49, v49, s25, v218
	v_cvt_pk_fp8_f32 v56, v43, v49
	v_mul_f32_e32 v50, 0x41800000, v53
	v_mul_f32_e32 v43, 0x41800000, v55
	v_med3_f32 v49, v50, s25, v218
	v_med3_f32 v43, v43, s25, v218
	v_cvt_pk_fp8_f32 v56, v49, v43 op_sel:[0,0,1]
	v_mul_f32_e32 v43, 0x41800000, v41
	v_mul_f32_e32 v49, 0x41800000, v42
	v_med3_f32 v43, v43, s25, v218
	v_med3_f32 v49, v49, s25, v218
	v_cvt_pk_fp8_f32 v57, v43, v49
	v_mul_f32_e32 v50, 0x41800000, v48
	v_mul_f32_e32 v43, 0x41800000, v51
	v_med3_f32 v49, v50, s25, v218
	v_med3_f32 v43, v43, s25, v218
	v_cvt_pk_fp8_f32 v57, v49, v43 op_sel:[0,0,1]
	global_store_dwordx2 v[144:145], v[56:57], off offset:672
.LBB0_1274:
	s_or_b64 exec, exec, s[0:1]
	v_cvt_pk_bf16_f32 v56, v52, v40
	v_cvt_pk_bf16_f32 v57, v53, v55
	v_cvt_pk_bf16_f32 v58, v41, v42
	v_cvt_pk_bf16_f32 v59, v48, v51
	s_nop 0
	v_and_b32_e32 v49, 0xffff0000, v56
	v_lshlrev_b32_e32 v43, 16, v56
	v_sub_f32_e32 v40, v40, v49
	v_sub_f32_e32 v43, v52, v43
	v_cvt_pk_bf16_f32 v52, v43, v40
	v_lshlrev_b32_e32 v40, 16, v57
	v_sub_f32_e32 v40, v53, v40
	v_and_b32_e32 v43, 0xffff0000, v57
	v_sub_f32_e32 v43, v55, v43
	v_cvt_pk_bf16_f32 v53, v40, v43
	v_lshlrev_b32_e32 v40, 16, v58
	v_sub_f32_e32 v40, v41, v40
	v_and_b32_e32 v41, 0xffff0000, v58
	v_sub_f32_e32 v41, v42, v41
	v_cvt_pk_bf16_f32 v54, v40, v41
	v_lshlrev_b32_e32 v40, 16, v59
	v_and_b32_e32 v41, 0xffff0000, v59
	v_sub_f32_e32 v40, v48, v40
	v_sub_f32_e32 v41, v51, v41
	v_cvt_pk_bf16_f32 v55, v40, v41
	ds_read_b128 v[40:43], v153 offset:2368
	s_waitcnt lgkmcnt(0)
	v_mfma_f32_16x16x32_bf16 v[44:47], v[56:59], v[40:43], v[44:47]
	v_mfma_f32_16x16x32_bf16 v[40:43], v[52:55], v[40:43], v[44:47]
	s_nop 6
	ds_read_b128 v[44:47], v153 offset:35392
	s_waitcnt lgkmcnt(0)
	v_mfma_f32_16x16x32_bf16 v[40:43], v[56:59], v[44:47], v[40:43]
	ds_read_b128 v[48:51], v162 offset:6912
	ds_read_b128 v[52:55], v162 offset:2816
	ds_read_b128 v[56:59], v162 offset:2832
	ds_read_b128 v[44:47], v162 offset:6928
	v_lshlrev_b32_e32 v60, 16, v36
	v_and_b32_e32 v36, 0xffff0000, v36
	v_mul_f32_e32 v36, v112, v36
	s_waitcnt lgkmcnt(2)
	v_fma_f32 v36, v36, v53, v49
	v_lshlrev_b32_e32 v49, 16, v37
	v_and_b32_e32 v37, 0xffff0000, v37
	v_mul_f32_e32 v37, v112, v37
	v_fmac_f32_e32 v51, v37, v55
	v_lshlrev_b32_e32 v37, 16, v38
	v_mul_f32_e32 v37, v112, v37
	s_waitcnt lgkmcnt(0)
	v_fma_f32 v37, v37, v56, v44
	v_and_b32_e32 v38, 0xffff0000, v38
	v_lshlrev_b32_e32 v44, 16, v39
	v_and_b32_e32 v39, 0xffff0000, v39
	v_mul_f32_e32 v60, v112, v60
	v_mul_f32_e32 v49, v112, v49
	v_mul_f32_e32 v38, v112, v38
	v_mul_f32_e32 v44, v112, v44
	v_mul_f32_e32 v39, v112, v39
	v_fma_f32 v48, v60, v52, v48
	v_fma_f32 v49, v49, v54, v50
	v_fma_f32 v38, v38, v57, v45
	v_fma_f32 v44, v44, v58, v46
	v_fmac_f32_e32 v47, v39, v59
	s_and_saveexec_b64 s[0:1], s[42:43]
	v_mul_f32_e32 v39, 0x41800000, v48
	v_mul_f32_e32 v45, 0x41800000, v36
	v_med3_f32 v39, v39, s25, v218
	v_med3_f32 v45, v45, s25, v218
	v_cvt_pk_fp8_f32 v52, v39, v45
	v_mul_f32_e32 v46, 0x41800000, v49
	v_mul_f32_e32 v39, 0x41800000, v51
	v_med3_f32 v45, v46, s25, v218
	v_med3_f32 v39, v39, s25, v218
	v_cvt_pk_fp8_f32 v52, v45, v39 op_sel:[0,0,1]
	v_mul_f32_e32 v39, 0x41800000, v37
	v_mul_f32_e32 v45, 0x41800000, v38
	v_med3_f32 v39, v39, s25, v218
	v_med3_f32 v45, v45, s25, v218
	v_cvt_pk_fp8_f32 v53, v39, v45
	v_mul_f32_e32 v46, 0x41800000, v44
	v_mul_f32_e32 v39, 0x41800000, v47
	v_med3_f32 v45, v46, s25, v218
	v_med3_f32 v39, v39, s25, v218
	v_cvt_pk_fp8_f32 v53, v45, v39 op_sel:[0,0,1]
	global_store_dwordx2 v[144:145], v[52:53], off offset:704
.LBB0_1276:
	s_or_b64 exec, exec, s[0:1]
	v_cvt_pk_bf16_f32 v52, v48, v36
	v_cvt_pk_bf16_f32 v53, v49, v51
	v_cvt_pk_bf16_f32 v54, v37, v38
	v_cvt_pk_bf16_f32 v55, v44, v47
	v_lshlrev_b32_e32 v56, 16, v32
	v_and_b32_e32 v45, 0xffff0000, v52
	v_lshlrev_b32_e32 v39, 16, v52
	v_sub_f32_e32 v36, v36, v45
	v_sub_f32_e32 v39, v48, v39
	v_cvt_pk_bf16_f32 v48, v39, v36
	v_lshlrev_b32_e32 v36, 16, v53
	v_sub_f32_e32 v36, v49, v36
	v_and_b32_e32 v39, 0xffff0000, v53
	v_sub_f32_e32 v39, v51, v39
	v_cvt_pk_bf16_f32 v49, v36, v39
	v_lshlrev_b32_e32 v36, 16, v54
	v_sub_f32_e32 v36, v37, v36
	v_and_b32_e32 v37, 0xffff0000, v54
	v_sub_f32_e32 v37, v38, v37
	v_cvt_pk_bf16_f32 v50, v36, v37
	v_lshlrev_b32_e32 v36, 16, v55
	v_and_b32_e32 v37, 0xffff0000, v55
	v_sub_f32_e32 v36, v44, v36
	v_sub_f32_e32 v37, v47, v37
	v_cvt_pk_bf16_f32 v51, v36, v37
	ds_read_b128 v[36:39], v153 offset:2432
	v_and_b32_e32 v32, 0xffff0000, v32
	s_waitcnt lgkmcnt(0)
	v_mfma_f32_16x16x32_bf16 v[40:43], v[52:55], v[36:39], v[40:43]
	v_mul_f32_e32 v32, v112, v32
	v_mul_f32_e32 v56, v112, v56
	v_mfma_f32_16x16x32_bf16 v[36:39], v[48:51], v[36:39], v[40:43]
	s_nop 4
	ds_read_b128 v[40:43], v153 offset:35456
	s_waitcnt lgkmcnt(0)
	v_mfma_f32_16x16x32_bf16 v[36:39], v[52:55], v[40:43], v[36:39]
	ds_read_b128 v[44:47], v162 offset:7040
	ds_read_b128 v[48:51], v162 offset:2944
	ds_read_b128 v[40:43], v162 offset:7056
	ds_read_b128 v[52:55], v162 offset:2960
	s_waitcnt lgkmcnt(2)
	v_fma_f32 v32, v32, v49, v45
	v_lshlrev_b32_e32 v45, 16, v33
	v_and_b32_e32 v33, 0xffff0000, v33
	v_mul_f32_e32 v33, v112, v33
	v_fmac_f32_e32 v47, v33, v51
	v_lshlrev_b32_e32 v33, 16, v34
	v_mul_f32_e32 v33, v112, v33
	s_waitcnt lgkmcnt(0)
	v_fma_f32 v33, v33, v52, v40
	v_and_b32_e32 v34, 0xffff0000, v34
	v_lshlrev_b32_e32 v40, 16, v35
	v_and_b32_e32 v35, 0xffff0000, v35
	v_mul_f32_e32 v45, v112, v45
	v_mul_f32_e32 v34, v112, v34
	v_mul_f32_e32 v40, v112, v40
	v_mul_f32_e32 v35, v112, v35
	v_fma_f32 v44, v56, v48, v44
	v_fma_f32 v45, v45, v50, v46
	v_fma_f32 v34, v34, v53, v41
	v_fma_f32 v40, v40, v54, v42
	v_fmac_f32_e32 v43, v35, v55
	s_and_saveexec_b64 s[0:1], s[42:43]
	v_mul_f32_e32 v35, 0x41800000, v44
	v_mul_f32_e32 v41, 0x41800000, v32
	v_med3_f32 v35, v35, s25, v218
	v_med3_f32 v41, v41, s25, v218
	v_cvt_pk_fp8_f32 v48, v35, v41
	v_mul_f32_e32 v42, 0x41800000, v45
	v_mul_f32_e32 v35, 0x41800000, v47
	v_med3_f32 v41, v42, s25, v218
	v_med3_f32 v35, v35, s25, v218
	v_cvt_pk_fp8_f32 v48, v41, v35 op_sel:[0,0,1]
	v_mul_f32_e32 v35, 0x41800000, v33
	v_mul_f32_e32 v41, 0x41800000, v34
	v_med3_f32 v35, v35, s25, v218
	v_med3_f32 v41, v41, s25, v218
	v_cvt_pk_fp8_f32 v49, v35, v41
	v_mul_f32_e32 v42, 0x41800000, v40
	v_mul_f32_e32 v35, 0x41800000, v43
	v_med3_f32 v41, v42, s25, v218
	v_med3_f32 v35, v35, s25, v218
	v_cvt_pk_fp8_f32 v49, v41, v35 op_sel:[0,0,1]
	global_store_dwordx2 v[144:145], v[48:49], off offset:736
.LBB0_1278:
	s_or_b64 exec, exec, s[0:1]
	v_cvt_pk_bf16_f32 v48, v44, v32
	v_cvt_pk_bf16_f32 v49, v45, v47
	v_cvt_pk_bf16_f32 v50, v33, v34
	v_cvt_pk_bf16_f32 v51, v40, v43
	s_nop 0
	v_and_b32_e32 v41, 0xffff0000, v48
	v_lshlrev_b32_e32 v35, 16, v48
	v_sub_f32_e32 v32, v32, v41
	v_sub_f32_e32 v35, v44, v35
	v_cvt_pk_bf16_f32 v44, v35, v32
	v_lshlrev_b32_e32 v32, 16, v49
	v_sub_f32_e32 v32, v45, v32
	v_and_b32_e32 v35, 0xffff0000, v49
	v_sub_f32_e32 v35, v47, v35
	v_cvt_pk_bf16_f32 v45, v32, v35
	v_lshlrev_b32_e32 v32, 16, v50
	v_sub_f32_e32 v32, v33, v32
	v_and_b32_e32 v33, 0xffff0000, v50
	v_sub_f32_e32 v33, v34, v33
	v_cvt_pk_bf16_f32 v46, v32, v33
	v_lshlrev_b32_e32 v32, 16, v51
	v_and_b32_e32 v33, 0xffff0000, v51
	v_sub_f32_e32 v32, v40, v32
	v_sub_f32_e32 v33, v43, v33
	v_cvt_pk_bf16_f32 v47, v32, v33
	ds_read_b128 v[32:35], v153 offset:2496
	s_waitcnt lgkmcnt(0)
	v_mfma_f32_16x16x32_bf16 v[36:39], v[48:51], v[32:35], v[36:39]
	v_mfma_f32_16x16x32_bf16 v[32:35], v[44:47], v[32:35], v[36:39]
	s_nop 6
	ds_read_b128 v[36:39], v153 offset:35520
	s_waitcnt lgkmcnt(0)
	v_mfma_f32_16x16x32_bf16 v[32:35], v[48:51], v[36:39], v[32:35]
	ds_read_b128 v[40:43], v162 offset:7168
	ds_read_b128 v[44:47], v162 offset:3072
	ds_read_b128 v[48:51], v162 offset:3088
	ds_read_b128 v[36:39], v162 offset:7184
	v_lshlrev_b32_e32 v52, 16, v28
	v_and_b32_e32 v28, 0xffff0000, v28
	v_mul_f32_e32 v28, v112, v28
	s_waitcnt lgkmcnt(2)
	v_fma_f32 v28, v28, v45, v41
	v_lshlrev_b32_e32 v41, 16, v29
	v_and_b32_e32 v29, 0xffff0000, v29
	v_mul_f32_e32 v29, v112, v29
	v_fmac_f32_e32 v43, v29, v47
	v_lshlrev_b32_e32 v29, 16, v30
	v_mul_f32_e32 v29, v112, v29
	s_waitcnt lgkmcnt(0)
	v_fma_f32 v29, v29, v48, v36
	v_and_b32_e32 v30, 0xffff0000, v30
	v_lshlrev_b32_e32 v36, 16, v31
	v_and_b32_e32 v31, 0xffff0000, v31
	v_mul_f32_e32 v52, v112, v52
	v_mul_f32_e32 v41, v112, v41
	v_mul_f32_e32 v30, v112, v30
	v_mul_f32_e32 v36, v112, v36
	v_mul_f32_e32 v31, v112, v31
	v_fma_f32 v40, v52, v44, v40
	v_fma_f32 v41, v41, v46, v42
	v_fma_f32 v30, v30, v49, v37
	v_fma_f32 v36, v36, v50, v38
	v_fmac_f32_e32 v39, v31, v51
	s_and_saveexec_b64 s[0:1], s[42:43]
	v_mul_f32_e32 v31, 0x41800000, v40
	v_mul_f32_e32 v37, 0x41800000, v28
	v_med3_f32 v31, v31, s25, v218
	v_med3_f32 v37, v37, s25, v218
	v_cvt_pk_fp8_f32 v44, v31, v37
	v_mul_f32_e32 v38, 0x41800000, v41
	v_mul_f32_e32 v31, 0x41800000, v43
	v_med3_f32 v37, v38, s25, v218
	v_med3_f32 v31, v31, s25, v218
	v_cvt_pk_fp8_f32 v44, v37, v31 op_sel:[0,0,1]
	v_mul_f32_e32 v31, 0x41800000, v29
	v_mul_f32_e32 v37, 0x41800000, v30
	v_med3_f32 v31, v31, s25, v218
	v_med3_f32 v37, v37, s25, v218
	v_cvt_pk_fp8_f32 v45, v31, v37
	v_mul_f32_e32 v38, 0x41800000, v36
	v_mul_f32_e32 v31, 0x41800000, v39
	v_med3_f32 v37, v38, s25, v218
	v_med3_f32 v31, v31, s25, v218
	v_cvt_pk_fp8_f32 v45, v37, v31 op_sel:[0,0,1]
	global_store_dwordx2 v[144:145], v[44:45], off offset:768
.LBB0_1280:
	s_or_b64 exec, exec, s[0:1]
	v_cvt_pk_bf16_f32 v44, v40, v28
	v_cvt_pk_bf16_f32 v45, v41, v43
	v_cvt_pk_bf16_f32 v46, v29, v30
	v_cvt_pk_bf16_f32 v47, v36, v39
	v_lshlrev_b32_e32 v48, 16, v24
	v_and_b32_e32 v37, 0xffff0000, v44
	v_lshlrev_b32_e32 v31, 16, v44
	v_sub_f32_e32 v28, v28, v37
	v_sub_f32_e32 v31, v40, v31
	v_cvt_pk_bf16_f32 v40, v31, v28
	v_lshlrev_b32_e32 v28, 16, v45
	v_sub_f32_e32 v28, v41, v28
	v_and_b32_e32 v31, 0xffff0000, v45
	v_sub_f32_e32 v31, v43, v31
	v_cvt_pk_bf16_f32 v41, v28, v31
	v_lshlrev_b32_e32 v28, 16, v46
	v_sub_f32_e32 v28, v29, v28
	v_and_b32_e32 v29, 0xffff0000, v46
	v_sub_f32_e32 v29, v30, v29
	v_cvt_pk_bf16_f32 v42, v28, v29
	v_lshlrev_b32_e32 v28, 16, v47
	v_and_b32_e32 v29, 0xffff0000, v47
	v_sub_f32_e32 v28, v36, v28
	v_sub_f32_e32 v29, v39, v29
	v_cvt_pk_bf16_f32 v43, v28, v29
	ds_read_b128 v[28:31], v153 offset:2560
	v_and_b32_e32 v24, 0xffff0000, v24
	s_waitcnt lgkmcnt(0)
	v_mfma_f32_16x16x32_bf16 v[32:35], v[44:47], v[28:31], v[32:35]
	v_mul_f32_e32 v24, v112, v24
	v_mul_f32_e32 v48, v112, v48
	v_mfma_f32_16x16x32_bf16 v[28:31], v[40:43], v[28:31], v[32:35]
	s_nop 4
	ds_read_b128 v[32:35], v153 offset:35584
	s_waitcnt lgkmcnt(0)
	v_mfma_f32_16x16x32_bf16 v[28:31], v[44:47], v[32:35], v[28:31]
	ds_read_b128 v[36:39], v162 offset:7296
	ds_read_b128 v[40:43], v162 offset:3200
	ds_read_b128 v[32:35], v162 offset:7312
	ds_read_b128 v[44:47], v162 offset:3216
	s_waitcnt lgkmcnt(2)
	v_fma_f32 v24, v24, v41, v37
	v_lshlrev_b32_e32 v37, 16, v25
	v_and_b32_e32 v25, 0xffff0000, v25
	v_mul_f32_e32 v25, v112, v25
	v_fmac_f32_e32 v39, v25, v43
	v_lshlrev_b32_e32 v25, 16, v26
	v_mul_f32_e32 v25, v112, v25
	s_waitcnt lgkmcnt(0)
	v_fma_f32 v25, v25, v44, v32
	v_and_b32_e32 v26, 0xffff0000, v26
	v_lshlrev_b32_e32 v32, 16, v27
	v_and_b32_e32 v27, 0xffff0000, v27
	v_mul_f32_e32 v37, v112, v37
	v_mul_f32_e32 v26, v112, v26
	v_mul_f32_e32 v32, v112, v32
	v_mul_f32_e32 v27, v112, v27
	v_fma_f32 v36, v48, v40, v36
	v_fma_f32 v37, v37, v42, v38
	v_fma_f32 v26, v26, v45, v33
	v_fma_f32 v32, v32, v46, v34
	v_fmac_f32_e32 v35, v27, v47
	s_and_saveexec_b64 s[0:1], s[42:43]
	v_mul_f32_e32 v27, 0x41800000, v36
	v_mul_f32_e32 v33, 0x41800000, v24
	v_med3_f32 v27, v27, s25, v218
	v_med3_f32 v33, v33, s25, v218
	v_cvt_pk_fp8_f32 v40, v27, v33
	v_mul_f32_e32 v34, 0x41800000, v37
	v_mul_f32_e32 v27, 0x41800000, v39
	v_med3_f32 v33, v34, s25, v218
	v_med3_f32 v27, v27, s25, v218
	v_cvt_pk_fp8_f32 v40, v33, v27 op_sel:[0,0,1]
	v_mul_f32_e32 v27, 0x41800000, v25
	v_mul_f32_e32 v33, 0x41800000, v26
	v_med3_f32 v27, v27, s25, v218
	v_med3_f32 v33, v33, s25, v218
	v_cvt_pk_fp8_f32 v41, v27, v33
	v_mul_f32_e32 v34, 0x41800000, v32
	v_mul_f32_e32 v27, 0x41800000, v35
	v_med3_f32 v33, v34, s25, v218
	v_med3_f32 v27, v27, s25, v218
	v_cvt_pk_fp8_f32 v41, v33, v27 op_sel:[0,0,1]
	global_store_dwordx2 v[144:145], v[40:41], off offset:800
.LBB0_1282:
	s_or_b64 exec, exec, s[0:1]
	v_cvt_pk_bf16_f32 v40, v36, v24
	v_cvt_pk_bf16_f32 v41, v37, v39
	v_cvt_pk_bf16_f32 v42, v25, v26
	v_cvt_pk_bf16_f32 v43, v32, v35
	s_nop 0
	v_and_b32_e32 v33, 0xffff0000, v40
	v_lshlrev_b32_e32 v27, 16, v40
	v_sub_f32_e32 v24, v24, v33
	v_sub_f32_e32 v27, v36, v27
	v_cvt_pk_bf16_f32 v36, v27, v24
	v_lshlrev_b32_e32 v24, 16, v41
	v_sub_f32_e32 v24, v37, v24
	v_and_b32_e32 v27, 0xffff0000, v41
	v_sub_f32_e32 v27, v39, v27
	v_cvt_pk_bf16_f32 v37, v24, v27
	v_lshlrev_b32_e32 v24, 16, v42
	v_sub_f32_e32 v24, v25, v24
	v_and_b32_e32 v25, 0xffff0000, v42
	v_sub_f32_e32 v25, v26, v25
	v_cvt_pk_bf16_f32 v38, v24, v25
	v_lshlrev_b32_e32 v24, 16, v43
	v_and_b32_e32 v25, 0xffff0000, v43
	v_sub_f32_e32 v24, v32, v24
	v_sub_f32_e32 v25, v35, v25
	v_cvt_pk_bf16_f32 v39, v24, v25
	ds_read_b128 v[24:27], v153 offset:2624
	s_waitcnt lgkmcnt(0)
	v_mfma_f32_16x16x32_bf16 v[28:31], v[40:43], v[24:27], v[28:31]
	v_mfma_f32_16x16x32_bf16 v[24:27], v[36:39], v[24:27], v[28:31]
	s_nop 6
	ds_read_b128 v[28:31], v153 offset:35648
	s_waitcnt lgkmcnt(0)
	v_mfma_f32_16x16x32_bf16 v[24:27], v[40:43], v[28:31], v[24:27]
	ds_read_b128 v[32:35], v162 offset:7424
	ds_read_b128 v[36:39], v162 offset:3328
	ds_read_b128 v[40:43], v162 offset:3344
	ds_read_b128 v[28:31], v162 offset:7440
	v_lshlrev_b32_e32 v44, 16, v20
	v_and_b32_e32 v20, 0xffff0000, v20
	v_mul_f32_e32 v20, v112, v20
	s_waitcnt lgkmcnt(2)
	v_fma_f32 v20, v20, v37, v33
	v_lshlrev_b32_e32 v33, 16, v21
	v_and_b32_e32 v21, 0xffff0000, v21
	v_mul_f32_e32 v21, v112, v21
	v_fmac_f32_e32 v35, v21, v39
	v_lshlrev_b32_e32 v21, 16, v22
	v_mul_f32_e32 v21, v112, v21
	s_waitcnt lgkmcnt(0)
	v_fma_f32 v21, v21, v40, v28
	v_and_b32_e32 v22, 0xffff0000, v22
	v_lshlrev_b32_e32 v28, 16, v23
	v_and_b32_e32 v23, 0xffff0000, v23
	v_mul_f32_e32 v44, v112, v44
	v_mul_f32_e32 v33, v112, v33
	v_mul_f32_e32 v22, v112, v22
	v_mul_f32_e32 v28, v112, v28
	v_mul_f32_e32 v23, v112, v23
	v_fma_f32 v32, v44, v36, v32
	v_fma_f32 v33, v33, v38, v34
	v_fma_f32 v22, v22, v41, v29
	v_fma_f32 v28, v28, v42, v30
	v_fmac_f32_e32 v31, v23, v43
	s_and_saveexec_b64 s[0:1], s[42:43]
	v_mul_f32_e32 v23, 0x41800000, v32
	v_mul_f32_e32 v29, 0x41800000, v20
	v_med3_f32 v23, v23, s25, v218
	v_med3_f32 v29, v29, s25, v218
	v_cvt_pk_fp8_f32 v36, v23, v29
	v_mul_f32_e32 v30, 0x41800000, v33
	v_mul_f32_e32 v23, 0x41800000, v35
	v_med3_f32 v29, v30, s25, v218
	v_med3_f32 v23, v23, s25, v218
	v_cvt_pk_fp8_f32 v36, v29, v23 op_sel:[0,0,1]
	v_mul_f32_e32 v23, 0x41800000, v21
	v_mul_f32_e32 v29, 0x41800000, v22
	v_med3_f32 v23, v23, s25, v218
	v_med3_f32 v29, v29, s25, v218
	v_cvt_pk_fp8_f32 v37, v23, v29
	v_mul_f32_e32 v30, 0x41800000, v28
	v_mul_f32_e32 v23, 0x41800000, v31
	v_med3_f32 v29, v30, s25, v218
	v_med3_f32 v23, v23, s25, v218
	v_cvt_pk_fp8_f32 v37, v29, v23 op_sel:[0,0,1]
	global_store_dwordx2 v[144:145], v[36:37], off offset:832
.LBB0_1284:
	s_or_b64 exec, exec, s[0:1]
	v_cvt_pk_bf16_f32 v36, v32, v20
	v_cvt_pk_bf16_f32 v37, v33, v35
	v_cvt_pk_bf16_f32 v38, v21, v22
	v_cvt_pk_bf16_f32 v39, v28, v31
	v_lshlrev_b32_e32 v40, 16, v16
	v_and_b32_e32 v29, 0xffff0000, v36
	v_lshlrev_b32_e32 v23, 16, v36
	v_sub_f32_e32 v20, v20, v29
	v_sub_f32_e32 v23, v32, v23
	v_cvt_pk_bf16_f32 v32, v23, v20
	v_lshlrev_b32_e32 v20, 16, v37
	v_sub_f32_e32 v20, v33, v20
	v_and_b32_e32 v23, 0xffff0000, v37
	v_sub_f32_e32 v23, v35, v23
	v_cvt_pk_bf16_f32 v33, v20, v23
	v_lshlrev_b32_e32 v20, 16, v38
	v_sub_f32_e32 v20, v21, v20
	v_and_b32_e32 v21, 0xffff0000, v38
	v_sub_f32_e32 v21, v22, v21
	v_cvt_pk_bf16_f32 v34, v20, v21
	v_lshlrev_b32_e32 v20, 16, v39
	v_and_b32_e32 v21, 0xffff0000, v39
	v_sub_f32_e32 v20, v28, v20
	v_sub_f32_e32 v21, v31, v21
	v_cvt_pk_bf16_f32 v35, v20, v21
	ds_read_b128 v[20:23], v153 offset:2688
	v_and_b32_e32 v16, 0xffff0000, v16
	s_waitcnt lgkmcnt(0)
	v_mfma_f32_16x16x32_bf16 v[24:27], v[36:39], v[20:23], v[24:27]
	v_mul_f32_e32 v16, v112, v16
	v_mul_f32_e32 v40, v112, v40
	v_mfma_f32_16x16x32_bf16 v[20:23], v[32:35], v[20:23], v[24:27]
	s_nop 4
	ds_read_b128 v[24:27], v153 offset:35712
	s_waitcnt lgkmcnt(0)
	v_mfma_f32_16x16x32_bf16 v[20:23], v[36:39], v[24:27], v[20:23]
	ds_read_b128 v[28:31], v162 offset:7552
	ds_read_b128 v[32:35], v162 offset:3456
	ds_read_b128 v[24:27], v162 offset:7568
	ds_read_b128 v[36:39], v162 offset:3472
	s_waitcnt lgkmcnt(2)
	v_fma_f32 v16, v16, v33, v29
	v_lshlrev_b32_e32 v29, 16, v17
	v_and_b32_e32 v17, 0xffff0000, v17
	v_mul_f32_e32 v17, v112, v17
	v_fmac_f32_e32 v31, v17, v35
	v_lshlrev_b32_e32 v17, 16, v18
	v_mul_f32_e32 v17, v112, v17
	s_waitcnt lgkmcnt(0)
	v_fma_f32 v17, v17, v36, v24
	v_and_b32_e32 v18, 0xffff0000, v18
	v_lshlrev_b32_e32 v24, 16, v19
	v_and_b32_e32 v19, 0xffff0000, v19
	v_mul_f32_e32 v29, v112, v29
	v_mul_f32_e32 v18, v112, v18
	v_mul_f32_e32 v24, v112, v24
	v_mul_f32_e32 v19, v112, v19
	v_fma_f32 v28, v40, v32, v28
	v_fma_f32 v29, v29, v34, v30
	v_fma_f32 v18, v18, v37, v25
	v_fma_f32 v24, v24, v38, v26
	v_fmac_f32_e32 v27, v19, v39
	s_and_saveexec_b64 s[0:1], s[42:43]
	v_mul_f32_e32 v19, 0x41800000, v28
	v_mul_f32_e32 v25, 0x41800000, v16
	v_med3_f32 v19, v19, s25, v218
	v_med3_f32 v25, v25, s25, v218
	v_cvt_pk_fp8_f32 v32, v19, v25
	v_mul_f32_e32 v26, 0x41800000, v29
	v_mul_f32_e32 v19, 0x41800000, v31
	v_med3_f32 v25, v26, s25, v218
	v_med3_f32 v19, v19, s25, v218
	v_cvt_pk_fp8_f32 v32, v25, v19 op_sel:[0,0,1]
	v_mul_f32_e32 v19, 0x41800000, v17
	v_mul_f32_e32 v25, 0x41800000, v18
	v_med3_f32 v19, v19, s25, v218
	v_med3_f32 v25, v25, s25, v218
	v_cvt_pk_fp8_f32 v33, v19, v25
	v_mul_f32_e32 v26, 0x41800000, v24
	v_mul_f32_e32 v19, 0x41800000, v27
	v_med3_f32 v25, v26, s25, v218
	v_med3_f32 v19, v19, s25, v218
	v_cvt_pk_fp8_f32 v33, v25, v19 op_sel:[0,0,1]
	global_store_dwordx2 v[144:145], v[32:33], off offset:864
.LBB0_1286:
	s_or_b64 exec, exec, s[0:1]
	v_cvt_pk_bf16_f32 v32, v28, v16
	v_cvt_pk_bf16_f32 v33, v29, v31
	v_cvt_pk_bf16_f32 v34, v17, v18
	v_cvt_pk_bf16_f32 v35, v24, v27
	s_nop 0
	v_and_b32_e32 v25, 0xffff0000, v32
	v_lshlrev_b32_e32 v19, 16, v32
	v_sub_f32_e32 v16, v16, v25
	v_sub_f32_e32 v19, v28, v19
	v_cvt_pk_bf16_f32 v28, v19, v16
	v_lshlrev_b32_e32 v16, 16, v33
	v_sub_f32_e32 v16, v29, v16
	v_and_b32_e32 v19, 0xffff0000, v33
	v_sub_f32_e32 v19, v31, v19
	v_cvt_pk_bf16_f32 v29, v16, v19
	v_lshlrev_b32_e32 v16, 16, v34
	v_sub_f32_e32 v16, v17, v16
	v_and_b32_e32 v17, 0xffff0000, v34
	v_sub_f32_e32 v17, v18, v17
	v_cvt_pk_bf16_f32 v30, v16, v17
	v_lshlrev_b32_e32 v16, 16, v35
	v_and_b32_e32 v17, 0xffff0000, v35
	v_sub_f32_e32 v16, v24, v16
	v_sub_f32_e32 v17, v27, v17
	v_cvt_pk_bf16_f32 v31, v16, v17
	ds_read_b128 v[16:19], v153 offset:2752
	s_waitcnt lgkmcnt(0)
	v_mfma_f32_16x16x32_bf16 v[20:23], v[32:35], v[16:19], v[20:23]
	v_mfma_f32_16x16x32_bf16 v[16:19], v[28:31], v[16:19], v[20:23]
	s_nop 6
	ds_read_b128 v[20:23], v153 offset:35776
	s_waitcnt lgkmcnt(0)
	v_mfma_f32_16x16x32_bf16 v[16:19], v[32:35], v[20:23], v[16:19]
	ds_read_b128 v[24:27], v162 offset:7680
	ds_read_b128 v[28:31], v162 offset:3584
	ds_read_b128 v[32:35], v162 offset:3600
	ds_read_b128 v[20:23], v162 offset:7696
	v_lshlrev_b32_e32 v36, 16, v12
	v_and_b32_e32 v12, 0xffff0000, v12
	v_mul_f32_e32 v12, v112, v12
	s_waitcnt lgkmcnt(2)
	v_fma_f32 v12, v12, v29, v25
	v_lshlrev_b32_e32 v25, 16, v13
	v_and_b32_e32 v13, 0xffff0000, v13
	v_mul_f32_e32 v13, v112, v13
	v_fmac_f32_e32 v27, v13, v31
	v_lshlrev_b32_e32 v13, 16, v14
	v_mul_f32_e32 v13, v112, v13
	s_waitcnt lgkmcnt(0)
	v_fma_f32 v13, v13, v32, v20
	v_and_b32_e32 v14, 0xffff0000, v14
	v_lshlrev_b32_e32 v20, 16, v15
	v_and_b32_e32 v15, 0xffff0000, v15
	v_mul_f32_e32 v36, v112, v36
	v_mul_f32_e32 v25, v112, v25
	v_mul_f32_e32 v14, v112, v14
	v_mul_f32_e32 v20, v112, v20
	v_mul_f32_e32 v15, v112, v15
	v_fma_f32 v24, v36, v28, v24
	v_fma_f32 v25, v25, v30, v26
	v_fma_f32 v14, v14, v33, v21
	v_fma_f32 v20, v20, v34, v22
	v_fmac_f32_e32 v23, v15, v35
	s_and_saveexec_b64 s[0:1], s[42:43]
	v_mul_f32_e32 v15, 0x41800000, v24
	v_mul_f32_e32 v21, 0x41800000, v12
	v_med3_f32 v15, v15, s25, v218
	v_med3_f32 v21, v21, s25, v218
	v_cvt_pk_fp8_f32 v28, v15, v21
	v_mul_f32_e32 v22, 0x41800000, v25
	v_mul_f32_e32 v15, 0x41800000, v27
	v_med3_f32 v21, v22, s25, v218
	v_med3_f32 v15, v15, s25, v218
	v_cvt_pk_fp8_f32 v28, v21, v15 op_sel:[0,0,1]
	v_mul_f32_e32 v15, 0x41800000, v13
	v_mul_f32_e32 v21, 0x41800000, v14
	v_med3_f32 v15, v15, s25, v218
	v_med3_f32 v21, v21, s25, v218
	v_cvt_pk_fp8_f32 v29, v15, v21
	v_mul_f32_e32 v22, 0x41800000, v20
	v_mul_f32_e32 v15, 0x41800000, v23
	v_med3_f32 v21, v22, s25, v218
	v_med3_f32 v15, v15, s25, v218
	v_cvt_pk_fp8_f32 v29, v21, v15 op_sel:[0,0,1]
	global_store_dwordx2 v[144:145], v[28:29], off offset:896
.LBB0_1288:
	s_or_b64 exec, exec, s[0:1]
	v_cvt_pk_bf16_f32 v28, v24, v12
	v_cvt_pk_bf16_f32 v29, v25, v27
	v_cvt_pk_bf16_f32 v30, v13, v14
	v_cvt_pk_bf16_f32 v31, v20, v23
	v_lshlrev_b32_e32 v32, 16, v8
	v_and_b32_e32 v21, 0xffff0000, v28
	v_lshlrev_b32_e32 v15, 16, v28
	v_sub_f32_e32 v12, v12, v21
	v_sub_f32_e32 v15, v24, v15
	v_cvt_pk_bf16_f32 v24, v15, v12
	v_lshlrev_b32_e32 v12, 16, v29
	v_sub_f32_e32 v12, v25, v12
	v_and_b32_e32 v15, 0xffff0000, v29
	v_sub_f32_e32 v15, v27, v15
	v_cvt_pk_bf16_f32 v25, v12, v15
	v_lshlrev_b32_e32 v12, 16, v30
	v_sub_f32_e32 v12, v13, v12
	v_and_b32_e32 v13, 0xffff0000, v30
	v_sub_f32_e32 v13, v14, v13
	v_cvt_pk_bf16_f32 v26, v12, v13
	v_lshlrev_b32_e32 v12, 16, v31
	v_and_b32_e32 v13, 0xffff0000, v31
	v_sub_f32_e32 v12, v20, v12
	v_sub_f32_e32 v13, v23, v13
	v_cvt_pk_bf16_f32 v27, v12, v13
	ds_read_b128 v[12:15], v153 offset:2816
	v_and_b32_e32 v8, 0xffff0000, v8
	s_waitcnt lgkmcnt(0)
	v_mfma_f32_16x16x32_bf16 v[16:19], v[28:31], v[12:15], v[16:19]
	v_mul_f32_e32 v8, v112, v8
	v_mul_f32_e32 v32, v112, v32
	v_mfma_f32_16x16x32_bf16 v[12:15], v[24:27], v[12:15], v[16:19]
	s_nop 4
	ds_read_b128 v[16:19], v153 offset:35840
	s_waitcnt lgkmcnt(0)
	v_mfma_f32_16x16x32_bf16 v[12:15], v[28:31], v[16:19], v[12:15]
	ds_read_b128 v[20:23], v162 offset:7808
	ds_read_b128 v[24:27], v162 offset:3712
	ds_read_b128 v[16:19], v162 offset:7824
	ds_read_b128 v[28:31], v162 offset:3728
	s_waitcnt lgkmcnt(2)
	v_fma_f32 v8, v8, v25, v21
	v_lshlrev_b32_e32 v21, 16, v9
	v_and_b32_e32 v9, 0xffff0000, v9
	v_mul_f32_e32 v9, v112, v9
	v_fmac_f32_e32 v23, v9, v27
	v_lshlrev_b32_e32 v9, 16, v10
	v_mul_f32_e32 v9, v112, v9
	s_waitcnt lgkmcnt(0)
	v_fma_f32 v9, v9, v28, v16
	v_and_b32_e32 v10, 0xffff0000, v10
	v_lshlrev_b32_e32 v16, 16, v11
	v_and_b32_e32 v11, 0xffff0000, v11
	v_mul_f32_e32 v21, v112, v21
	v_mul_f32_e32 v10, v112, v10
	v_mul_f32_e32 v16, v112, v16
	v_mul_f32_e32 v11, v112, v11
	v_fma_f32 v20, v32, v24, v20
	v_fma_f32 v21, v21, v26, v22
	v_fma_f32 v10, v10, v29, v17
	v_fma_f32 v16, v16, v30, v18
	v_fmac_f32_e32 v19, v11, v31
	s_and_saveexec_b64 s[0:1], s[42:43]
	v_mul_f32_e32 v11, 0x41800000, v20
	v_mul_f32_e32 v17, 0x41800000, v8
	v_med3_f32 v11, v11, s25, v218
	v_med3_f32 v17, v17, s25, v218
	v_cvt_pk_fp8_f32 v24, v11, v17
	v_mul_f32_e32 v18, 0x41800000, v21
	v_mul_f32_e32 v11, 0x41800000, v23
	v_med3_f32 v17, v18, s25, v218
	v_med3_f32 v11, v11, s25, v218
	v_cvt_pk_fp8_f32 v24, v17, v11 op_sel:[0,0,1]
	v_mul_f32_e32 v11, 0x41800000, v9
	v_mul_f32_e32 v17, 0x41800000, v10
	v_med3_f32 v11, v11, s25, v218
	v_med3_f32 v17, v17, s25, v218
	v_cvt_pk_fp8_f32 v25, v11, v17
	v_mul_f32_e32 v18, 0x41800000, v16
	v_mul_f32_e32 v11, 0x41800000, v19
	v_med3_f32 v17, v18, s25, v218
	v_med3_f32 v11, v11, s25, v218
	v_cvt_pk_fp8_f32 v25, v17, v11 op_sel:[0,0,1]
	global_store_dwordx2 v[144:145], v[24:25], off offset:928
.LBB0_1290:
	s_or_b64 exec, exec, s[0:1]
	v_cvt_pk_bf16_f32 v24, v20, v8
	v_cvt_pk_bf16_f32 v25, v21, v23
	v_cvt_pk_bf16_f32 v26, v9, v10
	v_cvt_pk_bf16_f32 v27, v16, v19
	s_nop 0
	v_and_b32_e32 v17, 0xffff0000, v24
	v_lshlrev_b32_e32 v11, 16, v24
	v_sub_f32_e32 v8, v8, v17
	v_sub_f32_e32 v11, v20, v11
	v_cvt_pk_bf16_f32 v20, v11, v8
	v_lshlrev_b32_e32 v8, 16, v25
	v_sub_f32_e32 v8, v21, v8
	v_and_b32_e32 v11, 0xffff0000, v25
	v_sub_f32_e32 v11, v23, v11
	v_cvt_pk_bf16_f32 v21, v8, v11
	v_lshlrev_b32_e32 v8, 16, v26
	v_sub_f32_e32 v8, v9, v8
	v_and_b32_e32 v9, 0xffff0000, v26
	v_sub_f32_e32 v9, v10, v9
	v_cvt_pk_bf16_f32 v22, v8, v9
	v_lshlrev_b32_e32 v8, 16, v27
	v_and_b32_e32 v9, 0xffff0000, v27
	v_sub_f32_e32 v8, v16, v8
	v_sub_f32_e32 v9, v19, v9
	v_cvt_pk_bf16_f32 v23, v8, v9
	ds_read_b128 v[8:11], v153 offset:2880
	s_waitcnt lgkmcnt(0)
	v_mfma_f32_16x16x32_bf16 v[12:15], v[24:27], v[8:11], v[12:15]
	v_mfma_f32_16x16x32_bf16 v[8:11], v[20:23], v[8:11], v[12:15]
	s_nop 6
	ds_read_b128 v[12:15], v153 offset:35904
	s_waitcnt lgkmcnt(0)
	v_mfma_f32_16x16x32_bf16 v[8:11], v[24:27], v[12:15], v[8:11]
	ds_read_b128 v[16:19], v162 offset:7936
	ds_read_b128 v[20:23], v162 offset:3840
	ds_read_b128 v[24:27], v162 offset:3856
	ds_read_b128 v[12:15], v162 offset:7952
	v_lshlrev_b32_e32 v28, 16, v4
	v_and_b32_e32 v4, 0xffff0000, v4
	v_mul_f32_e32 v4, v112, v4
	s_waitcnt lgkmcnt(2)
	v_fma_f32 v4, v4, v21, v17
	v_lshlrev_b32_e32 v17, 16, v5
	v_and_b32_e32 v5, 0xffff0000, v5
	v_mul_f32_e32 v5, v112, v5
	v_fmac_f32_e32 v19, v5, v23
	v_lshlrev_b32_e32 v5, 16, v6
	v_mul_f32_e32 v5, v112, v5
	s_waitcnt lgkmcnt(0)
	v_fma_f32 v5, v5, v24, v12
	v_and_b32_e32 v6, 0xffff0000, v6
	v_lshlrev_b32_e32 v12, 16, v7
	v_and_b32_e32 v7, 0xffff0000, v7
	v_mul_f32_e32 v28, v112, v28
	v_mul_f32_e32 v17, v112, v17
	v_mul_f32_e32 v6, v112, v6
	v_mul_f32_e32 v12, v112, v12
	v_mul_f32_e32 v7, v112, v7
	v_fma_f32 v16, v28, v20, v16
	v_fma_f32 v17, v17, v22, v18
	v_fma_f32 v6, v6, v25, v13
	v_fma_f32 v12, v12, v26, v14
	v_fmac_f32_e32 v15, v7, v27
	s_and_saveexec_b64 s[0:1], s[42:43]
	v_mul_f32_e32 v7, 0x41800000, v16
	v_mul_f32_e32 v13, 0x41800000, v4
	v_med3_f32 v7, v7, s25, v218
	v_med3_f32 v13, v13, s25, v218
	v_cvt_pk_fp8_f32 v20, v7, v13
	v_mul_f32_e32 v14, 0x41800000, v17
	v_mul_f32_e32 v7, 0x41800000, v19
	v_med3_f32 v13, v14, s25, v218
	v_med3_f32 v7, v7, s25, v218
	v_cvt_pk_fp8_f32 v20, v13, v7 op_sel:[0,0,1]
	v_mul_f32_e32 v7, 0x41800000, v5
	v_mul_f32_e32 v13, 0x41800000, v6
	v_med3_f32 v7, v7, s25, v218
	v_med3_f32 v13, v13, s25, v218
	v_cvt_pk_fp8_f32 v21, v7, v13
	v_mul_f32_e32 v14, 0x41800000, v12
	v_mul_f32_e32 v7, 0x41800000, v15
	v_med3_f32 v13, v14, s25, v218
	v_med3_f32 v7, v7, s25, v218
	v_cvt_pk_fp8_f32 v21, v13, v7 op_sel:[0,0,1]
	global_store_dwordx2 v[144:145], v[20:21], off offset:960
.LBB0_1292:
	s_or_b64 exec, exec, s[0:1]
	v_cvt_pk_bf16_f32 v20, v16, v4
	v_cvt_pk_bf16_f32 v21, v17, v19
	v_cvt_pk_bf16_f32 v22, v5, v6
	v_cvt_pk_bf16_f32 v23, v12, v15
	v_lshlrev_b32_e32 v24, 16, v0
	v_and_b32_e32 v13, 0xffff0000, v20
	v_lshlrev_b32_e32 v7, 16, v20
	v_sub_f32_e32 v4, v4, v13
	v_sub_f32_e32 v7, v16, v7
	v_cvt_pk_bf16_f32 v16, v7, v4
	v_lshlrev_b32_e32 v4, 16, v21
	v_sub_f32_e32 v4, v17, v4
	v_and_b32_e32 v7, 0xffff0000, v21
	v_sub_f32_e32 v7, v19, v7
	v_cvt_pk_bf16_f32 v17, v4, v7
	v_lshlrev_b32_e32 v4, 16, v22
	v_sub_f32_e32 v4, v5, v4
	v_and_b32_e32 v5, 0xffff0000, v22
	v_sub_f32_e32 v5, v6, v5
	v_cvt_pk_bf16_f32 v18, v4, v5
	v_lshlrev_b32_e32 v4, 16, v23
	v_and_b32_e32 v5, 0xffff0000, v23
	v_sub_f32_e32 v4, v12, v4
	v_sub_f32_e32 v5, v15, v5
	v_cvt_pk_bf16_f32 v19, v4, v5
	ds_read_b128 v[4:7], v153 offset:2944
	v_and_b32_e32 v0, 0xffff0000, v0
	s_waitcnt lgkmcnt(0)
	v_mfma_f32_16x16x32_bf16 v[8:11], v[20:23], v[4:7], v[8:11]
	v_mul_f32_e32 v0, v112, v0
	v_mul_f32_e32 v24, v112, v24
	v_mfma_f32_16x16x32_bf16 v[4:7], v[16:19], v[4:7], v[8:11]
	s_nop 4
	ds_read_b128 v[8:11], v153 offset:35968
	s_waitcnt lgkmcnt(0)
	v_mfma_f32_16x16x32_bf16 v[4:7], v[20:23], v[8:11], v[4:7]
	ds_read_b128 v[12:15], v162 offset:8064
	ds_read_b128 v[16:19], v162 offset:3968
	ds_read_b128 v[8:11], v162 offset:8080
	ds_read_b128 v[20:23], v162 offset:3984
	s_waitcnt lgkmcnt(2)
	v_fma_f32 v0, v0, v17, v13
	v_lshlrev_b32_e32 v13, 16, v1
	v_and_b32_e32 v1, 0xffff0000, v1
	v_mul_f32_e32 v1, v112, v1
	v_fmac_f32_e32 v15, v1, v19
	v_lshlrev_b32_e32 v1, 16, v2
	v_mul_f32_e32 v1, v112, v1
	s_waitcnt lgkmcnt(0)
	v_fma_f32 v1, v1, v20, v8
	v_and_b32_e32 v2, 0xffff0000, v2
	v_lshlrev_b32_e32 v8, 16, v3
	v_and_b32_e32 v3, 0xffff0000, v3
	v_mul_f32_e32 v13, v112, v13
	v_mul_f32_e32 v2, v112, v2
	v_mul_f32_e32 v8, v112, v8
	v_mul_f32_e32 v3, v112, v3
	v_fma_f32 v12, v24, v16, v12
	v_fma_f32 v13, v13, v18, v14
	v_fma_f32 v2, v2, v21, v9
	v_fma_f32 v8, v8, v22, v10
	v_fmac_f32_e32 v11, v3, v23
	s_and_saveexec_b64 s[0:1], s[42:43]
	v_mul_f32_e32 v3, 0x41800000, v12
	v_mul_f32_e32 v9, 0x41800000, v0
	v_med3_f32 v3, v3, s25, v218
	v_med3_f32 v9, v9, s25, v218
	v_cvt_pk_fp8_f32 v16, v3, v9
	v_mul_f32_e32 v10, 0x41800000, v13
	v_mul_f32_e32 v14, 0x41800000, v15
	v_med3_f32 v3, v10, s25, v218
	v_med3_f32 v9, v14, s25, v218
	v_cvt_pk_fp8_f32 v16, v3, v9 op_sel:[0,0,1]
	v_mul_f32_e32 v3, 0x41800000, v1
	v_mul_f32_e32 v9, 0x41800000, v2
	v_med3_f32 v3, v3, s25, v218
	v_med3_f32 v9, v9, s25, v218
	v_cvt_pk_fp8_f32 v17, v3, v9
	v_mul_f32_e32 v10, 0x41800000, v8
	v_mul_f32_e32 v14, 0x41800000, v11
	v_med3_f32 v3, v10, s25, v218
	v_med3_f32 v9, v14, s25, v218
	v_cvt_pk_fp8_f32 v17, v3, v9 op_sel:[0,0,1]
	global_store_dwordx2 v[144:145], v[16:17], off offset:992

.LBB0_1505:
	v_sub_u32_e32 v5, v11, v5
	s_waitcnt lgkmcnt(0)
	v_add_u32_e32 v11, v53, v52
	v_add_u32_e32 v11, v11, v51
	v_add_u32_e32 v11, v11, v50
	v_add_u32_e32 v11, v11, v33
	v_add_u32_e32 v11, v11, v29
	v_add_u32_e32 v11, v11, v21
	v_add_u32_e32 v11, v11, v15
	s_mulk_i32 s30, 0x1200
	v_add_u32_e32 v5, v11, v5
	s_add_i32 s35, s30, s35
	v_mov_b32_e32 v11, -1
	v_mov_b32_e32 v15, -1
	s_and_saveexec_b64 s[64:65], s[92:93]
	v_add_u32_e32 v50, s35, v5
	v_ashrrev_i32_e32 v51, 31, v50
	v_add_u32_e32 v21, 1, v5
	v_lshl_add_u64 v[50:51], v[50:51], 2, s[16:17]
	v_mov_b32_e32 v15, v5
	v_mov_b32_e32 v5, v21
	global_store_dword v[50:51], v32, off
.LBB0_1507:
	s_or_b64 exec, exec, s[64:65]
	s_add_u32 s64, s14, s96
	s_addc_u32 s65, s15, 0
	v_lshl_add_u64 v[30:31], s[64:65], 0, v[30:31]
	global_store_dword v[30:31], v15, off
	s_and_saveexec_b64 s[66:67], s[88:89]
	v_add_u32_e32 v30, s35, v5
	v_ashrrev_i32_e32 v31, 31, v30
	v_add_u32_e32 v15, 1, v5
	v_lshl_add_u64 v[30:31], v[30:31], 2, s[16:17]
	v_mov_b32_e32 v11, v5
	v_mov_b32_e32 v5, v15
	global_store_dword v[30:31], v28, off
.LBB0_1509:
	s_or_b64 exec, exec, s[66:67]
	v_lshl_add_u64 v[26:27], s[64:65], 0, v[26:27]
	global_store_dword v[26:27], v11, off
	v_mov_b32_e32 v11, -1
	v_mov_b32_e32 v15, -1
	s_and_saveexec_b64 s[66:67], s[86:87]
	v_add_u32_e32 v26, s35, v5
	v_ashrrev_i32_e32 v27, 31, v26
	v_add_u32_e32 v21, 1, v5
	v_lshl_add_u64 v[26:27], v[26:27], 2, s[16:17]
	v_mov_b32_e32 v15, v5
	v_mov_b32_e32 v5, v21
	global_store_dword v[26:27], v24, off
.LBB0_1511:
	s_or_b64 exec, exec, s[66:67]
	v_lshl_add_u64 v[22:23], s[64:65], 0, v[22:23]
	global_store_dword v[22:23], v15, off
	s_and_saveexec_b64 s[66:67], s[84:85]
	v_add_u32_e32 v22, s35, v5
	v_ashrrev_i32_e32 v23, 31, v22
	v_lshl_add_u64 v[22:23], v[22:23], 2, s[16:17]
	v_mov_b32_e32 v11, v5
	global_store_dword v[22:23], v20, off
